# speedup vs baseline: 1.0432x; 1.0288x over previous
_Z10qkv_kernelPKfPK15HIP_vector_typeIjLj4EEPDv8_DF16_S6_S6_:
	s_load_dwordx8 s[4:11], s[0:1], 0x0
	s_ashr_i32 s3, s2, 2
	s_and_b32 s3, s3, -8
	s_and_b32 s12, s2, 7
	s_bfe_u32 s2, s2, 0x20003
	s_or_b32 s12, s3, s12
	s_mul_i32 s3, s2, 0x36000
	s_waitcnt lgkmcnt(0)
	s_add_u32 s6, s6, s3
	s_addc_u32 s7, s7, 0
	s_mov_b64 s[22:23], s[6:7]
	s_cmp_eq_u32 s2, 3
	s_cbranch_scc1 .Lqkv_p1N
	v_mov_b32_e32 v211, 0
	v_lshlrev_b32_e32 v208, 4, v0
	v_mov_b32_e32 v209, v211
	v_lshl_add_u64 v[2:3], s[6:7], 0, v[208:209]
	s_movk_i32 s3, 0x2000
	v_add_co_u32_e32 v4, vcc, s3, v2
	v_lshrrev_b32_e32 v214, 6, v0
	s_nop 0
	v_addc_co_u32_e32 v5, vcc, 0, v3, vcc
	s_movk_i32 s3, 0x4000
	v_add_co_u32_e32 v6, vcc, s3, v2
	v_lshlrev_b32_e32 v1, 5, v214
	v_addc_co_u32_e32 v7, vcc, 0, v3, vcc
	v_lshl_or_b32 v1, s12, 8, v1
	s_movk_i32 s6, 0x600
	v_mov_b64_e32 v[4:5], s[4:5]
	v_mad_i64_i32 v[72:73], s[4:5], v1, s6, v[4:5]
	v_bfe_u32 v1, v0, 4, 2
	v_and_b32_e32 v80, 15, v0
	v_lshlrev_b32_e32 v210, 4, v80
	v_mul_u32_u24_e32 v4, 0x180, v1
	v_lshl_add_u64 v[40:41], v[72:73], 0, v[210:211]
	v_lshlrev_b32_e32 v48, 2, v4
	v_mov_b32_e32 v49, v211
	v_lshl_add_u64 v[12:13], v[40:41], 0, v[48:49]
	s_movk_i32 s4, 0x1000
	v_add_co_u32_e32 v14, vcc, s4, v12
	s_movk_i32 s4, 0x3000
	s_nop 0
	v_addc_co_u32_e32 v15, vcc, 0, v13, vcc
	v_add_co_u32_e32 v32, vcc, s4, v12
	global_load_dwordx4 v[4:7], v[12:13], off nt
	global_load_dwordx4 v[8:11], v[14:15], off offset:2048 nt
	v_addc_co_u32_e32 v33, vcc, 0, v13, vcc
	v_add_co_u32_e32 v34, vcc, s3, v12
	v_or_b32_e32 v64, 0x6000, v48
	v_mov_b32_e32 v65, v211
	v_addc_co_u32_e32 v35, vcc, 0, v13, vcc
	global_load_dwordx4 v[12:15], v[32:33], off nt
	global_load_dwordx4 v[28:31], v[34:35], off offset:2048 nt
	v_lshl_add_u64 v[42:43], v[40:41], 0, v[64:65]
	v_add_u32_e32 v66, 0x7800, v48
	v_mov_b32_e32 v67, v211
	v_add_u32_e32 v74, 0x9000, v48
	v_mov_b32_e32 v75, v211
	v_lshl_add_u64 v[44:45], v[40:41], 0, v[66:67]
	global_load_dwordx4 v[32:35], v[42:43], off nt
	global_load_dwordx4 v[36:39], v[44:45], off nt
	v_lshl_add_u64 v[50:51], v[40:41], 0, v[74:75]
	v_add_u32_e32 v76, 0xa800, v48
	v_mov_b32_e32 v77, v211
	v_lshl_add_u64 v[52:53], v[40:41], 0, v[76:77]
	global_load_dwordx4 v[40:43], v[50:51], off nt
	global_load_dwordx4 v[44:47], v[52:53], off nt
	v_lshl_add_u64 v[48:49], v[72:73], 0, v[48:49]
	v_lshl_add_u64 v[140:141], v[48:49], 0, v[210:211]
	s_mov_b64 s[4:5], 0x1800
	v_lshl_add_u64 v[142:143], v[140:141], 0, s[4:5]
	s_mov_b64 s[4:5], 0x3000
	v_lshl_add_u64 v[64:65], v[72:73], 0, v[64:65]
	v_lshl_add_u64 v[74:75], v[72:73], 0, v[74:75]
	v_lshl_add_u64 v[144:145], v[140:141], 0, s[4:5]
	s_mov_b64 s[4:5], 0x4800
	v_lshl_add_u64 v[148:149], v[64:65], 0, v[210:211]
	v_lshl_add_u64 v[64:65], v[72:73], 0, v[66:67]
	v_lshl_add_u64 v[152:153], v[74:75], 0, v[210:211]
	v_lshl_add_u64 v[72:73], v[72:73], 0, v[76:77]
	global_load_dwordx4 v[48:51], v[140:141], off offset:256 nt
	global_load_dwordx4 v[52:55], v[142:143], off offset:256 nt
	v_lshl_add_u64 v[146:147], v[140:141], 0, s[4:5]
	global_load_dwordx4 v[56:59], v[144:145], off offset:256 nt
	global_load_dwordx4 v[60:63], v[146:147], off offset:256 nt
	v_lshl_add_u64 v[150:151], v[64:65], 0, v[210:211]
	global_load_dwordx4 v[64:67], v[148:149], off offset:256 nt
	global_load_dwordx4 v[68:71], v[150:151], off offset:256 nt
	v_lshl_add_u64 v[154:155], v[72:73], 0, v[210:211]
	global_load_dwordx4 v[72:75], v[152:153], off offset:256 nt
	global_load_dwordx4 v[76:79], v[154:155], off offset:256 nt
	v_mov_b32_e32 v236, v208
	v_add_u32_e32 v237, 0x2000, v208
	v_add_u32_e32 v238, 0x4000, v208
	global_load_dwordx4 v[160:163], v236, s[22:23]
	global_load_dwordx4 v[164:167], v237, s[22:23]
	global_load_dwordx4 v[168:171], v238, s[22:23]
	s_add_u32 s20, s22, 24576
	s_addc_u32 s21, s23, 0
	global_load_dwordx4 v[172:175], v236, s[20:21]
	global_load_dwordx4 v[176:179], v237, s[20:21]
	global_load_dwordx4 v[180:183], v238, s[20:21]
	s_add_u32 s20, s22, 49152
	s_addc_u32 s21, s23, 0
	global_load_dwordx4 v[184:187], v236, s[20:21]
	global_load_dwordx4 v[188:191], v237, s[20:21]
	global_load_dwordx4 v[192:195], v238, s[20:21]
	s_add_u32 s20, s22, 73728
	s_addc_u32 s21, s23, 0
	global_load_dwordx4 v[196:199], v236, s[20:21]
	global_load_dwordx4 v[200:203], v237, s[20:21]
	global_load_dwordx4 v[204:207], v238, s[20:21]
	s_add_u32 s20, s22, 98304
	s_addc_u32 s21, s23, 0
	global_load_dwordx4 v[216:219], v236, s[20:21]
	global_load_dwordx4 v[220:223], v237, s[20:21]
	global_load_dwordx4 v[224:227], v238, s[20:21]
	v_mul_u32_u24_e32 v82, 0x1200, v214
	v_lshl_or_b32 v80, v80, 3, v82
	s_movk_i32 s3, 0x90
	v_mad_u32_u24 v1, v1, s3, v80
	v_add_u32_e32 v157, 0x1e000, v1
	v_and_b32_e32 v81, 31, v0
	v_lshrrev_b32_e32 v83, 1, v0
	v_add_u32_e32 v1, 0x1e800, v1
	v_mul_u32_u24_e32 v81, 0x90, v81
	v_and_b32_e32 v83, 16, v83
	v_add3_u32 v156, v82, v81, v83
	v_add_u32_e32 v156, 0x12000, v156
	s_load_dwordx2 s[0:1], s[0:1], 0x20
	s_mov_b32 s3, 0
	v_and_b32_e32 v0, 63, v0
	s_waitcnt vmcnt(30)
	v_cvt_pk_f16_f32 v7, v6, v7
	v_cvt_pk_f16_f32 v6, v4, v5
	s_waitcnt vmcnt(29)
	v_cvt_pk_f16_f32 v5, v10, v11
	v_cvt_pk_f16_f32 v4, v8, v9
	ds_write2_b64 v157, v[6:7], v[4:5] offset1:72
	s_waitcnt vmcnt(28)
	v_cvt_pk_f16_f32 v5, v14, v15
	v_cvt_pk_f16_f32 v4, v12, v13
	s_waitcnt vmcnt(27)
	v_cvt_pk_f16_f32 v7, v30, v31
	v_cvt_pk_f16_f32 v6, v28, v29
	ds_write2_b64 v157, v[4:5], v[6:7] offset0:144 offset1:216
	s_waitcnt vmcnt(26)
	v_cvt_pk_f16_f32 v5, v34, v35
	v_cvt_pk_f16_f32 v4, v32, v33
	s_waitcnt vmcnt(25)
	v_cvt_pk_f16_f32 v7, v38, v39
	v_cvt_pk_f16_f32 v6, v36, v37
	ds_write2_b64 v1, v[4:5], v[6:7] offset0:32 offset1:104
	s_waitcnt vmcnt(24)
	v_cvt_pk_f16_f32 v5, v42, v43
	v_cvt_pk_f16_f32 v4, v40, v41
	s_waitcnt vmcnt(23)
	v_cvt_pk_f16_f32 v7, v46, v47
	v_cvt_pk_f16_f32 v6, v44, v45
	ds_write2_b64 v1, v[4:5], v[6:7] offset0:176 offset1:248
	ds_read_b128 v[28:31], v156 offset:49152
	ds_read_b128 v[32:35], v156 offset:49184
	ds_read_b128 v[36:39], v156 offset:49216
	ds_read_b128 v[40:43], v156 offset:49248
	global_load_dwordx4 v[4:7], v[140:141], off offset:512 nt
	global_load_dwordx4 v[8:11], v[142:143], off offset:512 nt
	global_load_dwordx4 v[12:15], v[144:145], off offset:512 nt
	global_load_dwordx4 v[80:83], v[146:147], off offset:512 nt
	global_load_dwordx4 v[84:87], v[148:149], off offset:512 nt
	global_load_dwordx4 v[88:91], v[150:151], off offset:512 nt
	global_load_dwordx4 v[92:95], v[152:153], off offset:512 nt
	global_load_dwordx4 v[96:99], v[154:155], off offset:512 nt
	s_waitcnt vmcnt(15)
	v_cvt_pk_f16_f32 v45, v50, v51
	v_cvt_pk_f16_f32 v44, v48, v49
	s_waitcnt vmcnt(14)
	v_cvt_pk_f16_f32 v47, v54, v55
	v_cvt_pk_f16_f32 v46, v52, v53
	ds_write2_b64 v157, v[44:45], v[46:47] offset1:72
	s_waitcnt vmcnt(13)
	v_cvt_pk_f16_f32 v45, v58, v59
	v_cvt_pk_f16_f32 v44, v56, v57
	s_waitcnt vmcnt(12)
	v_cvt_pk_f16_f32 v47, v62, v63
	v_cvt_pk_f16_f32 v46, v60, v61
	ds_write2_b64 v157, v[44:45], v[46:47] offset0:144 offset1:216
	s_waitcnt vmcnt(11)
	v_cvt_pk_f16_f32 v45, v66, v67
	v_cvt_pk_f16_f32 v44, v64, v65
	s_waitcnt vmcnt(10)
	v_cvt_pk_f16_f32 v47, v70, v71
	v_cvt_pk_f16_f32 v46, v68, v69
	ds_write2_b64 v1, v[44:45], v[46:47] offset0:32 offset1:104
	s_waitcnt vmcnt(9)
	v_cvt_pk_f16_f32 v45, v74, v75
	v_cvt_pk_f16_f32 v44, v72, v73
	s_waitcnt vmcnt(8)
	v_cvt_pk_f16_f32 v47, v78, v79
	v_cvt_pk_f16_f32 v46, v76, v77
	ds_write2_b64 v1, v[44:45], v[46:47] offset0:176 offset1:248
	ds_read_b128 v[44:47], v156 offset:49152
	ds_read_b128 v[48:51], v156 offset:49184
	ds_read_b128 v[52:55], v156 offset:49216
	ds_read_b128 v[56:59], v156 offset:49248
	global_load_dwordx4 v[76:79], v[140:141], off offset:768 nt
	global_load_dwordx4 v[100:103], v[142:143], off offset:768 nt
	global_load_dwordx4 v[104:107], v[144:145], off offset:768 nt
	global_load_dwordx4 v[108:111], v[146:147], off offset:768 nt
	global_load_dwordx4 v[112:115], v[148:149], off offset:768 nt
	global_load_dwordx4 v[116:119], v[150:151], off offset:768 nt
	global_load_dwordx4 v[120:123], v[152:153], off offset:768 nt
	global_load_dwordx4 v[124:127], v[154:155], off offset:768 nt
	s_mul_i32 s14, s2, 9
	s_mul_i32 s15, s12, 6
	v_lshlrev_b32_e32 v239, 4, v0
	v_add_u32_e32 v240, 0xc000, v239
	v_add_u32_e32 v242, 0x18000, v239
	v_lshlrev_b32_e32 v241, 12, v214
	v_or_b32_e32 v241, v241, v239
	v_add_u32_e32 v252, 0x12000, v236
	v_add_u32_e32 v253, 0x12000, v237
	v_add_u32_e32 v254, 0x12000, v238
	ds_write_b128 v236, v[160:163] offset:0
	ds_write_b128 v237, v[164:167] offset:0
	ds_write_b128 v238, v[168:171] offset:0
	ds_write_b128 v236, v[172:175] offset:24576
	ds_write_b128 v237, v[176:179] offset:24576
	ds_write_b128 v238, v[180:183] offset:24576
	ds_write_b128 v236, v[184:187] offset:49152
	ds_write_b128 v237, v[188:191] offset:49152
	ds_write_b128 v238, v[192:195] offset:49152
	ds_write_b128 v252, v[196:199] offset:0
	ds_write_b128 v253, v[200:203] offset:0
	ds_write_b128 v254, v[204:207] offset:0
	ds_write_b128 v252, v[216:219] offset:24576
	ds_write_b128 v253, v[220:223] offset:24576
	ds_write_b128 v254, v[224:227] offset:24576
	s_waitcnt lgkmcnt(0)
	s_barrier
	ds_read_b128 v[216:219], v239 offset:0
	ds_read_b128 v[220:223], v239 offset:24576
	ds_read_b128 v[224:227], v240 offset:0
	ds_read_b128 v[228:231], v239 offset:1024
	s_waitcnt lgkmcnt(3)
	v_mfma_f32_32x32x16_f16 v[160:175], v[216:219], v[28:31], 0
	ds_read_b128 v[216:219], v239 offset:25600
	s_waitcnt lgkmcnt(3)
	v_mfma_f32_32x32x16_f16 v[176:191], v[220:223], v[28:31], 0
	ds_read_b128 v[220:223], v240 offset:1024
	s_waitcnt lgkmcnt(3)
	v_mfma_f32_32x32x16_f16 v[192:207], v[224:227], v[28:31], 0
	ds_read_b128 v[224:227], v239 offset:2048
	s_waitcnt lgkmcnt(3)
	v_mfma_f32_32x32x16_f16 v[160:175], v[228:231], v[32:35], v[160:175]
	ds_read_b128 v[228:231], v239 offset:26624
	s_waitcnt lgkmcnt(3)
	v_mfma_f32_32x32x16_f16 v[176:191], v[216:219], v[32:35], v[176:191]
	ds_read_b128 v[216:219], v240 offset:2048
	s_waitcnt lgkmcnt(3)
	v_mfma_f32_32x32x16_f16 v[192:207], v[220:223], v[32:35], v[192:207]
	ds_read_b128 v[220:223], v239 offset:3072
	s_waitcnt lgkmcnt(3)
	v_mfma_f32_32x32x16_f16 v[160:175], v[224:227], v[36:39], v[160:175]
	ds_read_b128 v[224:227], v239 offset:27648
	s_waitcnt lgkmcnt(3)
	v_mfma_f32_32x32x16_f16 v[176:191], v[228:231], v[36:39], v[176:191]
	ds_read_b128 v[228:231], v240 offset:3072
	s_waitcnt lgkmcnt(3)
	v_mfma_f32_32x32x16_f16 v[192:207], v[216:219], v[36:39], v[192:207]
	s_waitcnt lgkmcnt(2)
	v_mfma_f32_32x32x16_f16 v[160:175], v[220:223], v[40:43], v[160:175]
	s_waitcnt lgkmcnt(1)
	v_mfma_f32_32x32x16_f16 v[176:191], v[224:227], v[40:43], v[176:191]
	s_waitcnt lgkmcnt(0)
	v_mfma_f32_32x32x16_f16 v[192:207], v[228:231], v[40:43], v[192:207]
	ds_read_b128 v[216:219], v239 offset:4096
	ds_read_b128 v[220:223], v239 offset:28672
	ds_read_b128 v[224:227], v240 offset:4096
	ds_read_b128 v[228:231], v239 offset:5120
	s_waitcnt lgkmcnt(3)
	v_mfma_f32_32x32x16_f16 v[160:175], v[216:219], v[44:47], v[160:175]
	ds_read_b128 v[216:219], v239 offset:29696
	s_waitcnt lgkmcnt(3)
	v_mfma_f32_32x32x16_f16 v[176:191], v[220:223], v[44:47], v[176:191]
	ds_read_b128 v[220:223], v240 offset:5120
	s_waitcnt lgkmcnt(3)
	v_mfma_f32_32x32x16_f16 v[192:207], v[224:227], v[44:47], v[192:207]
	ds_read_b128 v[224:227], v239 offset:6144
	s_waitcnt lgkmcnt(3)
	v_mfma_f32_32x32x16_f16 v[160:175], v[228:231], v[48:51], v[160:175]
	ds_read_b128 v[228:231], v239 offset:30720
	s_waitcnt lgkmcnt(3)
	v_mfma_f32_32x32x16_f16 v[176:191], v[216:219], v[48:51], v[176:191]
	ds_read_b128 v[216:219], v240 offset:6144
	s_waitcnt lgkmcnt(3)
	v_mfma_f32_32x32x16_f16 v[192:207], v[220:223], v[48:51], v[192:207]
	ds_read_b128 v[220:223], v239 offset:7168
	s_waitcnt lgkmcnt(3)
	v_mfma_f32_32x32x16_f16 v[160:175], v[224:227], v[52:55], v[160:175]
	ds_read_b128 v[224:227], v239 offset:31744
	s_waitcnt lgkmcnt(3)
	v_mfma_f32_32x32x16_f16 v[176:191], v[228:231], v[52:55], v[176:191]
	ds_read_b128 v[228:231], v240 offset:7168
	s_waitcnt lgkmcnt(3)
	v_mfma_f32_32x32x16_f16 v[192:207], v[216:219], v[52:55], v[192:207]
	s_waitcnt lgkmcnt(2)
	v_mfma_f32_32x32x16_f16 v[160:175], v[220:223], v[56:59], v[160:175]
	s_waitcnt lgkmcnt(1)
	v_mfma_f32_32x32x16_f16 v[176:191], v[224:227], v[56:59], v[176:191]
	s_waitcnt lgkmcnt(0)
	v_mfma_f32_32x32x16_f16 v[192:207], v[228:231], v[56:59], v[192:207]
	s_waitcnt vmcnt(15)
	v_cvt_pk_f16_f32 v7, v6, v7
	v_cvt_pk_f16_f32 v6, v4, v5
	s_waitcnt vmcnt(14)
	v_cvt_pk_f16_f32 v5, v10, v11
	v_cvt_pk_f16_f32 v4, v8, v9
	ds_write2_b64 v157, v[6:7], v[4:5] offset1:72
	s_waitcnt vmcnt(13)
	v_cvt_pk_f16_f32 v5, v14, v15
	v_cvt_pk_f16_f32 v4, v12, v13
	s_waitcnt vmcnt(12)
	v_cvt_pk_f16_f32 v7, v82, v83
	v_cvt_pk_f16_f32 v6, v80, v81
	ds_write2_b64 v157, v[4:5], v[6:7] offset0:144 offset1:216
	s_waitcnt vmcnt(11)
	v_cvt_pk_f16_f32 v5, v86, v87
	v_cvt_pk_f16_f32 v4, v84, v85
	s_waitcnt vmcnt(10)
	v_cvt_pk_f16_f32 v7, v90, v91
	v_cvt_pk_f16_f32 v6, v88, v89
	ds_write2_b64 v1, v[4:5], v[6:7] offset0:32 offset1:104
	s_waitcnt vmcnt(9)
	v_cvt_pk_f16_f32 v5, v94, v95
	v_cvt_pk_f16_f32 v4, v92, v93
	s_waitcnt vmcnt(8)
	v_cvt_pk_f16_f32 v7, v98, v99
	v_cvt_pk_f16_f32 v6, v96, v97
	ds_write2_b64 v1, v[4:5], v[6:7] offset0:176 offset1:248
	ds_read_b128 v[60:63], v156 offset:49152
	ds_read_b128 v[64:67], v156 offset:49184
	ds_read_b128 v[68:71], v156 offset:49216
	ds_read_b128 v[72:75], v156 offset:49248
	global_load_dwordx4 v[4:7], v[140:141], off offset:1024 nt
	global_load_dwordx4 v[8:11], v[142:143], off offset:1024 nt
	global_load_dwordx4 v[12:15], v[144:145], off offset:1024 nt
	global_load_dwordx4 v[92:95], v[146:147], off offset:1024 nt
	global_load_dwordx4 v[96:99], v[148:149], off offset:1024 nt
	global_load_dwordx4 v[128:131], v[150:151], off offset:1024 nt
	global_load_dwordx4 v[132:135], v[152:153], off offset:1024 nt
	global_load_dwordx4 v[136:139], v[154:155], off offset:1024 nt
	ds_read_b128 v[216:219], v239 offset:8192
	ds_read_b128 v[220:223], v239 offset:32768
	ds_read_b128 v[224:227], v240 offset:8192
	ds_read_b128 v[228:231], v239 offset:9216
	s_waitcnt lgkmcnt(3)
	v_mfma_f32_32x32x16_f16 v[160:175], v[216:219], v[60:63], v[160:175]
	ds_read_b128 v[216:219], v239 offset:33792
	s_waitcnt lgkmcnt(3)
	v_mfma_f32_32x32x16_f16 v[176:191], v[220:223], v[60:63], v[176:191]
	ds_read_b128 v[220:223], v240 offset:9216
	s_waitcnt lgkmcnt(3)
	v_mfma_f32_32x32x16_f16 v[192:207], v[224:227], v[60:63], v[192:207]
	ds_read_b128 v[224:227], v239 offset:10240
	s_waitcnt lgkmcnt(3)
	v_mfma_f32_32x32x16_f16 v[160:175], v[228:231], v[64:67], v[160:175]
	ds_read_b128 v[228:231], v239 offset:34816
	s_waitcnt lgkmcnt(3)
	v_mfma_f32_32x32x16_f16 v[176:191], v[216:219], v[64:67], v[176:191]
	ds_read_b128 v[216:219], v240 offset:10240
	s_waitcnt lgkmcnt(3)
	v_mfma_f32_32x32x16_f16 v[192:207], v[220:223], v[64:67], v[192:207]
	ds_read_b128 v[220:223], v239 offset:11264
	s_waitcnt lgkmcnt(3)
	v_mfma_f32_32x32x16_f16 v[160:175], v[224:227], v[68:71], v[160:175]
	ds_read_b128 v[224:227], v239 offset:35840
	s_waitcnt lgkmcnt(3)
	v_mfma_f32_32x32x16_f16 v[176:191], v[228:231], v[68:71], v[176:191]
	ds_read_b128 v[228:231], v240 offset:11264
	s_waitcnt lgkmcnt(3)
	v_mfma_f32_32x32x16_f16 v[192:207], v[216:219], v[68:71], v[192:207]
	s_waitcnt lgkmcnt(2)
	v_mfma_f32_32x32x16_f16 v[160:175], v[220:223], v[72:75], v[160:175]
	s_waitcnt lgkmcnt(1)
	v_mfma_f32_32x32x16_f16 v[176:191], v[224:227], v[72:75], v[176:191]
	s_waitcnt lgkmcnt(0)
	v_mfma_f32_32x32x16_f16 v[192:207], v[228:231], v[72:75], v[192:207]
	s_waitcnt vmcnt(15)
	v_cvt_pk_f16_f32 v79, v78, v79
	v_cvt_pk_f16_f32 v78, v76, v77
	s_waitcnt vmcnt(14)
	v_cvt_pk_f16_f32 v77, v102, v103
	v_cvt_pk_f16_f32 v76, v100, v101
	ds_write2_b64 v157, v[78:79], v[76:77] offset1:72
	s_waitcnt vmcnt(13)
	v_cvt_pk_f16_f32 v77, v106, v107
	v_cvt_pk_f16_f32 v76, v104, v105
	s_waitcnt vmcnt(12)
	v_cvt_pk_f16_f32 v79, v110, v111
	v_cvt_pk_f16_f32 v78, v108, v109
	ds_write2_b64 v157, v[76:77], v[78:79] offset0:144 offset1:216
	s_waitcnt vmcnt(11)
	v_cvt_pk_f16_f32 v77, v114, v115
	v_cvt_pk_f16_f32 v76, v112, v113
	s_waitcnt vmcnt(10)
	v_cvt_pk_f16_f32 v79, v118, v119
	v_cvt_pk_f16_f32 v78, v116, v117
	ds_write2_b64 v1, v[76:77], v[78:79] offset0:32 offset1:104
	s_waitcnt vmcnt(9)
	v_cvt_pk_f16_f32 v77, v122, v123
	v_cvt_pk_f16_f32 v76, v120, v121
	s_waitcnt vmcnt(8)
	v_cvt_pk_f16_f32 v79, v126, v127
	v_cvt_pk_f16_f32 v78, v124, v125
	ds_write2_b64 v1, v[76:77], v[78:79] offset0:176 offset1:248
	ds_read_b128 v[76:79], v156 offset:49152
	ds_read_b128 v[80:83], v156 offset:49184
	ds_read_b128 v[84:87], v156 offset:49216
	ds_read_b128 v[88:91], v156 offset:49248
	global_load_dwordx4 v[108:111], v[140:141], off offset:1280 nt
	global_load_dwordx4 v[112:115], v[142:143], off offset:1280 nt
	global_load_dwordx4 v[116:119], v[144:145], off offset:1280 nt
	global_load_dwordx4 v[120:123], v[146:147], off offset:1280 nt
	global_load_dwordx4 v[124:127], v[148:149], off offset:1280 nt
	s_nop 0
	global_load_dwordx4 v[140:143], v[150:151], off offset:1280 nt
	global_load_dwordx4 v[144:147], v[152:153], off offset:1280 nt
	s_nop 0
	global_load_dwordx4 v[148:151], v[154:155], off offset:1280 nt
	ds_read_b128 v[216:219], v239 offset:12288
	ds_read_b128 v[220:223], v239 offset:36864
	ds_read_b128 v[224:227], v240 offset:12288
	ds_read_b128 v[228:231], v239 offset:13312
	s_waitcnt lgkmcnt(3)
	v_mfma_f32_32x32x16_f16 v[160:175], v[216:219], v[76:79], v[160:175]
	ds_read_b128 v[216:219], v239 offset:37888
	s_waitcnt lgkmcnt(3)
	v_mfma_f32_32x32x16_f16 v[176:191], v[220:223], v[76:79], v[176:191]
	ds_read_b128 v[220:223], v240 offset:13312
	s_waitcnt lgkmcnt(3)
	v_mfma_f32_32x32x16_f16 v[192:207], v[224:227], v[76:79], v[192:207]
	ds_read_b128 v[224:227], v239 offset:14336
	s_waitcnt lgkmcnt(3)
	v_mfma_f32_32x32x16_f16 v[160:175], v[228:231], v[80:83], v[160:175]
	ds_read_b128 v[228:231], v239 offset:38912
	s_waitcnt lgkmcnt(3)
	v_mfma_f32_32x32x16_f16 v[176:191], v[216:219], v[80:83], v[176:191]
	ds_read_b128 v[216:219], v240 offset:14336
	s_waitcnt lgkmcnt(3)
	v_mfma_f32_32x32x16_f16 v[192:207], v[220:223], v[80:83], v[192:207]
	ds_read_b128 v[220:223], v239 offset:15360
	s_waitcnt lgkmcnt(3)
	v_mfma_f32_32x32x16_f16 v[160:175], v[224:227], v[84:87], v[160:175]
	ds_read_b128 v[224:227], v239 offset:39936
	s_waitcnt lgkmcnt(3)
	v_mfma_f32_32x32x16_f16 v[176:191], v[228:231], v[84:87], v[176:191]
	ds_read_b128 v[228:231], v240 offset:15360
	s_waitcnt lgkmcnt(3)
	v_mfma_f32_32x32x16_f16 v[192:207], v[216:219], v[84:87], v[192:207]
	s_waitcnt lgkmcnt(2)
	v_mfma_f32_32x32x16_f16 v[160:175], v[220:223], v[88:91], v[160:175]
	s_waitcnt lgkmcnt(1)
	v_mfma_f32_32x32x16_f16 v[176:191], v[224:227], v[88:91], v[176:191]
	s_waitcnt lgkmcnt(0)
	v_mfma_f32_32x32x16_f16 v[192:207], v[228:231], v[88:91], v[192:207]
	s_waitcnt vmcnt(15)
	v_cvt_pk_f16_f32 v7, v6, v7
	v_cvt_pk_f16_f32 v6, v4, v5
	s_waitcnt vmcnt(14)
	v_cvt_pk_f16_f32 v5, v10, v11
	v_cvt_pk_f16_f32 v4, v8, v9
	ds_write2_b64 v157, v[6:7], v[4:5] offset1:72
	s_waitcnt vmcnt(13)
	v_cvt_pk_f16_f32 v5, v14, v15
	v_cvt_pk_f16_f32 v4, v12, v13
	s_waitcnt vmcnt(12)
	v_cvt_pk_f16_f32 v7, v94, v95
	v_cvt_pk_f16_f32 v6, v92, v93
	ds_write2_b64 v157, v[4:5], v[6:7] offset0:144 offset1:216
	s_waitcnt vmcnt(11)
	v_cvt_pk_f16_f32 v5, v98, v99
	v_cvt_pk_f16_f32 v4, v96, v97
	s_waitcnt vmcnt(10)
	v_cvt_pk_f16_f32 v7, v130, v131
	v_cvt_pk_f16_f32 v6, v128, v129
	ds_write2_b64 v1, v[4:5], v[6:7] offset0:32 offset1:104
	s_waitcnt vmcnt(9)
	v_cvt_pk_f16_f32 v5, v134, v135
	v_cvt_pk_f16_f32 v4, v132, v133
	s_waitcnt vmcnt(8)
	v_cvt_pk_f16_f32 v7, v138, v139
	v_cvt_pk_f16_f32 v6, v136, v137
	ds_write2_b64 v1, v[4:5], v[6:7] offset0:176 offset1:248
	ds_read_b128 v[92:95], v156 offset:49152
	ds_read_b128 v[96:99], v156 offset:49184
	ds_read_b128 v[100:103], v156 offset:49216
	ds_read_b128 v[104:107], v156 offset:49248
	ds_read_b128 v[216:219], v239 offset:16384
	ds_read_b128 v[220:223], v239 offset:40960
	ds_read_b128 v[224:227], v240 offset:16384
	ds_read_b128 v[228:231], v239 offset:17408
	s_waitcnt lgkmcnt(3)
	v_mfma_f32_32x32x16_f16 v[160:175], v[216:219], v[92:95], v[160:175]
	ds_read_b128 v[216:219], v239 offset:41984
	s_waitcnt lgkmcnt(3)
	v_mfma_f32_32x32x16_f16 v[176:191], v[220:223], v[92:95], v[176:191]
	ds_read_b128 v[220:223], v240 offset:17408
	s_waitcnt lgkmcnt(3)
	v_mfma_f32_32x32x16_f16 v[192:207], v[224:227], v[92:95], v[192:207]
	ds_read_b128 v[224:227], v239 offset:18432
	s_waitcnt lgkmcnt(3)
	v_mfma_f32_32x32x16_f16 v[160:175], v[228:231], v[96:99], v[160:175]
	ds_read_b128 v[228:231], v239 offset:43008
	s_waitcnt lgkmcnt(3)
	v_mfma_f32_32x32x16_f16 v[176:191], v[216:219], v[96:99], v[176:191]
	ds_read_b128 v[216:219], v240 offset:18432
	s_waitcnt lgkmcnt(3)
	v_mfma_f32_32x32x16_f16 v[192:207], v[220:223], v[96:99], v[192:207]
	ds_read_b128 v[220:223], v239 offset:19456
	s_waitcnt lgkmcnt(3)
	v_mfma_f32_32x32x16_f16 v[160:175], v[224:227], v[100:103], v[160:175]
	ds_read_b128 v[224:227], v239 offset:44032
	s_waitcnt lgkmcnt(3)
	v_mfma_f32_32x32x16_f16 v[176:191], v[228:231], v[100:103], v[176:191]
	ds_read_b128 v[228:231], v240 offset:19456
	s_waitcnt lgkmcnt(3)
	v_mfma_f32_32x32x16_f16 v[192:207], v[216:219], v[100:103], v[192:207]
	s_waitcnt lgkmcnt(2)
	v_mfma_f32_32x32x16_f16 v[160:175], v[220:223], v[104:107], v[160:175]
	s_waitcnt lgkmcnt(1)
	v_mfma_f32_32x32x16_f16 v[176:191], v[224:227], v[104:107], v[176:191]
	s_waitcnt lgkmcnt(0)
	v_mfma_f32_32x32x16_f16 v[192:207], v[228:231], v[104:107], v[192:207]
	s_waitcnt vmcnt(7)
	v_cvt_pk_f16_f32 v5, v110, v111
	v_cvt_pk_f16_f32 v4, v108, v109
	s_waitcnt vmcnt(6)
	v_cvt_pk_f16_f32 v7, v114, v115
	v_cvt_pk_f16_f32 v6, v112, v113
	ds_write2_b64 v157, v[4:5], v[6:7] offset1:72
	s_waitcnt vmcnt(5)
	v_cvt_pk_f16_f32 v5, v118, v119
	v_cvt_pk_f16_f32 v4, v116, v117
	s_waitcnt vmcnt(4)
	v_cvt_pk_f16_f32 v7, v122, v123
	v_cvt_pk_f16_f32 v6, v120, v121
	ds_write2_b64 v157, v[4:5], v[6:7] offset0:144 offset1:216
	s_waitcnt vmcnt(3)
	v_cvt_pk_f16_f32 v5, v126, v127
	v_cvt_pk_f16_f32 v4, v124, v125
	s_waitcnt vmcnt(2)
	v_cvt_pk_f16_f32 v7, v142, v143
	v_cvt_pk_f16_f32 v6, v140, v141
	ds_write2_b64 v1, v[4:5], v[6:7] offset0:32 offset1:104
	s_waitcnt vmcnt(1)
	v_cvt_pk_f16_f32 v5, v146, v147
	v_cvt_pk_f16_f32 v4, v144, v145
	s_waitcnt vmcnt(0)
	v_cvt_pk_f16_f32 v7, v150, v151
	v_cvt_pk_f16_f32 v6, v148, v149
	ds_write2_b64 v1, v[4:5], v[6:7] offset0:176 offset1:248
	ds_read_b128 v[108:111], v156 offset:49152
	ds_read_b128 v[112:115], v156 offset:49184
	ds_read_b128 v[116:119], v156 offset:49216
	ds_read_b128 v[120:123], v156 offset:49248
	ds_read_b128 v[216:219], v239 offset:20480
	ds_read_b128 v[220:223], v239 offset:45056
	ds_read_b128 v[224:227], v240 offset:20480
	ds_read_b128 v[228:231], v239 offset:21504
	s_waitcnt lgkmcnt(3)
	v_mfma_f32_32x32x16_f16 v[160:175], v[216:219], v[108:111], v[160:175]
	ds_read_b128 v[216:219], v239 offset:46080
	s_waitcnt lgkmcnt(3)
	v_mfma_f32_32x32x16_f16 v[176:191], v[220:223], v[108:111], v[176:191]
	ds_read_b128 v[220:223], v240 offset:21504
	s_waitcnt lgkmcnt(3)
	v_mfma_f32_32x32x16_f16 v[192:207], v[224:227], v[108:111], v[192:207]
	ds_read_b128 v[224:227], v239 offset:22528
	s_waitcnt lgkmcnt(3)
	v_mfma_f32_32x32x16_f16 v[160:175], v[228:231], v[112:115], v[160:175]
	ds_read_b128 v[228:231], v239 offset:47104
	s_waitcnt lgkmcnt(3)
	v_mfma_f32_32x32x16_f16 v[176:191], v[216:219], v[112:115], v[176:191]
	ds_read_b128 v[216:219], v240 offset:22528
	s_waitcnt lgkmcnt(3)
	v_mfma_f32_32x32x16_f16 v[192:207], v[220:223], v[112:115], v[192:207]
	ds_read_b128 v[220:223], v239 offset:23552
	s_waitcnt lgkmcnt(3)
	v_mfma_f32_32x32x16_f16 v[160:175], v[224:227], v[116:119], v[160:175]
	ds_read_b128 v[224:227], v239 offset:48128
	s_waitcnt lgkmcnt(3)
	v_mfma_f32_32x32x16_f16 v[176:191], v[228:231], v[116:119], v[176:191]
	ds_read_b128 v[228:231], v240 offset:23552
	s_waitcnt lgkmcnt(3)
	v_mfma_f32_32x32x16_f16 v[192:207], v[216:219], v[116:119], v[192:207]
	s_waitcnt lgkmcnt(2)
	v_mfma_f32_32x32x16_f16 v[160:175], v[220:223], v[120:123], v[160:175]
	s_waitcnt lgkmcnt(1)
	v_mfma_f32_32x32x16_f16 v[176:191], v[224:227], v[120:123], v[176:191]
	s_waitcnt lgkmcnt(0)
	v_mfma_f32_32x32x16_f16 v[192:207], v[228:231], v[120:123], v[192:207]
	s_add_i32 s20, s14, 0
	s_cmp_lt_u32 s20, 12
	s_cselect_b32 s26, s8, s10
	s_cselect_b32 s27, s9, s11
	s_cselect_b32 s21, 0, 12
	s_cmp_lt_u32 s20, 24
	s_cselect_b32 s26, s26, s0
	s_cselect_b32 s27, s27, s1
	s_cselect_b32 s21, s21, 24
	s_sub_i32 s20, s20, s21
	s_lshr_b32 s21, s20, 1
	s_and_b32 s20, s20, 1
	s_add_i32 s21, s21, s15
	s_lshl_b32 s21, s21, 15
	s_lshl_b32 s20, s20, 11
	s_add_i32 s21, s21, s20
	s_add_u32 s26, s26, s21
	s_addc_u32 s27, s27, 0
	s_mov_b64 s[28:29], s[26:27]
	s_add_i32 s20, s14, 1
	s_cmp_lt_u32 s20, 12
	s_cselect_b32 s26, s8, s10
	s_cselect_b32 s27, s9, s11
	s_cselect_b32 s21, 0, 12
	s_cmp_lt_u32 s20, 24
	s_cselect_b32 s26, s26, s0
	s_cselect_b32 s27, s27, s1
	s_cselect_b32 s21, s21, 24
	s_sub_i32 s20, s20, s21
	s_lshr_b32 s21, s20, 1
	s_and_b32 s20, s20, 1
	s_add_i32 s21, s21, s15
	s_lshl_b32 s21, s21, 15
	s_lshl_b32 s20, s20, 11
	s_add_i32 s21, s21, s20
	s_add_u32 s26, s26, s21
	s_addc_u32 s27, s27, 0
	s_mov_b64 s[30:31], s[26:27]
	s_add_i32 s20, s14, 2
	s_cmp_lt_u32 s20, 12
	s_cselect_b32 s26, s8, s10
	s_cselect_b32 s27, s9, s11
	s_cselect_b32 s21, 0, 12
	s_cmp_lt_u32 s20, 24
	s_cselect_b32 s26, s26, s0
	s_cselect_b32 s27, s27, s1
	s_cselect_b32 s21, s21, 24
	s_sub_i32 s20, s20, s21
	s_lshr_b32 s21, s20, 1
	s_and_b32 s20, s20, 1
	s_add_i32 s21, s21, s15
	s_lshl_b32 s21, s21, 15
	s_lshl_b32 s20, s20, 11
	s_add_i32 s21, s21, s20
	s_add_u32 s26, s26, s21
	s_addc_u32 s27, s27, 0
	v_cvt_pk_f16_f32 v244, v160, v161
	v_cvt_pk_f16_f32 v245, v162, v163
	v_cvt_pk_f16_f32 v246, v164, v165
	v_cvt_pk_f16_f32 v247, v166, v167
	v_cvt_pk_f16_f32 v248, v168, v169
	v_cvt_pk_f16_f32 v249, v170, v171
	v_cvt_pk_f16_f32 v250, v172, v173
	v_cvt_pk_f16_f32 v251, v174, v175
	global_store_dwordx4 v241, v[244:247], s[28:29] sc1
	global_store_dwordx4 v241, v[248:251], s[28:29] offset:1024 sc1
	v_cvt_pk_f16_f32 v124, v176, v177
	v_cvt_pk_f16_f32 v125, v178, v179
	v_cvt_pk_f16_f32 v126, v180, v181
	v_cvt_pk_f16_f32 v127, v182, v183
	v_cvt_pk_f16_f32 v128, v184, v185
	v_cvt_pk_f16_f32 v129, v186, v187
	v_cvt_pk_f16_f32 v130, v188, v189
	v_cvt_pk_f16_f32 v131, v190, v191
	global_store_dwordx4 v241, v[124:127], s[30:31] sc1
	global_store_dwordx4 v241, v[128:131], s[30:31] offset:1024 sc1
	v_cvt_pk_f16_f32 v132, v192, v193
	v_cvt_pk_f16_f32 v133, v194, v195
	v_cvt_pk_f16_f32 v134, v196, v197
	v_cvt_pk_f16_f32 v135, v198, v199
	v_cvt_pk_f16_f32 v136, v200, v201
	v_cvt_pk_f16_f32 v137, v202, v203
	v_cvt_pk_f16_f32 v138, v204, v205
	v_cvt_pk_f16_f32 v139, v206, v207
	global_store_dwordx4 v241, v[132:135], s[26:27] sc1
	global_store_dwordx4 v241, v[136:139], s[26:27] offset:1024 sc1
	s_waitcnt lgkmcnt(0)
	s_barrier
	s_cmp_lt_u32 s2, 2
	s_cbranch_scc1 .Lqkv_p2S
.Lqkv_p2M:
	ds_read_b128 v[124:127], v240 offset:24576
	ds_read_b128 v[128:131], v240 offset:25600
	ds_read_b128 v[132:135], v240 offset:26624
	ds_read_b128 v[136:139], v240 offset:27648
	ds_read_b128 v[140:143], v240 offset:28672
	ds_read_b128 v[144:147], v240 offset:29696
	ds_read_b128 v[148:151], v240 offset:30720
	ds_read_b128 v[152:155], v240 offset:31744
	ds_read_b128 v[156:159], v240 offset:32768
	ds_read_b128 v[160:163], v240 offset:33792
	ds_read_b128 v[164:167], v240 offset:34816
	ds_read_b128 v[168:171], v240 offset:35840
	ds_read_b128 v[172:175], v240 offset:36864
	ds_read_b128 v[176:179], v240 offset:37888
	ds_read_b128 v[180:183], v240 offset:38912
	ds_read_b128 v[184:187], v240 offset:39936
	ds_read_b128 v[188:191], v240 offset:40960
	ds_read_b128 v[192:195], v240 offset:41984
	ds_read_b128 v[196:199], v240 offset:43008
	ds_read_b128 v[200:203], v240 offset:44032
	ds_read_b128 v[204:207], v240 offset:45056
	ds_read_b128 v[208:211], v240 offset:46080
	ds_read_b128 v[212:215], v240 offset:47104
	ds_read_b128 v[216:219], v240 offset:48128
	s_add_u32 s24, s22, 122880
	s_addc_u32 s25, s23, 0
	s_waitcnt lgkmcnt(14)
	v_mfma_f32_32x32x16_f16 v[0:15], v[124:127], v[28:31], 0
	ds_read_b128 v[124:127], v242 offset:0
	global_load_dwordx4 v[16:19], v236, s[24:25]
	global_load_dwordx4 v[20:23], v237, s[24:25]
	global_load_dwordx4 v[24:27], v238, s[24:25]
	s_waitcnt lgkmcnt(14)
	v_mfma_f32_32x32x16_f16 v[0:15], v[128:131], v[32:35], v[0:15]
	ds_read_b128 v[128:131], v242 offset:1024
	s_waitcnt lgkmcnt(14)
	v_mfma_f32_32x32x16_f16 v[0:15], v[132:135], v[36:39], v[0:15]
	ds_read_b128 v[132:135], v242 offset:2048
	s_waitcnt lgkmcnt(14)
	v_mfma_f32_32x32x16_f16 v[0:15], v[136:139], v[40:43], v[0:15]
	ds_read_b128 v[136:139], v242 offset:3072
	s_waitcnt lgkmcnt(14)
	v_mfma_f32_32x32x16_f16 v[0:15], v[140:143], v[44:47], v[0:15]
	ds_read_b128 v[140:143], v242 offset:4096
	s_waitcnt lgkmcnt(14)
	v_mfma_f32_32x32x16_f16 v[0:15], v[144:147], v[48:51], v[0:15]
	ds_read_b128 v[144:147], v242 offset:5120
	s_waitcnt lgkmcnt(14)
	v_mfma_f32_32x32x16_f16 v[0:15], v[148:151], v[52:55], v[0:15]
	ds_read_b128 v[148:151], v242 offset:6144
	s_waitcnt lgkmcnt(14)
	v_mfma_f32_32x32x16_f16 v[0:15], v[152:155], v[56:59], v[0:15]
	ds_read_b128 v[152:155], v242 offset:7168
	s_waitcnt lgkmcnt(14)
	v_mfma_f32_32x32x16_f16 v[0:15], v[156:159], v[60:63], v[0:15]
	ds_read_b128 v[156:159], v242 offset:8192
	s_waitcnt lgkmcnt(14)
	v_mfma_f32_32x32x16_f16 v[0:15], v[160:163], v[64:67], v[0:15]
	ds_read_b128 v[160:163], v242 offset:9216
	s_waitcnt lgkmcnt(14)
	v_mfma_f32_32x32x16_f16 v[0:15], v[164:167], v[68:71], v[0:15]
	ds_read_b128 v[164:167], v242 offset:10240
	s_waitcnt lgkmcnt(14)
	v_mfma_f32_32x32x16_f16 v[0:15], v[168:171], v[72:75], v[0:15]
	ds_read_b128 v[168:171], v242 offset:11264
	s_waitcnt lgkmcnt(14)
	v_mfma_f32_32x32x16_f16 v[0:15], v[172:175], v[76:79], v[0:15]
	ds_read_b128 v[172:175], v242 offset:12288
	s_waitcnt lgkmcnt(14)
	v_mfma_f32_32x32x16_f16 v[0:15], v[176:179], v[80:83], v[0:15]
	ds_read_b128 v[176:179], v242 offset:13312
	s_waitcnt lgkmcnt(14)
	v_mfma_f32_32x32x16_f16 v[0:15], v[180:183], v[84:87], v[0:15]
	ds_read_b128 v[180:183], v242 offset:14336
	s_waitcnt lgkmcnt(14)
	v_mfma_f32_32x32x16_f16 v[0:15], v[184:187], v[88:91], v[0:15]
	ds_read_b128 v[184:187], v242 offset:15360
	s_waitcnt lgkmcnt(14)
	v_mfma_f32_32x32x16_f16 v[0:15], v[188:191], v[92:95], v[0:15]
	ds_read_b128 v[188:191], v242 offset:16384
	s_waitcnt lgkmcnt(14)
	v_mfma_f32_32x32x16_f16 v[0:15], v[192:195], v[96:99], v[0:15]
	ds_read_b128 v[192:195], v242 offset:17408
	s_waitcnt lgkmcnt(14)
	v_mfma_f32_32x32x16_f16 v[0:15], v[196:199], v[100:103], v[0:15]
	ds_read_b128 v[196:199], v242 offset:18432
	s_waitcnt vmcnt(0)
	ds_write_b128 v252, v[16:19] offset:49152
	ds_write_b128 v253, v[20:23] offset:49152
	ds_write_b128 v254, v[24:27] offset:49152
	s_waitcnt lgkmcnt(14)
	v_mfma_f32_32x32x16_f16 v[0:15], v[200:203], v[104:107], v[0:15]
	ds_read_b128 v[200:203], v242 offset:19456
	s_waitcnt lgkmcnt(14)
	v_mfma_f32_32x32x16_f16 v[0:15], v[204:207], v[108:111], v[0:15]
	ds_read_b128 v[204:207], v242 offset:20480
	s_waitcnt lgkmcnt(14)
	v_mfma_f32_32x32x16_f16 v[0:15], v[208:211], v[112:115], v[0:15]
	ds_read_b128 v[208:211], v242 offset:21504
	s_waitcnt lgkmcnt(14)
	v_mfma_f32_32x32x16_f16 v[0:15], v[212:215], v[116:119], v[0:15]
	ds_read_b128 v[212:215], v242 offset:22528
	s_waitcnt lgkmcnt(14)
	v_mfma_f32_32x32x16_f16 v[0:15], v[216:219], v[120:123], v[0:15]
	ds_read_b128 v[216:219], v242 offset:23552
	s_waitcnt lgkmcnt(5)
	s_barrier
	s_add_u32 s24, s22, 147456
	s_addc_u32 s25, s23, 0
	s_waitcnt lgkmcnt(14)
	v_mfma_f32_32x32x16_f16 v[220:235], v[124:127], v[28:31], 0
	ds_read_b128 v[124:127], v242 offset:24576
	global_load_dwordx4 v[16:19], v236, s[24:25]
	global_load_dwordx4 v[20:23], v237, s[24:25]
	global_load_dwordx4 v[24:27], v238, s[24:25]
	s_waitcnt lgkmcnt(14)
	v_mfma_f32_32x32x16_f16 v[220:235], v[128:131], v[32:35], v[220:235]
	ds_read_b128 v[128:131], v242 offset:25600
	s_add_i32 s20, s14, 3
	s_cmp_lt_u32 s20, 12
	s_cselect_b32 s26, s8, s10
	s_cselect_b32 s27, s9, s11
	s_waitcnt lgkmcnt(14)
	v_mfma_f32_32x32x16_f16 v[220:235], v[132:135], v[36:39], v[220:235]
	ds_read_b128 v[132:135], v242 offset:26624
	s_cselect_b32 s21, 0, 12
	s_cmp_lt_u32 s20, 24
	s_cselect_b32 s26, s26, s0
	s_cselect_b32 s27, s27, s1
	s_waitcnt lgkmcnt(14)
	v_mfma_f32_32x32x16_f16 v[220:235], v[136:139], v[40:43], v[220:235]
	ds_read_b128 v[136:139], v242 offset:27648
	s_cselect_b32 s21, s21, 24
	s_sub_i32 s20, s20, s21
	s_lshr_b32 s21, s20, 1
	s_and_b32 s20, s20, 1
	s_waitcnt lgkmcnt(14)
	v_mfma_f32_32x32x16_f16 v[220:235], v[140:143], v[44:47], v[220:235]
	ds_read_b128 v[140:143], v242 offset:28672
	s_add_i32 s21, s21, s15
	s_lshl_b32 s21, s21, 15
	s_lshl_b32 s20, s20, 11
	s_add_i32 s21, s21, s20
	s_waitcnt lgkmcnt(14)
	v_mfma_f32_32x32x16_f16 v[220:235], v[144:147], v[48:51], v[220:235]
	ds_read_b128 v[144:147], v242 offset:29696
	s_add_u32 s26, s26, s21
	s_addc_u32 s27, s27, 0
	s_waitcnt lgkmcnt(14)
	v_mfma_f32_32x32x16_f16 v[220:235], v[148:151], v[52:55], v[220:235]
	ds_read_b128 v[148:151], v242 offset:30720
	v_cvt_pk_f16_f32 v244, v0, v1
	v_cvt_pk_f16_f32 v245, v2, v3
	s_waitcnt lgkmcnt(14)
	v_mfma_f32_32x32x16_f16 v[220:235], v[152:155], v[56:59], v[220:235]
	ds_read_b128 v[152:155], v242 offset:31744
	v_cvt_pk_f16_f32 v246, v4, v5
	v_cvt_pk_f16_f32 v247, v6, v7
	s_waitcnt lgkmcnt(14)
	v_mfma_f32_32x32x16_f16 v[220:235], v[156:159], v[60:63], v[220:235]
	ds_read_b128 v[156:159], v242 offset:32768
	v_cvt_pk_f16_f32 v248, v8, v9
	v_cvt_pk_f16_f32 v249, v10, v11
	s_waitcnt lgkmcnt(14)
	v_mfma_f32_32x32x16_f16 v[220:235], v[160:163], v[64:67], v[220:235]
	ds_read_b128 v[160:163], v242 offset:33792
	v_cvt_pk_f16_f32 v250, v12, v13
	v_cvt_pk_f16_f32 v251, v14, v15
	s_waitcnt lgkmcnt(14)
	v_mfma_f32_32x32x16_f16 v[220:235], v[164:167], v[68:71], v[220:235]
	ds_read_b128 v[164:167], v242 offset:34816
	global_store_dwordx4 v241, v[244:247], s[26:27] sc1
	s_waitcnt lgkmcnt(14)
	v_mfma_f32_32x32x16_f16 v[220:235], v[168:171], v[72:75], v[220:235]
	ds_read_b128 v[168:171], v242 offset:35840
	global_store_dwordx4 v241, v[248:251], s[26:27] offset:1024 sc1
	s_waitcnt lgkmcnt(14)
	v_mfma_f32_32x32x16_f16 v[220:235], v[172:175], v[76:79], v[220:235]
	ds_read_b128 v[172:175], v242 offset:36864
	s_waitcnt lgkmcnt(14)
	v_mfma_f32_32x32x16_f16 v[220:235], v[176:179], v[80:83], v[220:235]
	ds_read_b128 v[176:179], v242 offset:37888
	s_waitcnt lgkmcnt(14)
	v_mfma_f32_32x32x16_f16 v[220:235], v[180:183], v[84:87], v[220:235]
	ds_read_b128 v[180:183], v242 offset:38912
	s_waitcnt lgkmcnt(14)
	v_mfma_f32_32x32x16_f16 v[220:235], v[184:187], v[88:91], v[220:235]
	ds_read_b128 v[184:187], v242 offset:39936
	s_waitcnt lgkmcnt(14)
	v_mfma_f32_32x32x16_f16 v[220:235], v[188:191], v[92:95], v[220:235]
	ds_read_b128 v[188:191], v242 offset:40960
	s_waitcnt lgkmcnt(14)
	v_mfma_f32_32x32x16_f16 v[220:235], v[192:195], v[96:99], v[220:235]
	ds_read_b128 v[192:195], v242 offset:41984
	s_waitcnt lgkmcnt(14)
	v_mfma_f32_32x32x16_f16 v[220:235], v[196:199], v[100:103], v[220:235]
	ds_read_b128 v[196:199], v242 offset:43008
	s_waitcnt vmcnt(2)
	ds_write_b128 v236, v[16:19] offset:0
	ds_write_b128 v237, v[20:23] offset:0
	ds_write_b128 v238, v[24:27] offset:0
	s_waitcnt lgkmcnt(14)
	v_mfma_f32_32x32x16_f16 v[220:235], v[200:203], v[104:107], v[220:235]
	ds_read_b128 v[200:203], v242 offset:44032
	s_waitcnt lgkmcnt(14)
	v_mfma_f32_32x32x16_f16 v[220:235], v[204:207], v[108:111], v[220:235]
	ds_read_b128 v[204:207], v242 offset:45056
	s_waitcnt lgkmcnt(14)
	v_mfma_f32_32x32x16_f16 v[220:235], v[208:211], v[112:115], v[220:235]
	ds_read_b128 v[208:211], v242 offset:46080
	s_waitcnt lgkmcnt(14)
	v_mfma_f32_32x32x16_f16 v[220:235], v[212:215], v[116:119], v[220:235]
	ds_read_b128 v[212:215], v242 offset:47104
	s_waitcnt lgkmcnt(14)
	v_mfma_f32_32x32x16_f16 v[220:235], v[216:219], v[120:123], v[220:235]
	ds_read_b128 v[216:219], v242 offset:48128
	s_waitcnt lgkmcnt(5)
	s_barrier
	s_add_u32 s24, s22, 172032
	s_addc_u32 s25, s23, 0
	s_waitcnt lgkmcnt(14)
	v_mfma_f32_32x32x16_f16 v[0:15], v[124:127], v[28:31], 0
	ds_read_b128 v[124:127], v239 offset:0
	global_load_dwordx4 v[16:19], v236, s[24:25]
	global_load_dwordx4 v[20:23], v237, s[24:25]
	global_load_dwordx4 v[24:27], v238, s[24:25]
	s_waitcnt lgkmcnt(14)
	v_mfma_f32_32x32x16_f16 v[0:15], v[128:131], v[32:35], v[0:15]
	ds_read_b128 v[128:131], v239 offset:1024
	s_add_i32 s20, s14, 4
	s_cmp_lt_u32 s20, 12
	s_cselect_b32 s26, s8, s10
	s_cselect_b32 s27, s9, s11
	s_waitcnt lgkmcnt(14)
	v_mfma_f32_32x32x16_f16 v[0:15], v[132:135], v[36:39], v[0:15]
	ds_read_b128 v[132:135], v239 offset:2048
	s_cselect_b32 s21, 0, 12
	s_cmp_lt_u32 s20, 24
	s_cselect_b32 s26, s26, s0
	s_cselect_b32 s27, s27, s1
	s_waitcnt lgkmcnt(14)
	v_mfma_f32_32x32x16_f16 v[0:15], v[136:139], v[40:43], v[0:15]
	ds_read_b128 v[136:139], v239 offset:3072
	s_cselect_b32 s21, s21, 24
	s_sub_i32 s20, s20, s21
	s_lshr_b32 s21, s20, 1
	s_and_b32 s20, s20, 1
	s_waitcnt lgkmcnt(14)
	v_mfma_f32_32x32x16_f16 v[0:15], v[140:143], v[44:47], v[0:15]
	ds_read_b128 v[140:143], v239 offset:4096
	s_add_i32 s21, s21, s15
	s_lshl_b32 s21, s21, 15
	s_lshl_b32 s20, s20, 11
	s_add_i32 s21, s21, s20
	s_waitcnt lgkmcnt(14)
	v_mfma_f32_32x32x16_f16 v[0:15], v[144:147], v[48:51], v[0:15]
	ds_read_b128 v[144:147], v239 offset:5120
	s_add_u32 s26, s26, s21
	s_addc_u32 s27, s27, 0
	s_waitcnt lgkmcnt(14)
	v_mfma_f32_32x32x16_f16 v[0:15], v[148:151], v[52:55], v[0:15]
	ds_read_b128 v[148:151], v239 offset:6144
	v_cvt_pk_f16_f32 v244, v220, v221
	v_cvt_pk_f16_f32 v245, v222, v223
	s_waitcnt lgkmcnt(14)
	v_mfma_f32_32x32x16_f16 v[0:15], v[152:155], v[56:59], v[0:15]
	ds_read_b128 v[152:155], v239 offset:7168
	v_cvt_pk_f16_f32 v246, v224, v225
	v_cvt_pk_f16_f32 v247, v226, v227
	s_waitcnt lgkmcnt(14)
	v_mfma_f32_32x32x16_f16 v[0:15], v[156:159], v[60:63], v[0:15]
	ds_read_b128 v[156:159], v239 offset:8192
	v_cvt_pk_f16_f32 v248, v228, v229
	v_cvt_pk_f16_f32 v249, v230, v231
	s_waitcnt lgkmcnt(14)
	v_mfma_f32_32x32x16_f16 v[0:15], v[160:163], v[64:67], v[0:15]
	ds_read_b128 v[160:163], v239 offset:9216
	v_cvt_pk_f16_f32 v250, v232, v233
	v_cvt_pk_f16_f32 v251, v234, v235
	s_waitcnt lgkmcnt(14)
	v_mfma_f32_32x32x16_f16 v[0:15], v[164:167], v[68:71], v[0:15]
	ds_read_b128 v[164:167], v239 offset:10240
	global_store_dwordx4 v241, v[244:247], s[26:27] sc1
	s_waitcnt lgkmcnt(14)
	v_mfma_f32_32x32x16_f16 v[0:15], v[168:171], v[72:75], v[0:15]
	ds_read_b128 v[168:171], v239 offset:11264
	global_store_dwordx4 v241, v[248:251], s[26:27] offset:1024 sc1
	s_waitcnt lgkmcnt(14)
	v_mfma_f32_32x32x16_f16 v[0:15], v[172:175], v[76:79], v[0:15]
	ds_read_b128 v[172:175], v239 offset:12288
	s_waitcnt lgkmcnt(14)
	v_mfma_f32_32x32x16_f16 v[0:15], v[176:179], v[80:83], v[0:15]
	ds_read_b128 v[176:179], v239 offset:13312
	s_waitcnt lgkmcnt(14)
	v_mfma_f32_32x32x16_f16 v[0:15], v[180:183], v[84:87], v[0:15]
	ds_read_b128 v[180:183], v239 offset:14336
	s_waitcnt lgkmcnt(14)
	v_mfma_f32_32x32x16_f16 v[0:15], v[184:187], v[88:91], v[0:15]
	ds_read_b128 v[184:187], v239 offset:15360
	s_waitcnt lgkmcnt(14)
	v_mfma_f32_32x32x16_f16 v[0:15], v[188:191], v[92:95], v[0:15]
	ds_read_b128 v[188:191], v239 offset:16384
	s_waitcnt lgkmcnt(14)
	v_mfma_f32_32x32x16_f16 v[0:15], v[192:195], v[96:99], v[0:15]
	ds_read_b128 v[192:195], v239 offset:17408
	s_waitcnt lgkmcnt(14)
	v_mfma_f32_32x32x16_f16 v[0:15], v[196:199], v[100:103], v[0:15]
	ds_read_b128 v[196:199], v239 offset:18432
	s_waitcnt vmcnt(2)
	ds_write_b128 v236, v[16:19] offset:24576
	ds_write_b128 v237, v[20:23] offset:24576
	ds_write_b128 v238, v[24:27] offset:24576
	s_waitcnt lgkmcnt(14)
	v_mfma_f32_32x32x16_f16 v[0:15], v[200:203], v[104:107], v[0:15]
	ds_read_b128 v[200:203], v239 offset:19456
	s_waitcnt lgkmcnt(14)
	v_mfma_f32_32x32x16_f16 v[0:15], v[204:207], v[108:111], v[0:15]
	ds_read_b128 v[204:207], v239 offset:20480
	s_waitcnt lgkmcnt(14)
	v_mfma_f32_32x32x16_f16 v[0:15], v[208:211], v[112:115], v[0:15]
	ds_read_b128 v[208:211], v239 offset:21504
	s_waitcnt lgkmcnt(14)
	v_mfma_f32_32x32x16_f16 v[0:15], v[212:215], v[116:119], v[0:15]
	ds_read_b128 v[212:215], v239 offset:22528
	s_waitcnt lgkmcnt(14)
	v_mfma_f32_32x32x16_f16 v[0:15], v[216:219], v[120:123], v[0:15]
	ds_read_b128 v[216:219], v239 offset:23552
	s_waitcnt lgkmcnt(5)
	s_barrier
	s_add_u32 s24, s22, 196608
	s_addc_u32 s25, s23, 0
	s_waitcnt lgkmcnt(14)
	v_mfma_f32_32x32x16_f16 v[220:235], v[28:31], v[124:127], 0
	ds_read_b128 v[124:127], v239 offset:24576
	global_load_dwordx4 v[16:19], v236, s[24:25]
	global_load_dwordx4 v[20:23], v237, s[24:25]
	global_load_dwordx4 v[24:27], v238, s[24:25]
	s_waitcnt lgkmcnt(14)
	v_mfma_f32_32x32x16_f16 v[220:235], v[32:35], v[128:131], v[220:235]
	ds_read_b128 v[128:131], v239 offset:25600
	s_add_i32 s20, s14, 5
	s_cmp_lt_u32 s20, 12
	s_cselect_b32 s26, s8, s10
	s_cselect_b32 s27, s9, s11
	s_waitcnt lgkmcnt(14)
	v_mfma_f32_32x32x16_f16 v[220:235], v[36:39], v[132:135], v[220:235]
	ds_read_b128 v[132:135], v239 offset:26624
	s_cselect_b32 s21, 0, 12
	s_cmp_lt_u32 s20, 24
	s_cselect_b32 s26, s26, s0
	s_cselect_b32 s27, s27, s1
	s_waitcnt lgkmcnt(14)
	v_mfma_f32_32x32x16_f16 v[220:235], v[40:43], v[136:139], v[220:235]
	ds_read_b128 v[136:139], v239 offset:27648
	s_cselect_b32 s21, s21, 24
	s_sub_i32 s20, s20, s21
	s_lshr_b32 s21, s20, 1
	s_and_b32 s20, s20, 1
	s_waitcnt lgkmcnt(14)
	v_mfma_f32_32x32x16_f16 v[220:235], v[44:47], v[140:143], v[220:235]
	ds_read_b128 v[140:143], v239 offset:28672
	s_add_i32 s21, s21, s15
	s_lshl_b32 s21, s21, 15
	s_lshl_b32 s20, s20, 11
	s_add_i32 s21, s21, s20
	s_waitcnt lgkmcnt(14)
	v_mfma_f32_32x32x16_f16 v[220:235], v[48:51], v[144:147], v[220:235]
	ds_read_b128 v[144:147], v239 offset:29696
	s_add_u32 s26, s26, s21
	s_addc_u32 s27, s27, 0
	s_waitcnt lgkmcnt(14)
	v_mfma_f32_32x32x16_f16 v[220:235], v[52:55], v[148:151], v[220:235]
	ds_read_b128 v[148:151], v239 offset:30720
	v_cvt_pk_f16_f32 v244, v0, v1
	v_cvt_pk_f16_f32 v245, v2, v3
	s_waitcnt lgkmcnt(14)
	v_mfma_f32_32x32x16_f16 v[220:235], v[56:59], v[152:155], v[220:235]
	ds_read_b128 v[152:155], v239 offset:31744
	v_cvt_pk_f16_f32 v246, v4, v5
	v_cvt_pk_f16_f32 v247, v6, v7
	s_waitcnt lgkmcnt(14)
	v_mfma_f32_32x32x16_f16 v[220:235], v[60:63], v[156:159], v[220:235]
	ds_read_b128 v[156:159], v239 offset:32768
	v_cvt_pk_f16_f32 v248, v8, v9
	v_cvt_pk_f16_f32 v249, v10, v11
	s_waitcnt lgkmcnt(14)
	v_mfma_f32_32x32x16_f16 v[220:235], v[64:67], v[160:163], v[220:235]
	ds_read_b128 v[160:163], v239 offset:33792
	v_cvt_pk_f16_f32 v250, v12, v13
	v_cvt_pk_f16_f32 v251, v14, v15
	s_waitcnt lgkmcnt(14)
	v_mfma_f32_32x32x16_f16 v[220:235], v[68:71], v[164:167], v[220:235]
	ds_read_b128 v[164:167], v239 offset:34816
	global_store_dwordx4 v241, v[244:247], s[26:27] sc1
	s_waitcnt lgkmcnt(14)
	v_mfma_f32_32x32x16_f16 v[220:235], v[72:75], v[168:171], v[220:235]
	ds_read_b128 v[168:171], v239 offset:35840
	global_store_dwordx4 v241, v[248:251], s[26:27] offset:1024 sc1
	s_waitcnt lgkmcnt(14)
	v_mfma_f32_32x32x16_f16 v[220:235], v[76:79], v[172:175], v[220:235]
	ds_read_b128 v[172:175], v239 offset:36864
	s_waitcnt lgkmcnt(14)
	v_mfma_f32_32x32x16_f16 v[220:235], v[80:83], v[176:179], v[220:235]
	ds_read_b128 v[176:179], v239 offset:37888
	s_waitcnt lgkmcnt(14)
	v_mfma_f32_32x32x16_f16 v[220:235], v[84:87], v[180:183], v[220:235]
	ds_read_b128 v[180:183], v239 offset:38912
	s_waitcnt lgkmcnt(14)
	v_mfma_f32_32x32x16_f16 v[220:235], v[88:91], v[184:187], v[220:235]
	ds_read_b128 v[184:187], v239 offset:39936
	s_waitcnt lgkmcnt(14)
	v_mfma_f32_32x32x16_f16 v[220:235], v[92:95], v[188:191], v[220:235]
	ds_read_b128 v[188:191], v239 offset:40960
	s_waitcnt lgkmcnt(14)
	v_mfma_f32_32x32x16_f16 v[220:235], v[96:99], v[192:195], v[220:235]
	ds_read_b128 v[192:195], v239 offset:41984
	s_waitcnt lgkmcnt(14)
	v_mfma_f32_32x32x16_f16 v[220:235], v[100:103], v[196:199], v[220:235]
	ds_read_b128 v[196:199], v239 offset:43008
	s_waitcnt vmcnt(2)
	ds_write_b128 v236, v[16:19] offset:49152
	ds_write_b128 v237, v[20:23] offset:49152
	ds_write_b128 v238, v[24:27] offset:49152
	s_waitcnt lgkmcnt(14)
	v_mfma_f32_32x32x16_f16 v[220:235], v[104:107], v[200:203], v[220:235]
	ds_read_b128 v[200:203], v239 offset:44032
	s_waitcnt lgkmcnt(14)
	v_mfma_f32_32x32x16_f16 v[220:235], v[108:111], v[204:207], v[220:235]
	ds_read_b128 v[204:207], v239 offset:45056
	s_waitcnt lgkmcnt(14)
	v_mfma_f32_32x32x16_f16 v[220:235], v[112:115], v[208:211], v[220:235]
	ds_read_b128 v[208:211], v239 offset:46080
	s_waitcnt lgkmcnt(14)
	v_mfma_f32_32x32x16_f16 v[220:235], v[116:119], v[212:215], v[220:235]
	ds_read_b128 v[212:215], v239 offset:47104
	s_waitcnt lgkmcnt(14)
	v_mfma_f32_32x32x16_f16 v[220:235], v[120:123], v[216:219], v[220:235]
	ds_read_b128 v[216:219], v239 offset:48128
	s_waitcnt lgkmcnt(5)
	s_barrier
	s_waitcnt lgkmcnt(14)
	v_mfma_f32_32x32x16_f16 v[0:15], v[28:31], v[124:127], 0
	ds_read_b128 v[124:127], v240 offset:0
	s_waitcnt lgkmcnt(14)
	v_mfma_f32_32x32x16_f16 v[0:15], v[32:35], v[128:131], v[0:15]
	ds_read_b128 v[128:131], v240 offset:1024
	s_add_i32 s20, s14, 6
	s_cmp_lt_u32 s20, 12
	s_cselect_b32 s26, s8, s10
	s_cselect_b32 s27, s9, s11
	s_waitcnt lgkmcnt(14)
	v_mfma_f32_32x32x16_f16 v[0:15], v[36:39], v[132:135], v[0:15]
	ds_read_b128 v[132:135], v240 offset:2048
	s_cselect_b32 s21, 0, 12
	s_cmp_lt_u32 s20, 24
	s_cselect_b32 s26, s26, s0
	s_cselect_b32 s27, s27, s1
	s_waitcnt lgkmcnt(14)
	v_mfma_f32_32x32x16_f16 v[0:15], v[40:43], v[136:139], v[0:15]
	ds_read_b128 v[136:139], v240 offset:3072
	s_cselect_b32 s21, s21, 24
	s_sub_i32 s20, s20, s21
	s_lshr_b32 s21, s20, 1
	s_and_b32 s20, s20, 1
	s_waitcnt lgkmcnt(14)
	v_mfma_f32_32x32x16_f16 v[0:15], v[44:47], v[140:143], v[0:15]
	ds_read_b128 v[140:143], v240 offset:4096
	s_add_i32 s21, s21, s15
	s_lshl_b32 s21, s21, 15
	s_lshl_b32 s20, s20, 11
	s_add_i32 s21, s21, s20
	s_waitcnt lgkmcnt(14)
	v_mfma_f32_32x32x16_f16 v[0:15], v[48:51], v[144:147], v[0:15]
	ds_read_b128 v[144:147], v240 offset:5120
	s_add_u32 s26, s26, s21
	s_addc_u32 s27, s27, 0
	s_waitcnt lgkmcnt(14)
	v_mfma_f32_32x32x16_f16 v[0:15], v[52:55], v[148:151], v[0:15]
	ds_read_b128 v[148:151], v240 offset:6144
	v_cvt_pk_f16_f32 v244, v220, v221
	v_cvt_pk_f16_f32 v245, v222, v223
	s_waitcnt lgkmcnt(14)
	v_mfma_f32_32x32x16_f16 v[0:15], v[56:59], v[152:155], v[0:15]
	ds_read_b128 v[152:155], v240 offset:7168
	v_cvt_pk_f16_f32 v246, v224, v225
	v_cvt_pk_f16_f32 v247, v226, v227
	s_waitcnt lgkmcnt(14)
	v_mfma_f32_32x32x16_f16 v[0:15], v[60:63], v[156:159], v[0:15]
	ds_read_b128 v[156:159], v240 offset:8192
	v_cvt_pk_f16_f32 v248, v228, v229
	v_cvt_pk_f16_f32 v249, v230, v231
	s_waitcnt lgkmcnt(14)
	v_mfma_f32_32x32x16_f16 v[0:15], v[64:67], v[160:163], v[0:15]
	ds_read_b128 v[160:163], v240 offset:9216
	v_cvt_pk_f16_f32 v250, v232, v233
	v_cvt_pk_f16_f32 v251, v234, v235
	s_waitcnt lgkmcnt(14)
	v_mfma_f32_32x32x16_f16 v[0:15], v[68:71], v[164:167], v[0:15]
	ds_read_b128 v[164:167], v240 offset:10240
	global_store_dwordx4 v241, v[244:247], s[26:27] sc1
	s_waitcnt lgkmcnt(14)
	v_mfma_f32_32x32x16_f16 v[0:15], v[72:75], v[168:171], v[0:15]
	ds_read_b128 v[168:171], v240 offset:11264
	global_store_dwordx4 v241, v[248:251], s[26:27] offset:1024 sc1
	s_waitcnt lgkmcnt(14)
	v_mfma_f32_32x32x16_f16 v[0:15], v[76:79], v[172:175], v[0:15]
	ds_read_b128 v[172:175], v240 offset:12288
	s_waitcnt lgkmcnt(14)
	v_mfma_f32_32x32x16_f16 v[0:15], v[80:83], v[176:179], v[0:15]
	ds_read_b128 v[176:179], v240 offset:13312
	s_waitcnt lgkmcnt(14)
	v_mfma_f32_32x32x16_f16 v[0:15], v[84:87], v[180:183], v[0:15]
	ds_read_b128 v[180:183], v240 offset:14336
	s_waitcnt lgkmcnt(14)
	v_mfma_f32_32x32x16_f16 v[0:15], v[88:91], v[184:187], v[0:15]
	ds_read_b128 v[184:187], v240 offset:15360
	s_waitcnt lgkmcnt(14)
	v_mfma_f32_32x32x16_f16 v[0:15], v[92:95], v[188:191], v[0:15]
	ds_read_b128 v[188:191], v240 offset:16384
	s_waitcnt lgkmcnt(14)
	v_mfma_f32_32x32x16_f16 v[0:15], v[96:99], v[192:195], v[0:15]
	ds_read_b128 v[192:195], v240 offset:17408
	s_waitcnt lgkmcnt(14)
	v_mfma_f32_32x32x16_f16 v[0:15], v[100:103], v[196:199], v[0:15]
	ds_read_b128 v[196:199], v240 offset:18432
	s_waitcnt lgkmcnt(14)
	v_mfma_f32_32x32x16_f16 v[0:15], v[104:107], v[200:203], v[0:15]
	ds_read_b128 v[200:203], v240 offset:19456
	s_waitcnt lgkmcnt(14)
	v_mfma_f32_32x32x16_f16 v[0:15], v[108:111], v[204:207], v[0:15]
	ds_read_b128 v[204:207], v240 offset:20480
	s_waitcnt lgkmcnt(14)
	v_mfma_f32_32x32x16_f16 v[0:15], v[112:115], v[208:211], v[0:15]
	ds_read_b128 v[208:211], v240 offset:21504
	s_waitcnt lgkmcnt(14)
	v_mfma_f32_32x32x16_f16 v[0:15], v[116:119], v[212:215], v[0:15]
	ds_read_b128 v[212:215], v240 offset:22528
	s_waitcnt lgkmcnt(14)
	v_mfma_f32_32x32x16_f16 v[0:15], v[120:123], v[216:219], v[0:15]
	ds_read_b128 v[216:219], v240 offset:23552
	s_waitcnt lgkmcnt(14)
	v_mfma_f32_32x32x16_f16 v[220:235], v[28:31], v[124:127], 0
	s_waitcnt lgkmcnt(14)
	v_mfma_f32_32x32x16_f16 v[220:235], v[32:35], v[128:131], v[220:235]
	s_add_i32 s20, s14, 7
	s_cmp_lt_u32 s20, 12
	s_cselect_b32 s26, s8, s10
	s_cselect_b32 s27, s9, s11
	s_waitcnt lgkmcnt(14)
	v_mfma_f32_32x32x16_f16 v[220:235], v[36:39], v[132:135], v[220:235]
	s_cselect_b32 s21, 0, 12
	s_cmp_lt_u32 s20, 24
	s_cselect_b32 s26, s26, s0
	s_cselect_b32 s27, s27, s1
	s_waitcnt lgkmcnt(14)
	v_mfma_f32_32x32x16_f16 v[220:235], v[40:43], v[136:139], v[220:235]
	s_cselect_b32 s21, s21, 24
	s_sub_i32 s20, s20, s21
	s_lshr_b32 s21, s20, 1
	s_and_b32 s20, s20, 1
	s_waitcnt lgkmcnt(14)
	v_mfma_f32_32x32x16_f16 v[220:235], v[44:47], v[140:143], v[220:235]
	s_add_i32 s21, s21, s15
	s_lshl_b32 s21, s21, 15
	s_lshl_b32 s20, s20, 11
	s_add_i32 s21, s21, s20
	s_waitcnt lgkmcnt(14)
	v_mfma_f32_32x32x16_f16 v[220:235], v[48:51], v[144:147], v[220:235]
	s_add_u32 s26, s26, s21
	s_addc_u32 s27, s27, 0
	s_waitcnt lgkmcnt(14)
	v_mfma_f32_32x32x16_f16 v[220:235], v[52:55], v[148:151], v[220:235]
	v_cvt_pk_f16_f32 v244, v0, v1
	v_cvt_pk_f16_f32 v245, v2, v3
	s_waitcnt lgkmcnt(14)
	v_mfma_f32_32x32x16_f16 v[220:235], v[56:59], v[152:155], v[220:235]
	v_cvt_pk_f16_f32 v246, v4, v5
	v_cvt_pk_f16_f32 v247, v6, v7
	s_waitcnt lgkmcnt(14)
	v_mfma_f32_32x32x16_f16 v[220:235], v[60:63], v[156:159], v[220:235]
	v_cvt_pk_f16_f32 v248, v8, v9
	v_cvt_pk_f16_f32 v249, v10, v11
	s_waitcnt lgkmcnt(14)
	v_mfma_f32_32x32x16_f16 v[220:235], v[64:67], v[160:163], v[220:235]
	v_cvt_pk_f16_f32 v250, v12, v13
	v_cvt_pk_f16_f32 v251, v14, v15
	s_waitcnt lgkmcnt(13)
	v_mfma_f32_32x32x16_f16 v[220:235], v[68:71], v[164:167], v[220:235]
	global_store_dwordx4 v241, v[244:247], s[26:27] sc1
	s_waitcnt lgkmcnt(12)
	v_mfma_f32_32x32x16_f16 v[220:235], v[72:75], v[168:171], v[220:235]
	global_store_dwordx4 v241, v[248:251], s[26:27] offset:1024 sc1
	s_waitcnt lgkmcnt(11)
	v_mfma_f32_32x32x16_f16 v[220:235], v[76:79], v[172:175], v[220:235]
	s_waitcnt lgkmcnt(10)
	v_mfma_f32_32x32x16_f16 v[220:235], v[80:83], v[176:179], v[220:235]
	s_waitcnt lgkmcnt(9)
	v_mfma_f32_32x32x16_f16 v[220:235], v[84:87], v[180:183], v[220:235]
	s_waitcnt lgkmcnt(8)
	v_mfma_f32_32x32x16_f16 v[220:235], v[88:91], v[184:187], v[220:235]
	s_waitcnt lgkmcnt(7)
	v_mfma_f32_32x32x16_f16 v[220:235], v[92:95], v[188:191], v[220:235]
	s_waitcnt lgkmcnt(6)
	v_mfma_f32_32x32x16_f16 v[220:235], v[96:99], v[192:195], v[220:235]
	s_waitcnt lgkmcnt(5)
	v_mfma_f32_32x32x16_f16 v[220:235], v[100:103], v[196:199], v[220:235]
	s_waitcnt lgkmcnt(4)
	v_mfma_f32_32x32x16_f16 v[220:235], v[104:107], v[200:203], v[220:235]
	s_waitcnt lgkmcnt(3)
	v_mfma_f32_32x32x16_f16 v[220:235], v[108:111], v[204:207], v[220:235]
	s_waitcnt lgkmcnt(2)
	v_mfma_f32_32x32x16_f16 v[220:235], v[112:115], v[208:211], v[220:235]
	s_waitcnt lgkmcnt(1)
	v_mfma_f32_32x32x16_f16 v[220:235], v[116:119], v[212:215], v[220:235]
	s_waitcnt lgkmcnt(0)
	v_mfma_f32_32x32x16_f16 v[220:235], v[120:123], v[216:219], v[220:235]
	s_add_i32 s20, s14, 8
	s_cmp_lt_u32 s20, 12
	s_cselect_b32 s26, s8, s10
	s_cselect_b32 s27, s9, s11
	s_cselect_b32 s21, 0, 12
	s_cmp_lt_u32 s20, 24
	s_cselect_b32 s26, s26, s0
	s_cselect_b32 s27, s27, s1
	s_cselect_b32 s21, s21, 24
	s_sub_i32 s20, s20, s21
	s_lshr_b32 s21, s20, 1
	s_and_b32 s20, s20, 1
	s_add_i32 s21, s21, s15
	s_lshl_b32 s21, s21, 15
	s_lshl_b32 s20, s20, 11
	s_add_i32 s21, s21, s20
	s_add_u32 s26, s26, s21
	s_addc_u32 s27, s27, 0
	s_nop 7
	v_cvt_pk_f16_f32 v244, v220, v221
	v_cvt_pk_f16_f32 v245, v222, v223
	v_cvt_pk_f16_f32 v246, v224, v225
	v_cvt_pk_f16_f32 v247, v226, v227
	v_cvt_pk_f16_f32 v248, v228, v229
	v_cvt_pk_f16_f32 v249, v230, v231
	v_cvt_pk_f16_f32 v250, v232, v233
	v_cvt_pk_f16_f32 v251, v234, v235
	global_store_dwordx4 v241, v[244:247], s[26:27] sc1
	global_store_dwordx4 v241, v[248:251], s[26:27] offset:1024 sc1
	s_endpgm
.Lqkv_p2S:
	ds_read_b128 v[124:127], v240 offset:24576
	ds_read_b128 v[128:131], v240 offset:25600
	ds_read_b128 v[132:135], v240 offset:26624
	ds_read_b128 v[136:139], v240 offset:27648
	ds_read_b128 v[140:143], v240 offset:28672
	ds_read_b128 v[144:147], v240 offset:29696
	ds_read_b128 v[148:151], v240 offset:30720
	ds_read_b128 v[152:155], v240 offset:31744
	ds_read_b128 v[156:159], v240 offset:32768
	ds_read_b128 v[160:163], v240 offset:33792
	ds_read_b128 v[164:167], v240 offset:34816
	ds_read_b128 v[168:171], v240 offset:35840
	ds_read_b128 v[172:175], v240 offset:36864
	ds_read_b128 v[176:179], v240 offset:37888
	ds_read_b128 v[180:183], v240 offset:38912
	ds_read_b128 v[184:187], v240 offset:39936
	ds_read_b128 v[188:191], v240 offset:40960
	ds_read_b128 v[192:195], v240 offset:41984
	ds_read_b128 v[196:199], v240 offset:43008
	ds_read_b128 v[200:203], v240 offset:44032
	ds_read_b128 v[204:207], v240 offset:45056
	ds_read_b128 v[208:211], v240 offset:46080
	ds_read_b128 v[212:215], v240 offset:47104
	ds_read_b128 v[216:219], v240 offset:48128
	s_add_u32 s24, s22, 122880
	s_addc_u32 s25, s23, 0
	s_waitcnt lgkmcnt(14)
	v_mfma_f32_32x32x16_f16 v[0:15], v[124:127], v[28:31], 0
	ds_read_b128 v[124:127], v242 offset:0
	global_load_dwordx4 v[16:19], v236, s[24:25]
	global_load_dwordx4 v[20:23], v237, s[24:25]
	global_load_dwordx4 v[24:27], v238, s[24:25]
	s_waitcnt lgkmcnt(14)
	v_mfma_f32_32x32x16_f16 v[0:15], v[128:131], v[32:35], v[0:15]
	ds_read_b128 v[128:131], v242 offset:1024
	s_waitcnt lgkmcnt(14)
	v_mfma_f32_32x32x16_f16 v[0:15], v[132:135], v[36:39], v[0:15]
	ds_read_b128 v[132:135], v242 offset:2048
	s_waitcnt lgkmcnt(14)
	v_mfma_f32_32x32x16_f16 v[0:15], v[136:139], v[40:43], v[0:15]
	ds_read_b128 v[136:139], v242 offset:3072
	s_waitcnt lgkmcnt(14)
	v_mfma_f32_32x32x16_f16 v[0:15], v[140:143], v[44:47], v[0:15]
	ds_read_b128 v[140:143], v242 offset:4096
	s_waitcnt lgkmcnt(14)
	v_mfma_f32_32x32x16_f16 v[0:15], v[144:147], v[48:51], v[0:15]
	ds_read_b128 v[144:147], v242 offset:5120
	s_waitcnt lgkmcnt(14)
	v_mfma_f32_32x32x16_f16 v[0:15], v[148:151], v[52:55], v[0:15]
	ds_read_b128 v[148:151], v242 offset:6144
	s_waitcnt lgkmcnt(14)
	v_mfma_f32_32x32x16_f16 v[0:15], v[152:155], v[56:59], v[0:15]
	ds_read_b128 v[152:155], v242 offset:7168
	s_waitcnt lgkmcnt(14)
	v_mfma_f32_32x32x16_f16 v[0:15], v[156:159], v[60:63], v[0:15]
	ds_read_b128 v[156:159], v242 offset:8192
	s_waitcnt lgkmcnt(14)
	v_mfma_f32_32x32x16_f16 v[0:15], v[160:163], v[64:67], v[0:15]
	ds_read_b128 v[160:163], v242 offset:9216
	s_waitcnt lgkmcnt(14)
	v_mfma_f32_32x32x16_f16 v[0:15], v[164:167], v[68:71], v[0:15]
	ds_read_b128 v[164:167], v242 offset:10240
	s_waitcnt lgkmcnt(14)
	v_mfma_f32_32x32x16_f16 v[0:15], v[168:171], v[72:75], v[0:15]
	ds_read_b128 v[168:171], v242 offset:11264
	s_waitcnt lgkmcnt(14)
	v_mfma_f32_32x32x16_f16 v[0:15], v[172:175], v[76:79], v[0:15]
	ds_read_b128 v[172:175], v242 offset:12288
	s_waitcnt lgkmcnt(14)
	v_mfma_f32_32x32x16_f16 v[0:15], v[176:179], v[80:83], v[0:15]
	ds_read_b128 v[176:179], v242 offset:13312
	s_waitcnt lgkmcnt(14)
	v_mfma_f32_32x32x16_f16 v[0:15], v[180:183], v[84:87], v[0:15]
	ds_read_b128 v[180:183], v242 offset:14336
	s_waitcnt lgkmcnt(14)
	v_mfma_f32_32x32x16_f16 v[0:15], v[184:187], v[88:91], v[0:15]
	ds_read_b128 v[184:187], v242 offset:15360
	s_waitcnt lgkmcnt(14)
	v_mfma_f32_32x32x16_f16 v[0:15], v[188:191], v[92:95], v[0:15]
	ds_read_b128 v[188:191], v242 offset:16384
	s_waitcnt lgkmcnt(14)
	v_mfma_f32_32x32x16_f16 v[0:15], v[192:195], v[96:99], v[0:15]
	ds_read_b128 v[192:195], v242 offset:17408
	s_waitcnt lgkmcnt(14)
	v_mfma_f32_32x32x16_f16 v[0:15], v[196:199], v[100:103], v[0:15]
	ds_read_b128 v[196:199], v242 offset:18432
	s_waitcnt vmcnt(0)
	ds_write_b128 v252, v[16:19] offset:49152
	ds_write_b128 v253, v[20:23] offset:49152
	ds_write_b128 v254, v[24:27] offset:49152
	s_waitcnt lgkmcnt(14)
	v_mfma_f32_32x32x16_f16 v[0:15], v[200:203], v[104:107], v[0:15]
	ds_read_b128 v[200:203], v242 offset:19456
	s_waitcnt lgkmcnt(14)
	v_mfma_f32_32x32x16_f16 v[0:15], v[204:207], v[108:111], v[0:15]
	ds_read_b128 v[204:207], v242 offset:20480
	s_waitcnt lgkmcnt(14)
	v_mfma_f32_32x32x16_f16 v[0:15], v[208:211], v[112:115], v[0:15]
	ds_read_b128 v[208:211], v242 offset:21504
	s_waitcnt lgkmcnt(14)
	v_mfma_f32_32x32x16_f16 v[0:15], v[212:215], v[116:119], v[0:15]
	ds_read_b128 v[212:215], v242 offset:22528
	s_waitcnt lgkmcnt(14)
	v_mfma_f32_32x32x16_f16 v[0:15], v[216:219], v[120:123], v[0:15]
	ds_read_b128 v[216:219], v242 offset:23552
	s_waitcnt lgkmcnt(5)
	s_barrier
	s_add_u32 s24, s22, 147456
	s_addc_u32 s25, s23, 0
	s_waitcnt lgkmcnt(14)
	v_mfma_f32_32x32x16_f16 v[220:235], v[124:127], v[28:31], 0
	ds_read_b128 v[124:127], v242 offset:24576
	global_load_dwordx4 v[16:19], v236, s[24:25]
	global_load_dwordx4 v[20:23], v237, s[24:25]
	global_load_dwordx4 v[24:27], v238, s[24:25]
	s_waitcnt lgkmcnt(14)
	v_mfma_f32_32x32x16_f16 v[220:235], v[128:131], v[32:35], v[220:235]
	ds_read_b128 v[128:131], v242 offset:25600
	s_add_i32 s20, s14, 3
	s_cmp_lt_u32 s20, 12
	s_cselect_b32 s26, s8, s10
	s_cselect_b32 s27, s9, s11
	s_waitcnt lgkmcnt(14)
	v_mfma_f32_32x32x16_f16 v[220:235], v[132:135], v[36:39], v[220:235]
	ds_read_b128 v[132:135], v242 offset:26624
	s_cselect_b32 s21, 0, 12
	s_cmp_lt_u32 s20, 24
	s_cselect_b32 s26, s26, s0
	s_cselect_b32 s27, s27, s1
	s_waitcnt lgkmcnt(14)
	v_mfma_f32_32x32x16_f16 v[220:235], v[136:139], v[40:43], v[220:235]
	ds_read_b128 v[136:139], v242 offset:27648
	s_cselect_b32 s21, s21, 24
	s_sub_i32 s20, s20, s21
	s_lshr_b32 s21, s20, 1
	s_and_b32 s20, s20, 1
	s_waitcnt lgkmcnt(14)
	v_mfma_f32_32x32x16_f16 v[220:235], v[140:143], v[44:47], v[220:235]
	ds_read_b128 v[140:143], v242 offset:28672
	s_add_i32 s21, s21, s15
	s_lshl_b32 s21, s21, 15
	s_lshl_b32 s20, s20, 11
	s_add_i32 s21, s21, s20
	s_waitcnt lgkmcnt(14)
	v_mfma_f32_32x32x16_f16 v[220:235], v[144:147], v[48:51], v[220:235]
	ds_read_b128 v[144:147], v242 offset:29696
	s_add_u32 s26, s26, s21
	s_addc_u32 s27, s27, 0
	s_waitcnt lgkmcnt(14)
	v_mfma_f32_32x32x16_f16 v[220:235], v[148:151], v[52:55], v[220:235]
	ds_read_b128 v[148:151], v242 offset:30720
	v_cvt_pk_f16_f32 v244, v0, v1
	v_cvt_pk_f16_f32 v245, v2, v3
	s_waitcnt lgkmcnt(14)
	v_mfma_f32_32x32x16_f16 v[220:235], v[152:155], v[56:59], v[220:235]
	ds_read_b128 v[152:155], v242 offset:31744
	v_cvt_pk_f16_f32 v246, v4, v5
	v_cvt_pk_f16_f32 v247, v6, v7
	s_waitcnt lgkmcnt(14)
	v_mfma_f32_32x32x16_f16 v[220:235], v[156:159], v[60:63], v[220:235]
	ds_read_b128 v[156:159], v242 offset:32768
	v_cvt_pk_f16_f32 v248, v8, v9
	v_cvt_pk_f16_f32 v249, v10, v11
	s_waitcnt lgkmcnt(14)
	v_mfma_f32_32x32x16_f16 v[220:235], v[160:163], v[64:67], v[220:235]
	ds_read_b128 v[160:163], v242 offset:33792
	v_cvt_pk_f16_f32 v250, v12, v13
	v_cvt_pk_f16_f32 v251, v14, v15
	s_waitcnt lgkmcnt(14)
	v_mfma_f32_32x32x16_f16 v[220:235], v[164:167], v[68:71], v[220:235]
	ds_read_b128 v[164:167], v242 offset:34816
	global_store_dwordx4 v241, v[244:247], s[26:27] sc1
	s_waitcnt lgkmcnt(14)
	v_mfma_f32_32x32x16_f16 v[220:235], v[168:171], v[72:75], v[220:235]
	ds_read_b128 v[168:171], v242 offset:35840
	global_store_dwordx4 v241, v[248:251], s[26:27] offset:1024 sc1
	s_waitcnt lgkmcnt(14)
	v_mfma_f32_32x32x16_f16 v[220:235], v[172:175], v[76:79], v[220:235]
	ds_read_b128 v[172:175], v242 offset:36864
	s_waitcnt lgkmcnt(14)
	v_mfma_f32_32x32x16_f16 v[220:235], v[176:179], v[80:83], v[220:235]
	ds_read_b128 v[176:179], v242 offset:37888
	s_waitcnt lgkmcnt(14)
	v_mfma_f32_32x32x16_f16 v[220:235], v[180:183], v[84:87], v[220:235]
	ds_read_b128 v[180:183], v242 offset:38912
	s_waitcnt lgkmcnt(14)
	v_mfma_f32_32x32x16_f16 v[220:235], v[184:187], v[88:91], v[220:235]
	ds_read_b128 v[184:187], v242 offset:39936
	s_waitcnt lgkmcnt(14)
	v_mfma_f32_32x32x16_f16 v[220:235], v[188:191], v[92:95], v[220:235]
	ds_read_b128 v[188:191], v242 offset:40960
	s_waitcnt lgkmcnt(14)
	v_mfma_f32_32x32x16_f16 v[220:235], v[192:195], v[96:99], v[220:235]
	ds_read_b128 v[192:195], v242 offset:41984
	s_waitcnt lgkmcnt(14)
	v_mfma_f32_32x32x16_f16 v[220:235], v[196:199], v[100:103], v[220:235]
	ds_read_b128 v[196:199], v242 offset:43008
	s_waitcnt vmcnt(2)
	ds_write_b128 v236, v[16:19] offset:0
	ds_write_b128 v237, v[20:23] offset:0
	ds_write_b128 v238, v[24:27] offset:0
	s_waitcnt lgkmcnt(14)
	v_mfma_f32_32x32x16_f16 v[220:235], v[200:203], v[104:107], v[220:235]
	ds_read_b128 v[200:203], v242 offset:44032
	s_waitcnt lgkmcnt(14)
	v_mfma_f32_32x32x16_f16 v[220:235], v[204:207], v[108:111], v[220:235]
	ds_read_b128 v[204:207], v242 offset:45056
	s_waitcnt lgkmcnt(14)
	v_mfma_f32_32x32x16_f16 v[220:235], v[208:211], v[112:115], v[220:235]
	ds_read_b128 v[208:211], v242 offset:46080
	s_waitcnt lgkmcnt(14)
	v_mfma_f32_32x32x16_f16 v[220:235], v[212:215], v[116:119], v[220:235]
	ds_read_b128 v[212:215], v242 offset:47104
	s_waitcnt lgkmcnt(14)
	v_mfma_f32_32x32x16_f16 v[220:235], v[216:219], v[120:123], v[220:235]
	ds_read_b128 v[216:219], v242 offset:48128
	s_waitcnt lgkmcnt(5)
	s_barrier
	s_add_u32 s24, s22, 172032
	s_addc_u32 s25, s23, 0
	s_waitcnt lgkmcnt(14)
	v_mfma_f32_32x32x16_f16 v[0:15], v[124:127], v[28:31], 0
	ds_read_b128 v[124:127], v239 offset:0
	global_load_dwordx4 v[16:19], v236, s[24:25]
	global_load_dwordx4 v[20:23], v237, s[24:25]
	global_load_dwordx4 v[24:27], v238, s[24:25]
	s_waitcnt lgkmcnt(14)
	v_mfma_f32_32x32x16_f16 v[0:15], v[128:131], v[32:35], v[0:15]
	ds_read_b128 v[128:131], v239 offset:1024
	s_add_i32 s20, s14, 4
	s_cmp_lt_u32 s20, 12
	s_cselect_b32 s26, s8, s10
	s_cselect_b32 s27, s9, s11
	s_waitcnt lgkmcnt(14)
	v_mfma_f32_32x32x16_f16 v[0:15], v[132:135], v[36:39], v[0:15]
	ds_read_b128 v[132:135], v239 offset:2048
	s_cselect_b32 s21, 0, 12
	s_cmp_lt_u32 s20, 24
	s_cselect_b32 s26, s26, s0
	s_cselect_b32 s27, s27, s1
	s_waitcnt lgkmcnt(14)
	v_mfma_f32_32x32x16_f16 v[0:15], v[136:139], v[40:43], v[0:15]
	ds_read_b128 v[136:139], v239 offset:3072
	s_cselect_b32 s21, s21, 24
	s_sub_i32 s20, s20, s21
	s_lshr_b32 s21, s20, 1
	s_and_b32 s20, s20, 1
	s_waitcnt lgkmcnt(14)
	v_mfma_f32_32x32x16_f16 v[0:15], v[140:143], v[44:47], v[0:15]
	ds_read_b128 v[140:143], v239 offset:4096
	s_add_i32 s21, s21, s15
	s_lshl_b32 s21, s21, 15
	s_lshl_b32 s20, s20, 11
	s_add_i32 s21, s21, s20
	s_waitcnt lgkmcnt(14)
	v_mfma_f32_32x32x16_f16 v[0:15], v[144:147], v[48:51], v[0:15]
	ds_read_b128 v[144:147], v239 offset:5120
	s_add_u32 s26, s26, s21
	s_addc_u32 s27, s27, 0
	s_waitcnt lgkmcnt(14)
	v_mfma_f32_32x32x16_f16 v[0:15], v[148:151], v[52:55], v[0:15]
	ds_read_b128 v[148:151], v239 offset:6144
	v_cvt_pk_f16_f32 v244, v220, v221
	v_cvt_pk_f16_f32 v245, v222, v223
	s_waitcnt lgkmcnt(14)
	v_mfma_f32_32x32x16_f16 v[0:15], v[152:155], v[56:59], v[0:15]
	ds_read_b128 v[152:155], v239 offset:7168
	v_cvt_pk_f16_f32 v246, v224, v225
	v_cvt_pk_f16_f32 v247, v226, v227
	s_waitcnt lgkmcnt(14)
	v_mfma_f32_32x32x16_f16 v[0:15], v[156:159], v[60:63], v[0:15]
	ds_read_b128 v[156:159], v239 offset:8192
	v_cvt_pk_f16_f32 v248, v228, v229
	v_cvt_pk_f16_f32 v249, v230, v231
	s_waitcnt lgkmcnt(14)
	v_mfma_f32_32x32x16_f16 v[0:15], v[160:163], v[64:67], v[0:15]
	ds_read_b128 v[160:163], v239 offset:9216
	v_cvt_pk_f16_f32 v250, v232, v233
	v_cvt_pk_f16_f32 v251, v234, v235
	s_waitcnt lgkmcnt(14)
	v_mfma_f32_32x32x16_f16 v[0:15], v[164:167], v[68:71], v[0:15]
	ds_read_b128 v[164:167], v239 offset:10240
	global_store_dwordx4 v241, v[244:247], s[26:27] sc1
	s_waitcnt lgkmcnt(14)
	v_mfma_f32_32x32x16_f16 v[0:15], v[168:171], v[72:75], v[0:15]
	ds_read_b128 v[168:171], v239 offset:11264
	global_store_dwordx4 v241, v[248:251], s[26:27] offset:1024 sc1
	s_waitcnt lgkmcnt(14)
	v_mfma_f32_32x32x16_f16 v[0:15], v[172:175], v[76:79], v[0:15]
	ds_read_b128 v[172:175], v239 offset:12288
	s_waitcnt lgkmcnt(14)
	v_mfma_f32_32x32x16_f16 v[0:15], v[176:179], v[80:83], v[0:15]
	ds_read_b128 v[176:179], v239 offset:13312
	s_waitcnt lgkmcnt(14)
	v_mfma_f32_32x32x16_f16 v[0:15], v[180:183], v[84:87], v[0:15]
	ds_read_b128 v[180:183], v239 offset:14336
	s_waitcnt lgkmcnt(14)
	v_mfma_f32_32x32x16_f16 v[0:15], v[184:187], v[88:91], v[0:15]
	ds_read_b128 v[184:187], v239 offset:15360
	s_waitcnt lgkmcnt(14)
	v_mfma_f32_32x32x16_f16 v[0:15], v[188:191], v[92:95], v[0:15]
	ds_read_b128 v[188:191], v239 offset:16384
	s_waitcnt lgkmcnt(14)
	v_mfma_f32_32x32x16_f16 v[0:15], v[192:195], v[96:99], v[0:15]
	ds_read_b128 v[192:195], v239 offset:17408
	s_waitcnt lgkmcnt(14)
	v_mfma_f32_32x32x16_f16 v[0:15], v[196:199], v[100:103], v[0:15]
	ds_read_b128 v[196:199], v239 offset:18432
	s_waitcnt vmcnt(2)
	ds_write_b128 v236, v[16:19] offset:24576
	ds_write_b128 v237, v[20:23] offset:24576
	ds_write_b128 v238, v[24:27] offset:24576
	s_waitcnt lgkmcnt(14)
	v_mfma_f32_32x32x16_f16 v[0:15], v[200:203], v[104:107], v[0:15]
	ds_read_b128 v[200:203], v239 offset:19456
	s_waitcnt lgkmcnt(14)
	v_mfma_f32_32x32x16_f16 v[0:15], v[204:207], v[108:111], v[0:15]
	ds_read_b128 v[204:207], v239 offset:20480
	s_waitcnt lgkmcnt(14)
	v_mfma_f32_32x32x16_f16 v[0:15], v[208:211], v[112:115], v[0:15]
	ds_read_b128 v[208:211], v239 offset:21504
	s_waitcnt lgkmcnt(14)
	v_mfma_f32_32x32x16_f16 v[0:15], v[212:215], v[116:119], v[0:15]
	ds_read_b128 v[212:215], v239 offset:22528
	s_waitcnt lgkmcnt(14)
	v_mfma_f32_32x32x16_f16 v[0:15], v[216:219], v[120:123], v[0:15]
	ds_read_b128 v[216:219], v239 offset:23552
	s_waitcnt lgkmcnt(5)
	s_barrier
	s_add_u32 s24, s22, 196608
	s_addc_u32 s25, s23, 0
	s_waitcnt lgkmcnt(14)
	v_mfma_f32_32x32x16_f16 v[220:235], v[124:127], v[28:31], 0
	ds_read_b128 v[124:127], v239 offset:24576
	global_load_dwordx4 v[16:19], v236, s[24:25]
	global_load_dwordx4 v[20:23], v237, s[24:25]
	global_load_dwordx4 v[24:27], v238, s[24:25]
	s_waitcnt lgkmcnt(14)
	v_mfma_f32_32x32x16_f16 v[220:235], v[128:131], v[32:35], v[220:235]
	ds_read_b128 v[128:131], v239 offset:25600
	s_add_i32 s20, s14, 5
	s_cmp_lt_u32 s20, 12
	s_cselect_b32 s26, s8, s10
	s_cselect_b32 s27, s9, s11
	s_waitcnt lgkmcnt(14)
	v_mfma_f32_32x32x16_f16 v[220:235], v[132:135], v[36:39], v[220:235]
	ds_read_b128 v[132:135], v239 offset:26624
	s_cselect_b32 s21, 0, 12
	s_cmp_lt_u32 s20, 24
	s_cselect_b32 s26, s26, s0
	s_cselect_b32 s27, s27, s1
	s_waitcnt lgkmcnt(14)
	v_mfma_f32_32x32x16_f16 v[220:235], v[136:139], v[40:43], v[220:235]
	ds_read_b128 v[136:139], v239 offset:27648
	s_cselect_b32 s21, s21, 24
	s_sub_i32 s20, s20, s21
	s_lshr_b32 s21, s20, 1
	s_and_b32 s20, s20, 1
	s_waitcnt lgkmcnt(14)
	v_mfma_f32_32x32x16_f16 v[220:235], v[140:143], v[44:47], v[220:235]
	ds_read_b128 v[140:143], v239 offset:28672
	s_add_i32 s21, s21, s15
	s_lshl_b32 s21, s21, 15
	s_lshl_b32 s20, s20, 11
	s_add_i32 s21, s21, s20
	s_waitcnt lgkmcnt(14)
	v_mfma_f32_32x32x16_f16 v[220:235], v[144:147], v[48:51], v[220:235]
	ds_read_b128 v[144:147], v239 offset:29696
	s_add_u32 s26, s26, s21
	s_addc_u32 s27, s27, 0
	s_waitcnt lgkmcnt(14)
	v_mfma_f32_32x32x16_f16 v[220:235], v[148:151], v[52:55], v[220:235]
	ds_read_b128 v[148:151], v239 offset:30720
	v_cvt_pk_f16_f32 v244, v0, v1
	v_cvt_pk_f16_f32 v245, v2, v3
	s_waitcnt lgkmcnt(14)
	v_mfma_f32_32x32x16_f16 v[220:235], v[152:155], v[56:59], v[220:235]
	ds_read_b128 v[152:155], v239 offset:31744
	v_cvt_pk_f16_f32 v246, v4, v5
	v_cvt_pk_f16_f32 v247, v6, v7
	s_waitcnt lgkmcnt(14)
	v_mfma_f32_32x32x16_f16 v[220:235], v[156:159], v[60:63], v[220:235]
	ds_read_b128 v[156:159], v239 offset:32768
	v_cvt_pk_f16_f32 v248, v8, v9
	v_cvt_pk_f16_f32 v249, v10, v11
	s_waitcnt lgkmcnt(14)
	v_mfma_f32_32x32x16_f16 v[220:235], v[160:163], v[64:67], v[220:235]
	ds_read_b128 v[160:163], v239 offset:33792
	v_cvt_pk_f16_f32 v250, v12, v13
	v_cvt_pk_f16_f32 v251, v14, v15
	s_waitcnt lgkmcnt(14)
	v_mfma_f32_32x32x16_f16 v[220:235], v[164:167], v[68:71], v[220:235]
	ds_read_b128 v[164:167], v239 offset:34816
	global_store_dwordx4 v241, v[244:247], s[26:27] sc1
	s_waitcnt lgkmcnt(14)
	v_mfma_f32_32x32x16_f16 v[220:235], v[168:171], v[72:75], v[220:235]
	ds_read_b128 v[168:171], v239 offset:35840
	global_store_dwordx4 v241, v[248:251], s[26:27] offset:1024 sc1
	s_waitcnt lgkmcnt(14)
	v_mfma_f32_32x32x16_f16 v[220:235], v[172:175], v[76:79], v[220:235]
	ds_read_b128 v[172:175], v239 offset:36864
	s_waitcnt lgkmcnt(14)
	v_mfma_f32_32x32x16_f16 v[220:235], v[176:179], v[80:83], v[220:235]
	ds_read_b128 v[176:179], v239 offset:37888
	s_waitcnt lgkmcnt(14)
	v_mfma_f32_32x32x16_f16 v[220:235], v[180:183], v[84:87], v[220:235]
	ds_read_b128 v[180:183], v239 offset:38912
	s_waitcnt lgkmcnt(14)
	v_mfma_f32_32x32x16_f16 v[220:235], v[184:187], v[88:91], v[220:235]
	ds_read_b128 v[184:187], v239 offset:39936
	s_waitcnt lgkmcnt(14)
	v_mfma_f32_32x32x16_f16 v[220:235], v[188:191], v[92:95], v[220:235]
	ds_read_b128 v[188:191], v239 offset:40960
	s_waitcnt lgkmcnt(14)
	v_mfma_f32_32x32x16_f16 v[220:235], v[192:195], v[96:99], v[220:235]
	ds_read_b128 v[192:195], v239 offset:41984
	s_waitcnt lgkmcnt(14)
	v_mfma_f32_32x32x16_f16 v[220:235], v[196:199], v[100:103], v[220:235]
	ds_read_b128 v[196:199], v239 offset:43008
	s_waitcnt vmcnt(2)
	ds_write_b128 v236, v[16:19] offset:49152
	ds_write_b128 v237, v[20:23] offset:49152
	ds_write_b128 v238, v[24:27] offset:49152
	s_waitcnt lgkmcnt(14)
	v_mfma_f32_32x32x16_f16 v[220:235], v[200:203], v[104:107], v[220:235]
	ds_read_b128 v[200:203], v239 offset:44032
	s_waitcnt lgkmcnt(14)
	v_mfma_f32_32x32x16_f16 v[220:235], v[204:207], v[108:111], v[220:235]
	ds_read_b128 v[204:207], v239 offset:45056
	s_waitcnt lgkmcnt(14)
	v_mfma_f32_32x32x16_f16 v[220:235], v[208:211], v[112:115], v[220:235]
	ds_read_b128 v[208:211], v239 offset:46080
	s_waitcnt lgkmcnt(14)
	v_mfma_f32_32x32x16_f16 v[220:235], v[212:215], v[116:119], v[220:235]
	ds_read_b128 v[212:215], v239 offset:47104
	s_waitcnt lgkmcnt(14)
	v_mfma_f32_32x32x16_f16 v[220:235], v[216:219], v[120:123], v[220:235]
	ds_read_b128 v[216:219], v239 offset:48128
	s_waitcnt lgkmcnt(5)
	s_barrier
	s_waitcnt lgkmcnt(14)
	v_mfma_f32_32x32x16_f16 v[0:15], v[124:127], v[28:31], 0
	ds_read_b128 v[124:127], v240 offset:0
	s_waitcnt lgkmcnt(14)
	v_mfma_f32_32x32x16_f16 v[0:15], v[128:131], v[32:35], v[0:15]
	ds_read_b128 v[128:131], v240 offset:1024
	s_add_i32 s20, s14, 6
	s_cmp_lt_u32 s20, 12
	s_cselect_b32 s26, s8, s10
	s_cselect_b32 s27, s9, s11
	s_waitcnt lgkmcnt(14)
	v_mfma_f32_32x32x16_f16 v[0:15], v[132:135], v[36:39], v[0:15]
	ds_read_b128 v[132:135], v240 offset:2048
	s_cselect_b32 s21, 0, 12
	s_cmp_lt_u32 s20, 24
	s_cselect_b32 s26, s26, s0
	s_cselect_b32 s27, s27, s1
	s_waitcnt lgkmcnt(14)
	v_mfma_f32_32x32x16_f16 v[0:15], v[136:139], v[40:43], v[0:15]
	ds_read_b128 v[136:139], v240 offset:3072
	s_cselect_b32 s21, s21, 24
	s_sub_i32 s20, s20, s21
	s_lshr_b32 s21, s20, 1
	s_and_b32 s20, s20, 1
	s_waitcnt lgkmcnt(14)
	v_mfma_f32_32x32x16_f16 v[0:15], v[140:143], v[44:47], v[0:15]
	ds_read_b128 v[140:143], v240 offset:4096
	s_add_i32 s21, s21, s15
	s_lshl_b32 s21, s21, 15
	s_lshl_b32 s20, s20, 11
	s_add_i32 s21, s21, s20
	s_waitcnt lgkmcnt(14)
	v_mfma_f32_32x32x16_f16 v[0:15], v[144:147], v[48:51], v[0:15]
	ds_read_b128 v[144:147], v240 offset:5120
	s_add_u32 s26, s26, s21
	s_addc_u32 s27, s27, 0
	s_waitcnt lgkmcnt(14)
	v_mfma_f32_32x32x16_f16 v[0:15], v[148:151], v[52:55], v[0:15]
	ds_read_b128 v[148:151], v240 offset:6144
	v_cvt_pk_f16_f32 v244, v220, v221
	v_cvt_pk_f16_f32 v245, v222, v223
	s_waitcnt lgkmcnt(14)
	v_mfma_f32_32x32x16_f16 v[0:15], v[152:155], v[56:59], v[0:15]
	ds_read_b128 v[152:155], v240 offset:7168
	v_cvt_pk_f16_f32 v246, v224, v225
	v_cvt_pk_f16_f32 v247, v226, v227
	s_waitcnt lgkmcnt(14)
	v_mfma_f32_32x32x16_f16 v[0:15], v[156:159], v[60:63], v[0:15]
	ds_read_b128 v[156:159], v240 offset:8192
	v_cvt_pk_f16_f32 v248, v228, v229
	v_cvt_pk_f16_f32 v249, v230, v231
	s_waitcnt lgkmcnt(14)
	v_mfma_f32_32x32x16_f16 v[0:15], v[160:163], v[64:67], v[0:15]
	ds_read_b128 v[160:163], v240 offset:9216
	v_cvt_pk_f16_f32 v250, v232, v233
	v_cvt_pk_f16_f32 v251, v234, v235
	s_waitcnt lgkmcnt(14)
	v_mfma_f32_32x32x16_f16 v[0:15], v[164:167], v[68:71], v[0:15]
	ds_read_b128 v[164:167], v240 offset:10240
	global_store_dwordx4 v241, v[244:247], s[26:27] sc1
	s_waitcnt lgkmcnt(14)
	v_mfma_f32_32x32x16_f16 v[0:15], v[168:171], v[72:75], v[0:15]
	ds_read_b128 v[168:171], v240 offset:11264
	global_store_dwordx4 v241, v[248:251], s[26:27] offset:1024 sc1
	s_waitcnt lgkmcnt(14)
	v_mfma_f32_32x32x16_f16 v[0:15], v[172:175], v[76:79], v[0:15]
	ds_read_b128 v[172:175], v240 offset:12288
	s_waitcnt lgkmcnt(14)
	v_mfma_f32_32x32x16_f16 v[0:15], v[176:179], v[80:83], v[0:15]
	ds_read_b128 v[176:179], v240 offset:13312
	s_waitcnt lgkmcnt(14)
	v_mfma_f32_32x32x16_f16 v[0:15], v[180:183], v[84:87], v[0:15]
	ds_read_b128 v[180:183], v240 offset:14336
	s_waitcnt lgkmcnt(14)
	v_mfma_f32_32x32x16_f16 v[0:15], v[184:187], v[88:91], v[0:15]
	ds_read_b128 v[184:187], v240 offset:15360
	s_waitcnt lgkmcnt(14)
	v_mfma_f32_32x32x16_f16 v[0:15], v[188:191], v[92:95], v[0:15]
	ds_read_b128 v[188:191], v240 offset:16384
	s_waitcnt lgkmcnt(14)
	v_mfma_f32_32x32x16_f16 v[0:15], v[192:195], v[96:99], v[0:15]
	ds_read_b128 v[192:195], v240 offset:17408
	s_waitcnt lgkmcnt(14)
	v_mfma_f32_32x32x16_f16 v[0:15], v[196:199], v[100:103], v[0:15]
	ds_read_b128 v[196:199], v240 offset:18432
	s_waitcnt lgkmcnt(14)
	v_mfma_f32_32x32x16_f16 v[0:15], v[200:203], v[104:107], v[0:15]
	ds_read_b128 v[200:203], v240 offset:19456
	s_waitcnt lgkmcnt(14)
	v_mfma_f32_32x32x16_f16 v[0:15], v[204:207], v[108:111], v[0:15]
	ds_read_b128 v[204:207], v240 offset:20480
	s_waitcnt lgkmcnt(14)
	v_mfma_f32_32x32x16_f16 v[0:15], v[208:211], v[112:115], v[0:15]
	ds_read_b128 v[208:211], v240 offset:21504
	s_waitcnt lgkmcnt(14)
	v_mfma_f32_32x32x16_f16 v[0:15], v[212:215], v[116:119], v[0:15]
	ds_read_b128 v[212:215], v240 offset:22528
	s_waitcnt lgkmcnt(14)
	v_mfma_f32_32x32x16_f16 v[0:15], v[216:219], v[120:123], v[0:15]
	ds_read_b128 v[216:219], v240 offset:23552
	s_waitcnt lgkmcnt(14)
	v_mfma_f32_32x32x16_f16 v[220:235], v[124:127], v[28:31], 0
	s_waitcnt lgkmcnt(14)
	v_mfma_f32_32x32x16_f16 v[220:235], v[128:131], v[32:35], v[220:235]
	s_add_i32 s20, s14, 7
	s_cmp_lt_u32 s20, 12
	s_cselect_b32 s26, s8, s10
	s_cselect_b32 s27, s9, s11
	s_waitcnt lgkmcnt(14)
	v_mfma_f32_32x32x16_f16 v[220:235], v[132:135], v[36:39], v[220:235]
	s_cselect_b32 s21, 0, 12
	s_cmp_lt_u32 s20, 24
	s_cselect_b32 s26, s26, s0
	s_cselect_b32 s27, s27, s1
	s_waitcnt lgkmcnt(14)
	v_mfma_f32_32x32x16_f16 v[220:235], v[136:139], v[40:43], v[220:235]
	s_cselect_b32 s21, s21, 24
	s_sub_i32 s20, s20, s21
	s_lshr_b32 s21, s20, 1
	s_and_b32 s20, s20, 1
	s_waitcnt lgkmcnt(14)
	v_mfma_f32_32x32x16_f16 v[220:235], v[140:143], v[44:47], v[220:235]
	s_add_i32 s21, s21, s15
	s_lshl_b32 s21, s21, 15
	s_lshl_b32 s20, s20, 11
	s_add_i32 s21, s21, s20
	s_waitcnt lgkmcnt(14)
	v_mfma_f32_32x32x16_f16 v[220:235], v[144:147], v[48:51], v[220:235]
	s_add_u32 s26, s26, s21
	s_addc_u32 s27, s27, 0
	s_waitcnt lgkmcnt(14)
	v_mfma_f32_32x32x16_f16 v[220:235], v[148:151], v[52:55], v[220:235]
	v_cvt_pk_f16_f32 v244, v0, v1
	v_cvt_pk_f16_f32 v245, v2, v3
	s_waitcnt lgkmcnt(14)
	v_mfma_f32_32x32x16_f16 v[220:235], v[152:155], v[56:59], v[220:235]
	v_cvt_pk_f16_f32 v246, v4, v5
	v_cvt_pk_f16_f32 v247, v6, v7
	s_waitcnt lgkmcnt(14)
	v_mfma_f32_32x32x16_f16 v[220:235], v[156:159], v[60:63], v[220:235]
	v_cvt_pk_f16_f32 v248, v8, v9
	v_cvt_pk_f16_f32 v249, v10, v11
	s_waitcnt lgkmcnt(14)
	v_mfma_f32_32x32x16_f16 v[220:235], v[160:163], v[64:67], v[220:235]
	v_cvt_pk_f16_f32 v250, v12, v13
	v_cvt_pk_f16_f32 v251, v14, v15
	s_waitcnt lgkmcnt(13)
	v_mfma_f32_32x32x16_f16 v[220:235], v[164:167], v[68:71], v[220:235]
	global_store_dwordx4 v241, v[244:247], s[26:27] sc1
	s_waitcnt lgkmcnt(12)
	v_mfma_f32_32x32x16_f16 v[220:235], v[168:171], v[72:75], v[220:235]
	global_store_dwordx4 v241, v[248:251], s[26:27] offset:1024 sc1
	s_waitcnt lgkmcnt(11)
	v_mfma_f32_32x32x16_f16 v[220:235], v[172:175], v[76:79], v[220:235]
	s_waitcnt lgkmcnt(10)
	v_mfma_f32_32x32x16_f16 v[220:235], v[176:179], v[80:83], v[220:235]
	s_waitcnt lgkmcnt(9)
	v_mfma_f32_32x32x16_f16 v[220:235], v[180:183], v[84:87], v[220:235]
	s_waitcnt lgkmcnt(8)
	v_mfma_f32_32x32x16_f16 v[220:235], v[184:187], v[88:91], v[220:235]
	s_waitcnt lgkmcnt(7)
	v_mfma_f32_32x32x16_f16 v[220:235], v[188:191], v[92:95], v[220:235]
	s_waitcnt lgkmcnt(6)
	v_mfma_f32_32x32x16_f16 v[220:235], v[192:195], v[96:99], v[220:235]
	s_waitcnt lgkmcnt(5)
	v_mfma_f32_32x32x16_f16 v[220:235], v[196:199], v[100:103], v[220:235]
	s_waitcnt lgkmcnt(4)
	v_mfma_f32_32x32x16_f16 v[220:235], v[200:203], v[104:107], v[220:235]
	s_waitcnt lgkmcnt(3)
	v_mfma_f32_32x32x16_f16 v[220:235], v[204:207], v[108:111], v[220:235]
	s_waitcnt lgkmcnt(2)
	v_mfma_f32_32x32x16_f16 v[220:235], v[208:211], v[112:115], v[220:235]
	s_waitcnt lgkmcnt(1)
	v_mfma_f32_32x32x16_f16 v[220:235], v[212:215], v[116:119], v[220:235]
	s_waitcnt lgkmcnt(0)
	v_mfma_f32_32x32x16_f16 v[220:235], v[216:219], v[120:123], v[220:235]
	s_add_i32 s20, s14, 8
	s_cmp_lt_u32 s20, 12
	s_cselect_b32 s26, s8, s10
	s_cselect_b32 s27, s9, s11
	s_cselect_b32 s21, 0, 12
	s_cmp_lt_u32 s20, 24
	s_cselect_b32 s26, s26, s0
	s_cselect_b32 s27, s27, s1
	s_cselect_b32 s21, s21, 24
	s_sub_i32 s20, s20, s21
	s_lshr_b32 s21, s20, 1
	s_and_b32 s20, s20, 1
	s_add_i32 s21, s21, s15
	s_lshl_b32 s21, s21, 15
	s_lshl_b32 s20, s20, 11
	s_add_i32 s21, s21, s20
	s_add_u32 s26, s26, s21
	s_addc_u32 s27, s27, 0
	s_nop 7
	v_cvt_pk_f16_f32 v244, v220, v221
	v_cvt_pk_f16_f32 v245, v222, v223
	v_cvt_pk_f16_f32 v246, v224, v225
	v_cvt_pk_f16_f32 v247, v226, v227
	v_cvt_pk_f16_f32 v248, v228, v229
	v_cvt_pk_f16_f32 v249, v230, v231
	v_cvt_pk_f16_f32 v250, v232, v233
	v_cvt_pk_f16_f32 v251, v234, v235
	global_store_dwordx4 v241, v[244:247], s[26:27] sc1
	global_store_dwordx4 v241, v[248:251], s[26:27] offset:1024 sc1
	s_endpgm
.Lqkv_p1N:
	v_mov_b32_e32 v211, 0
	v_lshlrev_b32_e32 v208, 4, v0
	v_mov_b32_e32 v209, v211
	v_lshl_add_u64 v[2:3], s[6:7], 0, v[208:209]
	s_movk_i32 s3, 0x2000
	v_add_co_u32_e32 v4, vcc, s3, v2
	v_lshrrev_b32_e32 v214, 6, v0
	s_nop 0
	v_addc_co_u32_e32 v5, vcc, 0, v3, vcc
	s_movk_i32 s3, 0x4000
	v_add_co_u32_e32 v6, vcc, s3, v2
	v_lshlrev_b32_e32 v1, 5, v214
	v_addc_co_u32_e32 v7, vcc, 0, v3, vcc
	v_lshl_or_b32 v1, s12, 8, v1
	s_movk_i32 s6, 0x600
	v_mov_b64_e32 v[4:5], s[4:5]
	v_mad_i64_i32 v[72:73], s[4:5], v1, s6, v[4:5]
	v_bfe_u32 v1, v0, 4, 2
	v_and_b32_e32 v80, 15, v0
	v_lshlrev_b32_e32 v210, 4, v80
	v_mul_u32_u24_e32 v4, 0x180, v1
	v_lshl_add_u64 v[40:41], v[72:73], 0, v[210:211]
	v_lshlrev_b32_e32 v48, 2, v4
	v_mov_b32_e32 v49, v211
	v_lshl_add_u64 v[12:13], v[40:41], 0, v[48:49]
	s_movk_i32 s4, 0x1000
	v_add_co_u32_e32 v14, vcc, s4, v12
	s_movk_i32 s4, 0x3000
	s_nop 0
	v_addc_co_u32_e32 v15, vcc, 0, v13, vcc
	v_add_co_u32_e32 v32, vcc, s4, v12
	global_load_dwordx4 v[4:7], v[12:13], off nt
	global_load_dwordx4 v[8:11], v[14:15], off offset:2048 nt
	v_addc_co_u32_e32 v33, vcc, 0, v13, vcc
	v_add_co_u32_e32 v34, vcc, s3, v12
	v_or_b32_e32 v64, 0x6000, v48
	v_mov_b32_e32 v65, v211
	v_addc_co_u32_e32 v35, vcc, 0, v13, vcc
	global_load_dwordx4 v[12:15], v[32:33], off nt
	global_load_dwordx4 v[28:31], v[34:35], off offset:2048 nt
	v_lshl_add_u64 v[42:43], v[40:41], 0, v[64:65]
	v_add_u32_e32 v66, 0x7800, v48
	v_mov_b32_e32 v67, v211
	v_add_u32_e32 v74, 0x9000, v48
	v_mov_b32_e32 v75, v211
	v_lshl_add_u64 v[44:45], v[40:41], 0, v[66:67]
	global_load_dwordx4 v[32:35], v[42:43], off nt
	global_load_dwordx4 v[36:39], v[44:45], off nt
	v_lshl_add_u64 v[50:51], v[40:41], 0, v[74:75]
	v_add_u32_e32 v76, 0xa800, v48
	v_mov_b32_e32 v77, v211
	v_lshl_add_u64 v[52:53], v[40:41], 0, v[76:77]
	global_load_dwordx4 v[40:43], v[50:51], off nt
	global_load_dwordx4 v[44:47], v[52:53], off nt
	v_lshl_add_u64 v[48:49], v[72:73], 0, v[48:49]
	v_lshl_add_u64 v[140:141], v[48:49], 0, v[210:211]
	s_mov_b64 s[4:5], 0x1800
	v_lshl_add_u64 v[142:143], v[140:141], 0, s[4:5]
	s_mov_b64 s[4:5], 0x3000
	v_lshl_add_u64 v[64:65], v[72:73], 0, v[64:65]
	v_lshl_add_u64 v[74:75], v[72:73], 0, v[74:75]
	v_lshl_add_u64 v[144:145], v[140:141], 0, s[4:5]
	s_mov_b64 s[4:5], 0x4800
	v_lshl_add_u64 v[148:149], v[64:65], 0, v[210:211]
	v_lshl_add_u64 v[64:65], v[72:73], 0, v[66:67]
	v_lshl_add_u64 v[152:153], v[74:75], 0, v[210:211]
	v_lshl_add_u64 v[72:73], v[72:73], 0, v[76:77]
	global_load_dwordx4 v[48:51], v[140:141], off offset:256 nt
	global_load_dwordx4 v[52:55], v[142:143], off offset:256 nt
	v_lshl_add_u64 v[146:147], v[140:141], 0, s[4:5]
	global_load_dwordx4 v[56:59], v[144:145], off offset:256 nt
	global_load_dwordx4 v[60:63], v[146:147], off offset:256 nt
	v_lshl_add_u64 v[150:151], v[64:65], 0, v[210:211]
	global_load_dwordx4 v[64:67], v[148:149], off offset:256 nt
	global_load_dwordx4 v[68:71], v[150:151], off offset:256 nt
	v_lshl_add_u64 v[154:155], v[72:73], 0, v[210:211]
	global_load_dwordx4 v[72:75], v[152:153], off offset:256 nt
	global_load_dwordx4 v[76:79], v[154:155], off offset:256 nt
	v_mov_b32_e32 v236, v208
	v_add_u32_e32 v237, 0x2000, v208
	v_add_u32_e32 v238, 0x4000, v208
	global_load_dwordx4 v[160:163], v236, s[22:23]
	global_load_dwordx4 v[164:167], v237, s[22:23]
	global_load_dwordx4 v[168:171], v238, s[22:23]
	s_add_u32 s20, s22, 24576
	s_addc_u32 s21, s23, 0
	global_load_dwordx4 v[172:175], v236, s[20:21]
	global_load_dwordx4 v[176:179], v237, s[20:21]
	global_load_dwordx4 v[180:183], v238, s[20:21]
	s_add_u32 s20, s22, 49152
	s_addc_u32 s21, s23, 0
	global_load_dwordx4 v[184:187], v236, s[20:21]
	global_load_dwordx4 v[188:191], v237, s[20:21]
	global_load_dwordx4 v[192:195], v238, s[20:21]
	s_add_u32 s20, s22, 73728
	s_addc_u32 s21, s23, 0
	global_load_dwordx4 v[196:199], v236, s[20:21]
	global_load_dwordx4 v[200:203], v237, s[20:21]
	global_load_dwordx4 v[204:207], v238, s[20:21]
	s_add_u32 s20, s22, 98304
	s_addc_u32 s21, s23, 0
	global_load_dwordx4 v[216:219], v236, s[20:21]
	global_load_dwordx4 v[220:223], v237, s[20:21]
	global_load_dwordx4 v[224:227], v238, s[20:21]
	v_mul_u32_u24_e32 v82, 0x1200, v214
	v_lshl_or_b32 v80, v80, 3, v82
	s_movk_i32 s3, 0x90
	v_mad_u32_u24 v1, v1, s3, v80
	v_add_u32_e32 v157, 0x1e000, v1
	v_and_b32_e32 v81, 31, v0
	v_lshrrev_b32_e32 v83, 1, v0
	v_add_u32_e32 v1, 0x1e800, v1
	v_mul_u32_u24_e32 v81, 0x90, v81
	v_and_b32_e32 v83, 16, v83
	v_add3_u32 v156, v82, v81, v83
	v_add_u32_e32 v156, 0x12000, v156
	s_load_dwordx2 s[0:1], s[0:1], 0x20
	s_mov_b32 s3, 0
	v_and_b32_e32 v0, 63, v0
	s_waitcnt vmcnt(30)
	v_cvt_pk_f16_f32 v7, v6, v7
	v_cvt_pk_f16_f32 v6, v4, v5
	s_waitcnt vmcnt(29)
	v_cvt_pk_f16_f32 v5, v10, v11
	v_cvt_pk_f16_f32 v4, v8, v9
	ds_write2_b64 v157, v[6:7], v[4:5] offset1:72
	s_waitcnt vmcnt(28)
	v_cvt_pk_f16_f32 v5, v14, v15
	v_cvt_pk_f16_f32 v4, v12, v13
	s_waitcnt vmcnt(27)
	v_cvt_pk_f16_f32 v7, v30, v31
	v_cvt_pk_f16_f32 v6, v28, v29
	ds_write2_b64 v157, v[4:5], v[6:7] offset0:144 offset1:216
	s_waitcnt vmcnt(26)
	v_cvt_pk_f16_f32 v5, v34, v35
	v_cvt_pk_f16_f32 v4, v32, v33
	s_waitcnt vmcnt(25)
	v_cvt_pk_f16_f32 v7, v38, v39
	v_cvt_pk_f16_f32 v6, v36, v37
	ds_write2_b64 v1, v[4:5], v[6:7] offset0:32 offset1:104
	s_waitcnt vmcnt(24)
	v_cvt_pk_f16_f32 v5, v42, v43
	v_cvt_pk_f16_f32 v4, v40, v41
	s_waitcnt vmcnt(23)
	v_cvt_pk_f16_f32 v7, v46, v47
	v_cvt_pk_f16_f32 v6, v44, v45
	ds_write2_b64 v1, v[4:5], v[6:7] offset0:176 offset1:248
	ds_read_b128 v[28:31], v156 offset:49152
	ds_read_b128 v[32:35], v156 offset:49184
	ds_read_b128 v[36:39], v156 offset:49216
	ds_read_b128 v[40:43], v156 offset:49248
	global_load_dwordx4 v[4:7], v[140:141], off offset:512 nt
	global_load_dwordx4 v[8:11], v[142:143], off offset:512 nt
	global_load_dwordx4 v[12:15], v[144:145], off offset:512 nt
	global_load_dwordx4 v[80:83], v[146:147], off offset:512 nt
	global_load_dwordx4 v[84:87], v[148:149], off offset:512 nt
	global_load_dwordx4 v[88:91], v[150:151], off offset:512 nt
	global_load_dwordx4 v[92:95], v[152:153], off offset:512 nt
	global_load_dwordx4 v[96:99], v[154:155], off offset:512 nt
	s_waitcnt vmcnt(15)
	v_cvt_pk_f16_f32 v45, v50, v51
	v_cvt_pk_f16_f32 v44, v48, v49
	s_waitcnt vmcnt(14)
	v_cvt_pk_f16_f32 v47, v54, v55
	v_cvt_pk_f16_f32 v46, v52, v53
	ds_write2_b64 v157, v[44:45], v[46:47] offset1:72
	s_waitcnt vmcnt(13)
	v_cvt_pk_f16_f32 v45, v58, v59
	v_cvt_pk_f16_f32 v44, v56, v57
	s_waitcnt vmcnt(12)
	v_cvt_pk_f16_f32 v47, v62, v63
	v_cvt_pk_f16_f32 v46, v60, v61
	ds_write2_b64 v157, v[44:45], v[46:47] offset0:144 offset1:216
	s_waitcnt vmcnt(11)
	v_cvt_pk_f16_f32 v45, v66, v67
	v_cvt_pk_f16_f32 v44, v64, v65
	s_waitcnt vmcnt(10)
	v_cvt_pk_f16_f32 v47, v70, v71
	v_cvt_pk_f16_f32 v46, v68, v69
	ds_write2_b64 v1, v[44:45], v[46:47] offset0:32 offset1:104
	s_waitcnt vmcnt(9)
	v_cvt_pk_f16_f32 v45, v74, v75
	v_cvt_pk_f16_f32 v44, v72, v73
	s_waitcnt vmcnt(8)
	v_cvt_pk_f16_f32 v47, v78, v79
	v_cvt_pk_f16_f32 v46, v76, v77
	ds_write2_b64 v1, v[44:45], v[46:47] offset0:176 offset1:248
	ds_read_b128 v[44:47], v156 offset:49152
	ds_read_b128 v[48:51], v156 offset:49184
	ds_read_b128 v[52:55], v156 offset:49216
	ds_read_b128 v[56:59], v156 offset:49248
	global_load_dwordx4 v[76:79], v[140:141], off offset:768 nt
	global_load_dwordx4 v[100:103], v[142:143], off offset:768 nt
	global_load_dwordx4 v[104:107], v[144:145], off offset:768 nt
	global_load_dwordx4 v[108:111], v[146:147], off offset:768 nt
	global_load_dwordx4 v[112:115], v[148:149], off offset:768 nt
	global_load_dwordx4 v[116:119], v[150:151], off offset:768 nt
	global_load_dwordx4 v[120:123], v[152:153], off offset:768 nt
	global_load_dwordx4 v[124:127], v[154:155], off offset:768 nt
	s_mul_i32 s14, s2, 9
	s_mul_i32 s15, s12, 6
	v_lshlrev_b32_e32 v239, 4, v0
	v_add_u32_e32 v240, 0xc000, v239
	v_add_u32_e32 v242, 0x18000, v239
	v_lshlrev_b32_e32 v241, 12, v214
	v_or_b32_e32 v241, v241, v239
	v_add_u32_e32 v252, 0x12000, v236
	v_add_u32_e32 v253, 0x12000, v237
	v_add_u32_e32 v254, 0x12000, v238
	ds_write_b128 v236, v[160:163] offset:0
	ds_write_b128 v237, v[164:167] offset:0
	ds_write_b128 v238, v[168:171] offset:0
	ds_write_b128 v236, v[172:175] offset:24576
	ds_write_b128 v237, v[176:179] offset:24576
	ds_write_b128 v238, v[180:183] offset:24576
	ds_write_b128 v236, v[184:187] offset:49152
	ds_write_b128 v237, v[188:191] offset:49152
	ds_write_b128 v238, v[192:195] offset:49152
	ds_write_b128 v252, v[196:199] offset:0
	ds_write_b128 v253, v[200:203] offset:0
	ds_write_b128 v254, v[204:207] offset:0
	ds_write_b128 v252, v[216:219] offset:24576
	ds_write_b128 v253, v[220:223] offset:24576
	ds_write_b128 v254, v[224:227] offset:24576
	s_waitcnt lgkmcnt(0)
	s_barrier
	ds_read_b128 v[216:219], v239 offset:0
	ds_read_b128 v[220:223], v239 offset:24576
	ds_read_b128 v[224:227], v240 offset:0
	ds_read_b128 v[228:231], v239 offset:1024
	s_waitcnt lgkmcnt(3)
	v_mfma_f32_32x32x16_f16 v[160:175], v[28:31], v[216:219], 0
	ds_read_b128 v[216:219], v239 offset:25600
	s_waitcnt lgkmcnt(3)
	v_mfma_f32_32x32x16_f16 v[176:191], v[28:31], v[220:223], 0
	ds_read_b128 v[220:223], v240 offset:1024
	s_waitcnt lgkmcnt(3)
	v_mfma_f32_32x32x16_f16 v[192:207], v[28:31], v[224:227], 0
	ds_read_b128 v[224:227], v239 offset:2048
	s_waitcnt lgkmcnt(3)
	v_mfma_f32_32x32x16_f16 v[160:175], v[32:35], v[228:231], v[160:175]
	ds_read_b128 v[228:231], v239 offset:26624
	s_waitcnt lgkmcnt(3)
	v_mfma_f32_32x32x16_f16 v[176:191], v[32:35], v[216:219], v[176:191]
	ds_read_b128 v[216:219], v240 offset:2048
	s_waitcnt lgkmcnt(3)
	v_mfma_f32_32x32x16_f16 v[192:207], v[32:35], v[220:223], v[192:207]
	ds_read_b128 v[220:223], v239 offset:3072
	s_waitcnt lgkmcnt(3)
	v_mfma_f32_32x32x16_f16 v[160:175], v[36:39], v[224:227], v[160:175]
	ds_read_b128 v[224:227], v239 offset:27648
	s_waitcnt lgkmcnt(3)
	v_mfma_f32_32x32x16_f16 v[176:191], v[36:39], v[228:231], v[176:191]
	ds_read_b128 v[228:231], v240 offset:3072
	s_waitcnt lgkmcnt(3)
	v_mfma_f32_32x32x16_f16 v[192:207], v[36:39], v[216:219], v[192:207]
	s_waitcnt lgkmcnt(2)
	v_mfma_f32_32x32x16_f16 v[160:175], v[40:43], v[220:223], v[160:175]
	s_waitcnt lgkmcnt(1)
	v_mfma_f32_32x32x16_f16 v[176:191], v[40:43], v[224:227], v[176:191]
	s_waitcnt lgkmcnt(0)
	v_mfma_f32_32x32x16_f16 v[192:207], v[40:43], v[228:231], v[192:207]
	ds_read_b128 v[216:219], v239 offset:4096
	ds_read_b128 v[220:223], v239 offset:28672
	ds_read_b128 v[224:227], v240 offset:4096
	ds_read_b128 v[228:231], v239 offset:5120
	s_waitcnt lgkmcnt(3)
	v_mfma_f32_32x32x16_f16 v[160:175], v[44:47], v[216:219], v[160:175]
	ds_read_b128 v[216:219], v239 offset:29696
	s_waitcnt lgkmcnt(3)
	v_mfma_f32_32x32x16_f16 v[176:191], v[44:47], v[220:223], v[176:191]
	ds_read_b128 v[220:223], v240 offset:5120
	s_waitcnt lgkmcnt(3)
	v_mfma_f32_32x32x16_f16 v[192:207], v[44:47], v[224:227], v[192:207]
	ds_read_b128 v[224:227], v239 offset:6144
	s_waitcnt lgkmcnt(3)
	v_mfma_f32_32x32x16_f16 v[160:175], v[48:51], v[228:231], v[160:175]
	ds_read_b128 v[228:231], v239 offset:30720
	s_waitcnt lgkmcnt(3)
	v_mfma_f32_32x32x16_f16 v[176:191], v[48:51], v[216:219], v[176:191]
	ds_read_b128 v[216:219], v240 offset:6144
	s_waitcnt lgkmcnt(3)
	v_mfma_f32_32x32x16_f16 v[192:207], v[48:51], v[220:223], v[192:207]
	ds_read_b128 v[220:223], v239 offset:7168
	s_waitcnt lgkmcnt(3)
	v_mfma_f32_32x32x16_f16 v[160:175], v[52:55], v[224:227], v[160:175]
	ds_read_b128 v[224:227], v239 offset:31744
	s_waitcnt lgkmcnt(3)
	v_mfma_f32_32x32x16_f16 v[176:191], v[52:55], v[228:231], v[176:191]
	ds_read_b128 v[228:231], v240 offset:7168
	s_waitcnt lgkmcnt(3)
	v_mfma_f32_32x32x16_f16 v[192:207], v[52:55], v[216:219], v[192:207]
	s_waitcnt lgkmcnt(2)
	v_mfma_f32_32x32x16_f16 v[160:175], v[56:59], v[220:223], v[160:175]
	s_waitcnt lgkmcnt(1)
	v_mfma_f32_32x32x16_f16 v[176:191], v[56:59], v[224:227], v[176:191]
	s_waitcnt lgkmcnt(0)
	v_mfma_f32_32x32x16_f16 v[192:207], v[56:59], v[228:231], v[192:207]
	s_waitcnt vmcnt(15)
	v_cvt_pk_f16_f32 v7, v6, v7
	v_cvt_pk_f16_f32 v6, v4, v5
	s_waitcnt vmcnt(14)
	v_cvt_pk_f16_f32 v5, v10, v11
	v_cvt_pk_f16_f32 v4, v8, v9
	ds_write2_b64 v157, v[6:7], v[4:5] offset1:72
	s_waitcnt vmcnt(13)
	v_cvt_pk_f16_f32 v5, v14, v15
	v_cvt_pk_f16_f32 v4, v12, v13
	s_waitcnt vmcnt(12)
	v_cvt_pk_f16_f32 v7, v82, v83
	v_cvt_pk_f16_f32 v6, v80, v81
	ds_write2_b64 v157, v[4:5], v[6:7] offset0:144 offset1:216
	s_waitcnt vmcnt(11)
	v_cvt_pk_f16_f32 v5, v86, v87
	v_cvt_pk_f16_f32 v4, v84, v85
	s_waitcnt vmcnt(10)
	v_cvt_pk_f16_f32 v7, v90, v91
	v_cvt_pk_f16_f32 v6, v88, v89
	ds_write2_b64 v1, v[4:5], v[6:7] offset0:32 offset1:104
	s_waitcnt vmcnt(9)
	v_cvt_pk_f16_f32 v5, v94, v95
	v_cvt_pk_f16_f32 v4, v92, v93
	s_waitcnt vmcnt(8)
	v_cvt_pk_f16_f32 v7, v98, v99
	v_cvt_pk_f16_f32 v6, v96, v97
	ds_write2_b64 v1, v[4:5], v[6:7] offset0:176 offset1:248
	ds_read_b128 v[60:63], v156 offset:49152
	ds_read_b128 v[64:67], v156 offset:49184
	ds_read_b128 v[68:71], v156 offset:49216
	ds_read_b128 v[72:75], v156 offset:49248
	global_load_dwordx4 v[4:7], v[140:141], off offset:1024 nt
	global_load_dwordx4 v[8:11], v[142:143], off offset:1024 nt
	global_load_dwordx4 v[12:15], v[144:145], off offset:1024 nt
	global_load_dwordx4 v[92:95], v[146:147], off offset:1024 nt
	global_load_dwordx4 v[96:99], v[148:149], off offset:1024 nt
	global_load_dwordx4 v[128:131], v[150:151], off offset:1024 nt
	global_load_dwordx4 v[132:135], v[152:153], off offset:1024 nt
	global_load_dwordx4 v[136:139], v[154:155], off offset:1024 nt
	ds_read_b128 v[216:219], v239 offset:8192
	ds_read_b128 v[220:223], v239 offset:32768
	ds_read_b128 v[224:227], v240 offset:8192
	ds_read_b128 v[228:231], v239 offset:9216
	s_waitcnt lgkmcnt(3)
	v_mfma_f32_32x32x16_f16 v[160:175], v[60:63], v[216:219], v[160:175]
	ds_read_b128 v[216:219], v239 offset:33792
	s_waitcnt lgkmcnt(3)
	v_mfma_f32_32x32x16_f16 v[176:191], v[60:63], v[220:223], v[176:191]
	ds_read_b128 v[220:223], v240 offset:9216
	s_waitcnt lgkmcnt(3)
	v_mfma_f32_32x32x16_f16 v[192:207], v[60:63], v[224:227], v[192:207]
	ds_read_b128 v[224:227], v239 offset:10240
	s_waitcnt lgkmcnt(3)
	v_mfma_f32_32x32x16_f16 v[160:175], v[64:67], v[228:231], v[160:175]
	ds_read_b128 v[228:231], v239 offset:34816
	s_waitcnt lgkmcnt(3)
	v_mfma_f32_32x32x16_f16 v[176:191], v[64:67], v[216:219], v[176:191]
	ds_read_b128 v[216:219], v240 offset:10240
	s_waitcnt lgkmcnt(3)
	v_mfma_f32_32x32x16_f16 v[192:207], v[64:67], v[220:223], v[192:207]
	ds_read_b128 v[220:223], v239 offset:11264
	s_waitcnt lgkmcnt(3)
	v_mfma_f32_32x32x16_f16 v[160:175], v[68:71], v[224:227], v[160:175]
	ds_read_b128 v[224:227], v239 offset:35840
	s_waitcnt lgkmcnt(3)
	v_mfma_f32_32x32x16_f16 v[176:191], v[68:71], v[228:231], v[176:191]
	ds_read_b128 v[228:231], v240 offset:11264
	s_waitcnt lgkmcnt(3)
	v_mfma_f32_32x32x16_f16 v[192:207], v[68:71], v[216:219], v[192:207]
	s_waitcnt lgkmcnt(2)
	v_mfma_f32_32x32x16_f16 v[160:175], v[72:75], v[220:223], v[160:175]
	s_waitcnt lgkmcnt(1)
	v_mfma_f32_32x32x16_f16 v[176:191], v[72:75], v[224:227], v[176:191]
	s_waitcnt lgkmcnt(0)
	v_mfma_f32_32x32x16_f16 v[192:207], v[72:75], v[228:231], v[192:207]
	s_waitcnt vmcnt(15)
	v_cvt_pk_f16_f32 v79, v78, v79
	v_cvt_pk_f16_f32 v78, v76, v77
	s_waitcnt vmcnt(14)
	v_cvt_pk_f16_f32 v77, v102, v103
	v_cvt_pk_f16_f32 v76, v100, v101
	ds_write2_b64 v157, v[78:79], v[76:77] offset1:72
	s_waitcnt vmcnt(13)
	v_cvt_pk_f16_f32 v77, v106, v107
	v_cvt_pk_f16_f32 v76, v104, v105
	s_waitcnt vmcnt(12)
	v_cvt_pk_f16_f32 v79, v110, v111
	v_cvt_pk_f16_f32 v78, v108, v109
	ds_write2_b64 v157, v[76:77], v[78:79] offset0:144 offset1:216
	s_waitcnt vmcnt(11)
	v_cvt_pk_f16_f32 v77, v114, v115
	v_cvt_pk_f16_f32 v76, v112, v113
	s_waitcnt vmcnt(10)
	v_cvt_pk_f16_f32 v79, v118, v119
	v_cvt_pk_f16_f32 v78, v116, v117
	ds_write2_b64 v1, v[76:77], v[78:79] offset0:32 offset1:104
	s_waitcnt vmcnt(9)
	v_cvt_pk_f16_f32 v77, v122, v123
	v_cvt_pk_f16_f32 v76, v120, v121
	s_waitcnt vmcnt(8)
	v_cvt_pk_f16_f32 v79, v126, v127
	v_cvt_pk_f16_f32 v78, v124, v125
	ds_write2_b64 v1, v[76:77], v[78:79] offset0:176 offset1:248
	ds_read_b128 v[76:79], v156 offset:49152
	ds_read_b128 v[80:83], v156 offset:49184
	ds_read_b128 v[84:87], v156 offset:49216
	ds_read_b128 v[88:91], v156 offset:49248
	global_load_dwordx4 v[108:111], v[140:141], off offset:1280 nt
	global_load_dwordx4 v[112:115], v[142:143], off offset:1280 nt
	global_load_dwordx4 v[116:119], v[144:145], off offset:1280 nt
	global_load_dwordx4 v[120:123], v[146:147], off offset:1280 nt
	global_load_dwordx4 v[124:127], v[148:149], off offset:1280 nt
	s_nop 0
	global_load_dwordx4 v[140:143], v[150:151], off offset:1280 nt
	global_load_dwordx4 v[144:147], v[152:153], off offset:1280 nt
	s_nop 0
	global_load_dwordx4 v[148:151], v[154:155], off offset:1280 nt
	ds_read_b128 v[216:219], v239 offset:12288
	ds_read_b128 v[220:223], v239 offset:36864
	ds_read_b128 v[224:227], v240 offset:12288
	ds_read_b128 v[228:231], v239 offset:13312
	s_waitcnt lgkmcnt(3)
	v_mfma_f32_32x32x16_f16 v[160:175], v[76:79], v[216:219], v[160:175]
	ds_read_b128 v[216:219], v239 offset:37888
	s_waitcnt lgkmcnt(3)
	v_mfma_f32_32x32x16_f16 v[176:191], v[76:79], v[220:223], v[176:191]
	ds_read_b128 v[220:223], v240 offset:13312
	s_waitcnt lgkmcnt(3)
	v_mfma_f32_32x32x16_f16 v[192:207], v[76:79], v[224:227], v[192:207]
	ds_read_b128 v[224:227], v239 offset:14336
	s_waitcnt lgkmcnt(3)
	v_mfma_f32_32x32x16_f16 v[160:175], v[80:83], v[228:231], v[160:175]
	ds_read_b128 v[228:231], v239 offset:38912
	s_waitcnt lgkmcnt(3)
	v_mfma_f32_32x32x16_f16 v[176:191], v[80:83], v[216:219], v[176:191]
	ds_read_b128 v[216:219], v240 offset:14336
	s_waitcnt lgkmcnt(3)
	v_mfma_f32_32x32x16_f16 v[192:207], v[80:83], v[220:223], v[192:207]
	ds_read_b128 v[220:223], v239 offset:15360
	s_waitcnt lgkmcnt(3)
	v_mfma_f32_32x32x16_f16 v[160:175], v[84:87], v[224:227], v[160:175]
	ds_read_b128 v[224:227], v239 offset:39936
	s_waitcnt lgkmcnt(3)
	v_mfma_f32_32x32x16_f16 v[176:191], v[84:87], v[228:231], v[176:191]
	ds_read_b128 v[228:231], v240 offset:15360
	s_waitcnt lgkmcnt(3)
	v_mfma_f32_32x32x16_f16 v[192:207], v[84:87], v[216:219], v[192:207]
	s_waitcnt lgkmcnt(2)
	v_mfma_f32_32x32x16_f16 v[160:175], v[88:91], v[220:223], v[160:175]
	s_waitcnt lgkmcnt(1)
	v_mfma_f32_32x32x16_f16 v[176:191], v[88:91], v[224:227], v[176:191]
	s_waitcnt lgkmcnt(0)
	v_mfma_f32_32x32x16_f16 v[192:207], v[88:91], v[228:231], v[192:207]
	s_waitcnt vmcnt(15)
	v_cvt_pk_f16_f32 v7, v6, v7
	v_cvt_pk_f16_f32 v6, v4, v5
	s_waitcnt vmcnt(14)
	v_cvt_pk_f16_f32 v5, v10, v11
	v_cvt_pk_f16_f32 v4, v8, v9
	ds_write2_b64 v157, v[6:7], v[4:5] offset1:72
	s_waitcnt vmcnt(13)
	v_cvt_pk_f16_f32 v5, v14, v15
	v_cvt_pk_f16_f32 v4, v12, v13
	s_waitcnt vmcnt(12)
	v_cvt_pk_f16_f32 v7, v94, v95
	v_cvt_pk_f16_f32 v6, v92, v93
	ds_write2_b64 v157, v[4:5], v[6:7] offset0:144 offset1:216
	s_waitcnt vmcnt(11)
	v_cvt_pk_f16_f32 v5, v98, v99
	v_cvt_pk_f16_f32 v4, v96, v97
	s_waitcnt vmcnt(10)
	v_cvt_pk_f16_f32 v7, v130, v131
	v_cvt_pk_f16_f32 v6, v128, v129
	ds_write2_b64 v1, v[4:5], v[6:7] offset0:32 offset1:104
	s_waitcnt vmcnt(9)
	v_cvt_pk_f16_f32 v5, v134, v135
	v_cvt_pk_f16_f32 v4, v132, v133
	s_waitcnt vmcnt(8)
	v_cvt_pk_f16_f32 v7, v138, v139
	v_cvt_pk_f16_f32 v6, v136, v137
	ds_write2_b64 v1, v[4:5], v[6:7] offset0:176 offset1:248
	ds_read_b128 v[92:95], v156 offset:49152
	ds_read_b128 v[96:99], v156 offset:49184
	ds_read_b128 v[100:103], v156 offset:49216
	ds_read_b128 v[104:107], v156 offset:49248
	ds_read_b128 v[216:219], v239 offset:16384
	ds_read_b128 v[220:223], v239 offset:40960
	ds_read_b128 v[224:227], v240 offset:16384
	ds_read_b128 v[228:231], v239 offset:17408
	s_waitcnt lgkmcnt(3)
	v_mfma_f32_32x32x16_f16 v[160:175], v[92:95], v[216:219], v[160:175]
	ds_read_b128 v[216:219], v239 offset:41984
	s_waitcnt lgkmcnt(3)
	v_mfma_f32_32x32x16_f16 v[176:191], v[92:95], v[220:223], v[176:191]
	ds_read_b128 v[220:223], v240 offset:17408
	s_waitcnt lgkmcnt(3)
	v_mfma_f32_32x32x16_f16 v[192:207], v[92:95], v[224:227], v[192:207]
	ds_read_b128 v[224:227], v239 offset:18432
	s_waitcnt lgkmcnt(3)
	v_mfma_f32_32x32x16_f16 v[160:175], v[96:99], v[228:231], v[160:175]
	ds_read_b128 v[228:231], v239 offset:43008
	s_waitcnt lgkmcnt(3)
	v_mfma_f32_32x32x16_f16 v[176:191], v[96:99], v[216:219], v[176:191]
	ds_read_b128 v[216:219], v240 offset:18432
	s_waitcnt lgkmcnt(3)
	v_mfma_f32_32x32x16_f16 v[192:207], v[96:99], v[220:223], v[192:207]
	ds_read_b128 v[220:223], v239 offset:19456
	s_waitcnt lgkmcnt(3)
	v_mfma_f32_32x32x16_f16 v[160:175], v[100:103], v[224:227], v[160:175]
	ds_read_b128 v[224:227], v239 offset:44032
	s_waitcnt lgkmcnt(3)
	v_mfma_f32_32x32x16_f16 v[176:191], v[100:103], v[228:231], v[176:191]
	ds_read_b128 v[228:231], v240 offset:19456
	s_waitcnt lgkmcnt(3)
	v_mfma_f32_32x32x16_f16 v[192:207], v[100:103], v[216:219], v[192:207]
	s_waitcnt lgkmcnt(2)
	v_mfma_f32_32x32x16_f16 v[160:175], v[104:107], v[220:223], v[160:175]
	s_waitcnt lgkmcnt(1)
	v_mfma_f32_32x32x16_f16 v[176:191], v[104:107], v[224:227], v[176:191]
	s_waitcnt lgkmcnt(0)
	v_mfma_f32_32x32x16_f16 v[192:207], v[104:107], v[228:231], v[192:207]
	s_waitcnt vmcnt(7)
	v_cvt_pk_f16_f32 v5, v110, v111
	v_cvt_pk_f16_f32 v4, v108, v109
	s_waitcnt vmcnt(6)
	v_cvt_pk_f16_f32 v7, v114, v115
	v_cvt_pk_f16_f32 v6, v112, v113
	ds_write2_b64 v157, v[4:5], v[6:7] offset1:72
	s_waitcnt vmcnt(5)
	v_cvt_pk_f16_f32 v5, v118, v119
	v_cvt_pk_f16_f32 v4, v116, v117
	s_waitcnt vmcnt(4)
	v_cvt_pk_f16_f32 v7, v122, v123
	v_cvt_pk_f16_f32 v6, v120, v121
	ds_write2_b64 v157, v[4:5], v[6:7] offset0:144 offset1:216
	s_waitcnt vmcnt(3)
	v_cvt_pk_f16_f32 v5, v126, v127
	v_cvt_pk_f16_f32 v4, v124, v125
	s_waitcnt vmcnt(2)
	v_cvt_pk_f16_f32 v7, v142, v143
	v_cvt_pk_f16_f32 v6, v140, v141
	ds_write2_b64 v1, v[4:5], v[6:7] offset0:32 offset1:104
	s_waitcnt vmcnt(1)
	v_cvt_pk_f16_f32 v5, v146, v147
	v_cvt_pk_f16_f32 v4, v144, v145
	s_waitcnt vmcnt(0)
	v_cvt_pk_f16_f32 v7, v150, v151
	v_cvt_pk_f16_f32 v6, v148, v149
	ds_write2_b64 v1, v[4:5], v[6:7] offset0:176 offset1:248
	ds_read_b128 v[108:111], v156 offset:49152
	ds_read_b128 v[112:115], v156 offset:49184
	ds_read_b128 v[116:119], v156 offset:49216
	ds_read_b128 v[120:123], v156 offset:49248
	ds_read_b128 v[216:219], v239 offset:20480
	ds_read_b128 v[220:223], v239 offset:45056
	ds_read_b128 v[224:227], v240 offset:20480
	ds_read_b128 v[228:231], v239 offset:21504
	s_waitcnt lgkmcnt(3)
	v_mfma_f32_32x32x16_f16 v[160:175], v[108:111], v[216:219], v[160:175]
	ds_read_b128 v[216:219], v239 offset:46080
	s_waitcnt lgkmcnt(3)
	v_mfma_f32_32x32x16_f16 v[176:191], v[108:111], v[220:223], v[176:191]
	ds_read_b128 v[220:223], v240 offset:21504
	s_waitcnt lgkmcnt(3)
	v_mfma_f32_32x32x16_f16 v[192:207], v[108:111], v[224:227], v[192:207]
	ds_read_b128 v[224:227], v239 offset:22528
	s_waitcnt lgkmcnt(3)
	v_mfma_f32_32x32x16_f16 v[160:175], v[112:115], v[228:231], v[160:175]
	ds_read_b128 v[228:231], v239 offset:47104
	s_waitcnt lgkmcnt(3)
	v_mfma_f32_32x32x16_f16 v[176:191], v[112:115], v[216:219], v[176:191]
	ds_read_b128 v[216:219], v240 offset:22528
	s_waitcnt lgkmcnt(3)
	v_mfma_f32_32x32x16_f16 v[192:207], v[112:115], v[220:223], v[192:207]
	ds_read_b128 v[220:223], v239 offset:23552
	s_waitcnt lgkmcnt(3)
	v_mfma_f32_32x32x16_f16 v[160:175], v[116:119], v[224:227], v[160:175]
	ds_read_b128 v[224:227], v239 offset:48128
	s_waitcnt lgkmcnt(3)
	v_mfma_f32_32x32x16_f16 v[176:191], v[116:119], v[228:231], v[176:191]
	ds_read_b128 v[228:231], v240 offset:23552
	s_waitcnt lgkmcnt(3)
	v_mfma_f32_32x32x16_f16 v[192:207], v[116:119], v[216:219], v[192:207]
	s_waitcnt lgkmcnt(2)
	v_mfma_f32_32x32x16_f16 v[160:175], v[120:123], v[220:223], v[160:175]
	s_waitcnt lgkmcnt(1)
	v_mfma_f32_32x32x16_f16 v[176:191], v[120:123], v[224:227], v[176:191]
	s_waitcnt lgkmcnt(0)
	v_mfma_f32_32x32x16_f16 v[192:207], v[120:123], v[228:231], v[192:207]
	s_add_i32 s20, s14, 0
	s_cmp_lt_u32 s20, 12
	s_cselect_b32 s26, s8, s10
	s_cselect_b32 s27, s9, s11
	s_cselect_b32 s21, 0, 12
	s_cmp_lt_u32 s20, 24
	s_cselect_b32 s26, s26, s0
	s_cselect_b32 s27, s27, s1
	s_cselect_b32 s21, s21, 24
	s_sub_i32 s20, s20, s21
	s_lshr_b32 s21, s20, 1
	s_and_b32 s20, s20, 1
	s_add_i32 s21, s21, s15
	s_lshl_b32 s21, s21, 15
	s_lshl_b32 s20, s20, 11
	s_add_i32 s21, s21, s20
	s_add_u32 s26, s26, s21
	s_addc_u32 s27, s27, 0
	s_mov_b64 s[28:29], s[26:27]
	s_add_i32 s20, s14, 1
	s_cmp_lt_u32 s20, 12
	s_cselect_b32 s26, s8, s10
	s_cselect_b32 s27, s9, s11
	s_cselect_b32 s21, 0, 12
	s_cmp_lt_u32 s20, 24
	s_cselect_b32 s26, s26, s0
	s_cselect_b32 s27, s27, s1
	s_cselect_b32 s21, s21, 24
	s_sub_i32 s20, s20, s21
	s_lshr_b32 s21, s20, 1
	s_and_b32 s20, s20, 1
	s_add_i32 s21, s21, s15
	s_lshl_b32 s21, s21, 15
	s_lshl_b32 s20, s20, 11
	s_add_i32 s21, s21, s20
	s_add_u32 s26, s26, s21
	s_addc_u32 s27, s27, 0
	s_mov_b64 s[30:31], s[26:27]
	s_add_i32 s20, s14, 2
	s_cmp_lt_u32 s20, 12
	s_cselect_b32 s26, s8, s10
	s_cselect_b32 s27, s9, s11
	s_cselect_b32 s21, 0, 12
	s_cmp_lt_u32 s20, 24
	s_cselect_b32 s26, s26, s0
	s_cselect_b32 s27, s27, s1
	s_cselect_b32 s21, s21, 24
	s_sub_i32 s20, s20, s21
	s_lshr_b32 s21, s20, 1
	s_and_b32 s20, s20, 1
	s_add_i32 s21, s21, s15
	s_lshl_b32 s21, s21, 15
	s_lshl_b32 s20, s20, 11
	s_add_i32 s21, s21, s20
	s_add_u32 s26, s26, s21
	s_addc_u32 s27, s27, 0
	v_cvt_pk_f16_f32 v244, v160, v161
	v_cvt_pk_f16_f32 v245, v162, v163
	v_cvt_pk_f16_f32 v246, v164, v165
	v_cvt_pk_f16_f32 v247, v166, v167
	v_cvt_pk_f16_f32 v248, v168, v169
	v_cvt_pk_f16_f32 v249, v170, v171
	v_cvt_pk_f16_f32 v250, v172, v173
	v_cvt_pk_f16_f32 v251, v174, v175
	global_store_dwordx4 v241, v[244:247], s[28:29] sc1
	global_store_dwordx4 v241, v[248:251], s[28:29] offset:1024 sc1
	v_cvt_pk_f16_f32 v124, v176, v177
	v_cvt_pk_f16_f32 v125, v178, v179
	v_cvt_pk_f16_f32 v126, v180, v181
	v_cvt_pk_f16_f32 v127, v182, v183
	v_cvt_pk_f16_f32 v128, v184, v185
	v_cvt_pk_f16_f32 v129, v186, v187
	v_cvt_pk_f16_f32 v130, v188, v189
	v_cvt_pk_f16_f32 v131, v190, v191
	global_store_dwordx4 v241, v[124:127], s[30:31] sc1
	global_store_dwordx4 v241, v[128:131], s[30:31] offset:1024 sc1
	v_cvt_pk_f16_f32 v132, v192, v193
	v_cvt_pk_f16_f32 v133, v194, v195
	v_cvt_pk_f16_f32 v134, v196, v197
	v_cvt_pk_f16_f32 v135, v198, v199
	v_cvt_pk_f16_f32 v136, v200, v201
	v_cvt_pk_f16_f32 v137, v202, v203
	v_cvt_pk_f16_f32 v138, v204, v205
	v_cvt_pk_f16_f32 v139, v206, v207
	global_store_dwordx4 v241, v[132:135], s[26:27] sc1
	global_store_dwordx4 v241, v[136:139], s[26:27] offset:1024 sc1
	s_waitcnt lgkmcnt(0)
	s_barrier
.Lqkv_p2N:
	ds_read_b128 v[124:127], v240 offset:24576
	ds_read_b128 v[128:131], v240 offset:25600
	ds_read_b128 v[132:135], v240 offset:26624
	ds_read_b128 v[136:139], v240 offset:27648
	ds_read_b128 v[140:143], v240 offset:28672
	ds_read_b128 v[144:147], v240 offset:29696
	ds_read_b128 v[148:151], v240 offset:30720
	ds_read_b128 v[152:155], v240 offset:31744
	ds_read_b128 v[156:159], v240 offset:32768
	ds_read_b128 v[160:163], v240 offset:33792
	ds_read_b128 v[164:167], v240 offset:34816
	ds_read_b128 v[168:171], v240 offset:35840
	ds_read_b128 v[172:175], v240 offset:36864
	ds_read_b128 v[176:179], v240 offset:37888
	ds_read_b128 v[180:183], v240 offset:38912
	ds_read_b128 v[184:187], v240 offset:39936
	ds_read_b128 v[188:191], v240 offset:40960
	ds_read_b128 v[192:195], v240 offset:41984
	ds_read_b128 v[196:199], v240 offset:43008
	ds_read_b128 v[200:203], v240 offset:44032
	ds_read_b128 v[204:207], v240 offset:45056
	ds_read_b128 v[208:211], v240 offset:46080
	ds_read_b128 v[212:215], v240 offset:47104
	ds_read_b128 v[216:219], v240 offset:48128
	s_add_u32 s24, s22, 122880
	s_addc_u32 s25, s23, 0
	s_waitcnt lgkmcnt(14)
	v_mfma_f32_32x32x16_f16 v[0:15], v[28:31], v[124:127], 0
	ds_read_b128 v[124:127], v242 offset:0
	global_load_dwordx4 v[16:19], v236, s[24:25]
	global_load_dwordx4 v[20:23], v237, s[24:25]
	global_load_dwordx4 v[24:27], v238, s[24:25]
	s_waitcnt lgkmcnt(14)
	v_mfma_f32_32x32x16_f16 v[0:15], v[32:35], v[128:131], v[0:15]
	ds_read_b128 v[128:131], v242 offset:1024
	s_waitcnt lgkmcnt(14)
	v_mfma_f32_32x32x16_f16 v[0:15], v[36:39], v[132:135], v[0:15]
	ds_read_b128 v[132:135], v242 offset:2048
	s_waitcnt lgkmcnt(14)
	v_mfma_f32_32x32x16_f16 v[0:15], v[40:43], v[136:139], v[0:15]
	ds_read_b128 v[136:139], v242 offset:3072
	s_waitcnt lgkmcnt(14)
	v_mfma_f32_32x32x16_f16 v[0:15], v[44:47], v[140:143], v[0:15]
	ds_read_b128 v[140:143], v242 offset:4096
	s_waitcnt lgkmcnt(14)
	v_mfma_f32_32x32x16_f16 v[0:15], v[48:51], v[144:147], v[0:15]
	ds_read_b128 v[144:147], v242 offset:5120
	s_waitcnt lgkmcnt(14)
	v_mfma_f32_32x32x16_f16 v[0:15], v[52:55], v[148:151], v[0:15]
	ds_read_b128 v[148:151], v242 offset:6144
	s_waitcnt lgkmcnt(14)
	v_mfma_f32_32x32x16_f16 v[0:15], v[56:59], v[152:155], v[0:15]
	ds_read_b128 v[152:155], v242 offset:7168
	s_waitcnt lgkmcnt(14)
	v_mfma_f32_32x32x16_f16 v[0:15], v[60:63], v[156:159], v[0:15]
	ds_read_b128 v[156:159], v242 offset:8192
	s_waitcnt lgkmcnt(14)
	v_mfma_f32_32x32x16_f16 v[0:15], v[64:67], v[160:163], v[0:15]
	ds_read_b128 v[160:163], v242 offset:9216
	s_waitcnt lgkmcnt(14)
	v_mfma_f32_32x32x16_f16 v[0:15], v[68:71], v[164:167], v[0:15]
	ds_read_b128 v[164:167], v242 offset:10240
	s_waitcnt lgkmcnt(14)
	v_mfma_f32_32x32x16_f16 v[0:15], v[72:75], v[168:171], v[0:15]
	ds_read_b128 v[168:171], v242 offset:11264
	s_waitcnt lgkmcnt(14)
	v_mfma_f32_32x32x16_f16 v[0:15], v[76:79], v[172:175], v[0:15]
	ds_read_b128 v[172:175], v242 offset:12288
	s_waitcnt lgkmcnt(14)
	v_mfma_f32_32x32x16_f16 v[0:15], v[80:83], v[176:179], v[0:15]
	ds_read_b128 v[176:179], v242 offset:13312
	s_waitcnt lgkmcnt(14)
	v_mfma_f32_32x32x16_f16 v[0:15], v[84:87], v[180:183], v[0:15]
	ds_read_b128 v[180:183], v242 offset:14336
	s_waitcnt lgkmcnt(14)
	v_mfma_f32_32x32x16_f16 v[0:15], v[88:91], v[184:187], v[0:15]
	ds_read_b128 v[184:187], v242 offset:15360
	s_waitcnt lgkmcnt(14)
	v_mfma_f32_32x32x16_f16 v[0:15], v[92:95], v[188:191], v[0:15]
	ds_read_b128 v[188:191], v242 offset:16384
	s_waitcnt lgkmcnt(14)
	v_mfma_f32_32x32x16_f16 v[0:15], v[96:99], v[192:195], v[0:15]
	ds_read_b128 v[192:195], v242 offset:17408
	s_waitcnt lgkmcnt(14)
	v_mfma_f32_32x32x16_f16 v[0:15], v[100:103], v[196:199], v[0:15]
	ds_read_b128 v[196:199], v242 offset:18432
	s_waitcnt vmcnt(0)
	ds_write_b128 v252, v[16:19] offset:49152
	ds_write_b128 v253, v[20:23] offset:49152
	ds_write_b128 v254, v[24:27] offset:49152
	s_waitcnt lgkmcnt(14)
	v_mfma_f32_32x32x16_f16 v[0:15], v[104:107], v[200:203], v[0:15]
	ds_read_b128 v[200:203], v242 offset:19456
	s_waitcnt lgkmcnt(14)
	v_mfma_f32_32x32x16_f16 v[0:15], v[108:111], v[204:207], v[0:15]
	ds_read_b128 v[204:207], v242 offset:20480
	s_waitcnt lgkmcnt(14)
	v_mfma_f32_32x32x16_f16 v[0:15], v[112:115], v[208:211], v[0:15]
	ds_read_b128 v[208:211], v242 offset:21504
	s_waitcnt lgkmcnt(14)
	v_mfma_f32_32x32x16_f16 v[0:15], v[116:119], v[212:215], v[0:15]
	ds_read_b128 v[212:215], v242 offset:22528
	s_waitcnt lgkmcnt(14)
	v_mfma_f32_32x32x16_f16 v[0:15], v[120:123], v[216:219], v[0:15]
	ds_read_b128 v[216:219], v242 offset:23552
	s_waitcnt lgkmcnt(5)
	s_barrier
	s_add_u32 s24, s22, 147456
	s_addc_u32 s25, s23, 0
	s_waitcnt lgkmcnt(14)
	v_mfma_f32_32x32x16_f16 v[220:235], v[28:31], v[124:127], 0
	ds_read_b128 v[124:127], v242 offset:24576
	global_load_dwordx4 v[16:19], v236, s[24:25]
	global_load_dwordx4 v[20:23], v237, s[24:25]
	global_load_dwordx4 v[24:27], v238, s[24:25]
	s_waitcnt lgkmcnt(14)
	v_mfma_f32_32x32x16_f16 v[220:235], v[32:35], v[128:131], v[220:235]
	ds_read_b128 v[128:131], v242 offset:25600
	s_add_i32 s20, s14, 3
	s_cmp_lt_u32 s20, 12
	s_cselect_b32 s26, s8, s10
	s_cselect_b32 s27, s9, s11
	s_waitcnt lgkmcnt(14)
	v_mfma_f32_32x32x16_f16 v[220:235], v[36:39], v[132:135], v[220:235]
	ds_read_b128 v[132:135], v242 offset:26624
	s_cselect_b32 s21, 0, 12
	s_cmp_lt_u32 s20, 24
	s_cselect_b32 s26, s26, s0
	s_cselect_b32 s27, s27, s1
	s_waitcnt lgkmcnt(14)
	v_mfma_f32_32x32x16_f16 v[220:235], v[40:43], v[136:139], v[220:235]
	ds_read_b128 v[136:139], v242 offset:27648
	s_cselect_b32 s21, s21, 24
	s_sub_i32 s20, s20, s21
	s_lshr_b32 s21, s20, 1
	s_and_b32 s20, s20, 1
	s_waitcnt lgkmcnt(14)
	v_mfma_f32_32x32x16_f16 v[220:235], v[44:47], v[140:143], v[220:235]
	ds_read_b128 v[140:143], v242 offset:28672
	s_add_i32 s21, s21, s15
	s_lshl_b32 s21, s21, 15
	s_lshl_b32 s20, s20, 11
	s_add_i32 s21, s21, s20
	s_waitcnt lgkmcnt(14)
	v_mfma_f32_32x32x16_f16 v[220:235], v[48:51], v[144:147], v[220:235]
	ds_read_b128 v[144:147], v242 offset:29696
	s_add_u32 s26, s26, s21
	s_addc_u32 s27, s27, 0
	s_waitcnt lgkmcnt(14)
	v_mfma_f32_32x32x16_f16 v[220:235], v[52:55], v[148:151], v[220:235]
	ds_read_b128 v[148:151], v242 offset:30720
	v_cvt_pk_f16_f32 v244, v0, v1
	v_cvt_pk_f16_f32 v245, v2, v3
	s_waitcnt lgkmcnt(14)
	v_mfma_f32_32x32x16_f16 v[220:235], v[56:59], v[152:155], v[220:235]
	ds_read_b128 v[152:155], v242 offset:31744
	v_cvt_pk_f16_f32 v246, v4, v5
	v_cvt_pk_f16_f32 v247, v6, v7
	s_waitcnt lgkmcnt(14)
	v_mfma_f32_32x32x16_f16 v[220:235], v[60:63], v[156:159], v[220:235]
	ds_read_b128 v[156:159], v242 offset:32768
	v_cvt_pk_f16_f32 v248, v8, v9
	v_cvt_pk_f16_f32 v249, v10, v11
	s_waitcnt lgkmcnt(14)
	v_mfma_f32_32x32x16_f16 v[220:235], v[64:67], v[160:163], v[220:235]
	ds_read_b128 v[160:163], v242 offset:33792
	v_cvt_pk_f16_f32 v250, v12, v13
	v_cvt_pk_f16_f32 v251, v14, v15
	s_waitcnt lgkmcnt(14)
	v_mfma_f32_32x32x16_f16 v[220:235], v[68:71], v[164:167], v[220:235]
	ds_read_b128 v[164:167], v242 offset:34816
	global_store_dwordx4 v241, v[244:247], s[26:27] sc1
	s_waitcnt lgkmcnt(14)
	v_mfma_f32_32x32x16_f16 v[220:235], v[72:75], v[168:171], v[220:235]
	ds_read_b128 v[168:171], v242 offset:35840
	global_store_dwordx4 v241, v[248:251], s[26:27] offset:1024 sc1
	s_waitcnt lgkmcnt(14)
	v_mfma_f32_32x32x16_f16 v[220:235], v[76:79], v[172:175], v[220:235]
	ds_read_b128 v[172:175], v242 offset:36864
	s_waitcnt lgkmcnt(14)
	v_mfma_f32_32x32x16_f16 v[220:235], v[80:83], v[176:179], v[220:235]
	ds_read_b128 v[176:179], v242 offset:37888
	s_waitcnt lgkmcnt(14)
	v_mfma_f32_32x32x16_f16 v[220:235], v[84:87], v[180:183], v[220:235]
	ds_read_b128 v[180:183], v242 offset:38912
	s_waitcnt lgkmcnt(14)
	v_mfma_f32_32x32x16_f16 v[220:235], v[88:91], v[184:187], v[220:235]
	ds_read_b128 v[184:187], v242 offset:39936
	s_waitcnt lgkmcnt(14)
	v_mfma_f32_32x32x16_f16 v[220:235], v[92:95], v[188:191], v[220:235]
	ds_read_b128 v[188:191], v242 offset:40960
	s_waitcnt lgkmcnt(14)
	v_mfma_f32_32x32x16_f16 v[220:235], v[96:99], v[192:195], v[220:235]
	ds_read_b128 v[192:195], v242 offset:41984
	s_waitcnt lgkmcnt(14)
	v_mfma_f32_32x32x16_f16 v[220:235], v[100:103], v[196:199], v[220:235]
	ds_read_b128 v[196:199], v242 offset:43008
	s_waitcnt vmcnt(2)
	ds_write_b128 v236, v[16:19] offset:0
	ds_write_b128 v237, v[20:23] offset:0
	ds_write_b128 v238, v[24:27] offset:0
	s_waitcnt lgkmcnt(14)
	v_mfma_f32_32x32x16_f16 v[220:235], v[104:107], v[200:203], v[220:235]
	ds_read_b128 v[200:203], v242 offset:44032
	s_waitcnt lgkmcnt(14)
	v_mfma_f32_32x32x16_f16 v[220:235], v[108:111], v[204:207], v[220:235]
	ds_read_b128 v[204:207], v242 offset:45056
	s_waitcnt lgkmcnt(14)
	v_mfma_f32_32x32x16_f16 v[220:235], v[112:115], v[208:211], v[220:235]
	ds_read_b128 v[208:211], v242 offset:46080
	s_waitcnt lgkmcnt(14)
	v_mfma_f32_32x32x16_f16 v[220:235], v[116:119], v[212:215], v[220:235]
	ds_read_b128 v[212:215], v242 offset:47104
	s_waitcnt lgkmcnt(14)
	v_mfma_f32_32x32x16_f16 v[220:235], v[120:123], v[216:219], v[220:235]
	ds_read_b128 v[216:219], v242 offset:48128
	s_waitcnt lgkmcnt(5)
	s_barrier
	s_add_u32 s24, s22, 172032
	s_addc_u32 s25, s23, 0
	s_waitcnt lgkmcnt(14)
	v_mfma_f32_32x32x16_f16 v[0:15], v[28:31], v[124:127], 0
	ds_read_b128 v[124:127], v239 offset:0
	global_load_dwordx4 v[16:19], v236, s[24:25]
	global_load_dwordx4 v[20:23], v237, s[24:25]
	global_load_dwordx4 v[24:27], v238, s[24:25]
	s_waitcnt lgkmcnt(14)
	v_mfma_f32_32x32x16_f16 v[0:15], v[32:35], v[128:131], v[0:15]
	ds_read_b128 v[128:131], v239 offset:1024
	s_add_i32 s20, s14, 4
	s_cmp_lt_u32 s20, 12
	s_cselect_b32 s26, s8, s10
	s_cselect_b32 s27, s9, s11
	s_waitcnt lgkmcnt(14)
	v_mfma_f32_32x32x16_f16 v[0:15], v[36:39], v[132:135], v[0:15]
	ds_read_b128 v[132:135], v239 offset:2048
	s_cselect_b32 s21, 0, 12
	s_cmp_lt_u32 s20, 24
	s_cselect_b32 s26, s26, s0
	s_cselect_b32 s27, s27, s1
	s_waitcnt lgkmcnt(14)
	v_mfma_f32_32x32x16_f16 v[0:15], v[40:43], v[136:139], v[0:15]
	ds_read_b128 v[136:139], v239 offset:3072
	s_cselect_b32 s21, s21, 24
	s_sub_i32 s20, s20, s21
	s_lshr_b32 s21, s20, 1
	s_and_b32 s20, s20, 1
	s_waitcnt lgkmcnt(14)
	v_mfma_f32_32x32x16_f16 v[0:15], v[44:47], v[140:143], v[0:15]
	ds_read_b128 v[140:143], v239 offset:4096
	s_add_i32 s21, s21, s15
	s_lshl_b32 s21, s21, 15
	s_lshl_b32 s20, s20, 11
	s_add_i32 s21, s21, s20
	s_waitcnt lgkmcnt(14)
	v_mfma_f32_32x32x16_f16 v[0:15], v[48:51], v[144:147], v[0:15]
	ds_read_b128 v[144:147], v239 offset:5120
	s_add_u32 s26, s26, s21
	s_addc_u32 s27, s27, 0
	s_waitcnt lgkmcnt(14)
	v_mfma_f32_32x32x16_f16 v[0:15], v[52:55], v[148:151], v[0:15]
	ds_read_b128 v[148:151], v239 offset:6144
	v_cvt_pk_f16_f32 v244, v220, v221
	v_cvt_pk_f16_f32 v245, v222, v223
	s_waitcnt lgkmcnt(14)
	v_mfma_f32_32x32x16_f16 v[0:15], v[56:59], v[152:155], v[0:15]
	ds_read_b128 v[152:155], v239 offset:7168
	v_cvt_pk_f16_f32 v246, v224, v225
	v_cvt_pk_f16_f32 v247, v226, v227
	s_waitcnt lgkmcnt(14)
	v_mfma_f32_32x32x16_f16 v[0:15], v[60:63], v[156:159], v[0:15]
	ds_read_b128 v[156:159], v239 offset:8192
	v_cvt_pk_f16_f32 v248, v228, v229
	v_cvt_pk_f16_f32 v249, v230, v231
	s_waitcnt lgkmcnt(14)
	v_mfma_f32_32x32x16_f16 v[0:15], v[64:67], v[160:163], v[0:15]
	ds_read_b128 v[160:163], v239 offset:9216
	v_cvt_pk_f16_f32 v250, v232, v233
	v_cvt_pk_f16_f32 v251, v234, v235
	s_waitcnt lgkmcnt(14)
	v_mfma_f32_32x32x16_f16 v[0:15], v[68:71], v[164:167], v[0:15]
	ds_read_b128 v[164:167], v239 offset:10240
	global_store_dwordx4 v241, v[244:247], s[26:27] sc1
	s_waitcnt lgkmcnt(14)
	v_mfma_f32_32x32x16_f16 v[0:15], v[72:75], v[168:171], v[0:15]
	ds_read_b128 v[168:171], v239 offset:11264
	global_store_dwordx4 v241, v[248:251], s[26:27] offset:1024 sc1
	s_waitcnt lgkmcnt(14)
	v_mfma_f32_32x32x16_f16 v[0:15], v[76:79], v[172:175], v[0:15]
	ds_read_b128 v[172:175], v239 offset:12288
	s_waitcnt lgkmcnt(14)
	v_mfma_f32_32x32x16_f16 v[0:15], v[80:83], v[176:179], v[0:15]
	ds_read_b128 v[176:179], v239 offset:13312
	s_waitcnt lgkmcnt(14)
	v_mfma_f32_32x32x16_f16 v[0:15], v[84:87], v[180:183], v[0:15]
	ds_read_b128 v[180:183], v239 offset:14336
	s_waitcnt lgkmcnt(14)
	v_mfma_f32_32x32x16_f16 v[0:15], v[88:91], v[184:187], v[0:15]
	ds_read_b128 v[184:187], v239 offset:15360
	s_waitcnt lgkmcnt(14)
	v_mfma_f32_32x32x16_f16 v[0:15], v[92:95], v[188:191], v[0:15]
	ds_read_b128 v[188:191], v239 offset:16384
	s_waitcnt lgkmcnt(14)
	v_mfma_f32_32x32x16_f16 v[0:15], v[96:99], v[192:195], v[0:15]
	ds_read_b128 v[192:195], v239 offset:17408
	s_waitcnt lgkmcnt(14)
	v_mfma_f32_32x32x16_f16 v[0:15], v[100:103], v[196:199], v[0:15]
	ds_read_b128 v[196:199], v239 offset:18432
	s_waitcnt vmcnt(2)
	ds_write_b128 v236, v[16:19] offset:24576
	ds_write_b128 v237, v[20:23] offset:24576
	ds_write_b128 v238, v[24:27] offset:24576
	s_waitcnt lgkmcnt(14)
	v_mfma_f32_32x32x16_f16 v[0:15], v[104:107], v[200:203], v[0:15]
	ds_read_b128 v[200:203], v239 offset:19456
	s_waitcnt lgkmcnt(14)
	v_mfma_f32_32x32x16_f16 v[0:15], v[108:111], v[204:207], v[0:15]
	ds_read_b128 v[204:207], v239 offset:20480
	s_waitcnt lgkmcnt(14)
	v_mfma_f32_32x32x16_f16 v[0:15], v[112:115], v[208:211], v[0:15]
	ds_read_b128 v[208:211], v239 offset:21504
	s_waitcnt lgkmcnt(14)
	v_mfma_f32_32x32x16_f16 v[0:15], v[116:119], v[212:215], v[0:15]
	ds_read_b128 v[212:215], v239 offset:22528
	s_waitcnt lgkmcnt(14)
	v_mfma_f32_32x32x16_f16 v[0:15], v[120:123], v[216:219], v[0:15]
	ds_read_b128 v[216:219], v239 offset:23552
	s_waitcnt lgkmcnt(5)
	s_barrier
	s_add_u32 s24, s22, 196608
	s_addc_u32 s25, s23, 0
	s_waitcnt lgkmcnt(14)
	v_mfma_f32_32x32x16_f16 v[220:235], v[28:31], v[124:127], 0
	ds_read_b128 v[124:127], v239 offset:24576
	global_load_dwordx4 v[16:19], v236, s[24:25]
	global_load_dwordx4 v[20:23], v237, s[24:25]
	global_load_dwordx4 v[24:27], v238, s[24:25]
	s_waitcnt lgkmcnt(14)
	v_mfma_f32_32x32x16_f16 v[220:235], v[32:35], v[128:131], v[220:235]
	ds_read_b128 v[128:131], v239 offset:25600
	s_add_i32 s20, s14, 5
	s_cmp_lt_u32 s20, 12
	s_cselect_b32 s26, s8, s10
	s_cselect_b32 s27, s9, s11
	s_waitcnt lgkmcnt(14)
	v_mfma_f32_32x32x16_f16 v[220:235], v[36:39], v[132:135], v[220:235]
	ds_read_b128 v[132:135], v239 offset:26624
	s_cselect_b32 s21, 0, 12
	s_cmp_lt_u32 s20, 24
	s_cselect_b32 s26, s26, s0
	s_cselect_b32 s27, s27, s1
	s_waitcnt lgkmcnt(14)
	v_mfma_f32_32x32x16_f16 v[220:235], v[40:43], v[136:139], v[220:235]
	ds_read_b128 v[136:139], v239 offset:27648
	s_cselect_b32 s21, s21, 24
	s_sub_i32 s20, s20, s21
	s_lshr_b32 s21, s20, 1
	s_and_b32 s20, s20, 1
	s_waitcnt lgkmcnt(14)
	v_mfma_f32_32x32x16_f16 v[220:235], v[44:47], v[140:143], v[220:235]
	ds_read_b128 v[140:143], v239 offset:28672
	s_add_i32 s21, s21, s15
	s_lshl_b32 s21, s21, 15
	s_lshl_b32 s20, s20, 11
	s_add_i32 s21, s21, s20
	s_waitcnt lgkmcnt(14)
	v_mfma_f32_32x32x16_f16 v[220:235], v[48:51], v[144:147], v[220:235]
	ds_read_b128 v[144:147], v239 offset:29696
	s_add_u32 s26, s26, s21
	s_addc_u32 s27, s27, 0
	s_waitcnt lgkmcnt(14)
	v_mfma_f32_32x32x16_f16 v[220:235], v[52:55], v[148:151], v[220:235]
	ds_read_b128 v[148:151], v239 offset:30720
	v_cvt_pk_f16_f32 v244, v0, v1
	v_cvt_pk_f16_f32 v245, v2, v3
	s_waitcnt lgkmcnt(14)
	v_mfma_f32_32x32x16_f16 v[220:235], v[56:59], v[152:155], v[220:235]
	ds_read_b128 v[152:155], v239 offset:31744
	v_cvt_pk_f16_f32 v246, v4, v5
	v_cvt_pk_f16_f32 v247, v6, v7
	s_waitcnt lgkmcnt(14)
	v_mfma_f32_32x32x16_f16 v[220:235], v[60:63], v[156:159], v[220:235]
	ds_read_b128 v[156:159], v239 offset:32768
	v_cvt_pk_f16_f32 v248, v8, v9
	v_cvt_pk_f16_f32 v249, v10, v11
	s_waitcnt lgkmcnt(14)
	v_mfma_f32_32x32x16_f16 v[220:235], v[64:67], v[160:163], v[220:235]
	ds_read_b128 v[160:163], v239 offset:33792
	v_cvt_pk_f16_f32 v250, v12, v13
	v_cvt_pk_f16_f32 v251, v14, v15
	s_waitcnt lgkmcnt(14)
	v_mfma_f32_32x32x16_f16 v[220:235], v[68:71], v[164:167], v[220:235]
	ds_read_b128 v[164:167], v239 offset:34816
	global_store_dwordx4 v241, v[244:247], s[26:27] sc1
	s_waitcnt lgkmcnt(14)
	v_mfma_f32_32x32x16_f16 v[220:235], v[72:75], v[168:171], v[220:235]
	ds_read_b128 v[168:171], v239 offset:35840
	global_store_dwordx4 v241, v[248:251], s[26:27] offset:1024 sc1
	s_waitcnt lgkmcnt(14)
	v_mfma_f32_32x32x16_f16 v[220:235], v[76:79], v[172:175], v[220:235]
	ds_read_b128 v[172:175], v239 offset:36864
	s_waitcnt lgkmcnt(14)
	v_mfma_f32_32x32x16_f16 v[220:235], v[80:83], v[176:179], v[220:235]
	ds_read_b128 v[176:179], v239 offset:37888
	s_waitcnt lgkmcnt(14)
	v_mfma_f32_32x32x16_f16 v[220:235], v[84:87], v[180:183], v[220:235]
	ds_read_b128 v[180:183], v239 offset:38912
	s_waitcnt lgkmcnt(14)
	v_mfma_f32_32x32x16_f16 v[220:235], v[88:91], v[184:187], v[220:235]
	ds_read_b128 v[184:187], v239 offset:39936
	s_waitcnt lgkmcnt(14)
	v_mfma_f32_32x32x16_f16 v[220:235], v[92:95], v[188:191], v[220:235]
	ds_read_b128 v[188:191], v239 offset:40960
	s_waitcnt lgkmcnt(14)
	v_mfma_f32_32x32x16_f16 v[220:235], v[96:99], v[192:195], v[220:235]
	ds_read_b128 v[192:195], v239 offset:41984
	s_waitcnt lgkmcnt(14)
	v_mfma_f32_32x32x16_f16 v[220:235], v[100:103], v[196:199], v[220:235]
	ds_read_b128 v[196:199], v239 offset:43008
	s_waitcnt vmcnt(2)
	ds_write_b128 v236, v[16:19] offset:49152
	ds_write_b128 v237, v[20:23] offset:49152
	ds_write_b128 v238, v[24:27] offset:49152
	s_waitcnt lgkmcnt(14)
	v_mfma_f32_32x32x16_f16 v[220:235], v[104:107], v[200:203], v[220:235]
	ds_read_b128 v[200:203], v239 offset:44032
	s_waitcnt lgkmcnt(14)
	v_mfma_f32_32x32x16_f16 v[220:235], v[108:111], v[204:207], v[220:235]
	ds_read_b128 v[204:207], v239 offset:45056
	s_waitcnt lgkmcnt(14)
	v_mfma_f32_32x32x16_f16 v[220:235], v[112:115], v[208:211], v[220:235]
	ds_read_b128 v[208:211], v239 offset:46080
	s_waitcnt lgkmcnt(14)
	v_mfma_f32_32x32x16_f16 v[220:235], v[116:119], v[212:215], v[220:235]
	ds_read_b128 v[212:215], v239 offset:47104
	s_waitcnt lgkmcnt(14)
	v_mfma_f32_32x32x16_f16 v[220:235], v[120:123], v[216:219], v[220:235]
	ds_read_b128 v[216:219], v239 offset:48128
	s_waitcnt lgkmcnt(5)
	s_barrier
	s_waitcnt lgkmcnt(14)
	v_mfma_f32_32x32x16_f16 v[0:15], v[28:31], v[124:127], 0
	ds_read_b128 v[124:127], v240 offset:0
	s_waitcnt lgkmcnt(14)
	v_mfma_f32_32x32x16_f16 v[0:15], v[32:35], v[128:131], v[0:15]
	ds_read_b128 v[128:131], v240 offset:1024
	s_add_i32 s20, s14, 6
	s_cmp_lt_u32 s20, 12
	s_cselect_b32 s26, s8, s10
	s_cselect_b32 s27, s9, s11
	s_waitcnt lgkmcnt(14)
	v_mfma_f32_32x32x16_f16 v[0:15], v[36:39], v[132:135], v[0:15]
	ds_read_b128 v[132:135], v240 offset:2048
	s_cselect_b32 s21, 0, 12
	s_cmp_lt_u32 s20, 24
	s_cselect_b32 s26, s26, s0
	s_cselect_b32 s27, s27, s1
	s_waitcnt lgkmcnt(14)
	v_mfma_f32_32x32x16_f16 v[0:15], v[40:43], v[136:139], v[0:15]
	ds_read_b128 v[136:139], v240 offset:3072
	s_cselect_b32 s21, s21, 24
	s_sub_i32 s20, s20, s21
	s_lshr_b32 s21, s20, 1
	s_and_b32 s20, s20, 1
	s_waitcnt lgkmcnt(14)
	v_mfma_f32_32x32x16_f16 v[0:15], v[44:47], v[140:143], v[0:15]
	ds_read_b128 v[140:143], v240 offset:4096
	s_add_i32 s21, s21, s15
	s_lshl_b32 s21, s21, 15
	s_lshl_b32 s20, s20, 11
	s_add_i32 s21, s21, s20
	s_waitcnt lgkmcnt(14)
	v_mfma_f32_32x32x16_f16 v[0:15], v[48:51], v[144:147], v[0:15]
	ds_read_b128 v[144:147], v240 offset:5120
	s_add_u32 s26, s26, s21
	s_addc_u32 s27, s27, 0
	s_waitcnt lgkmcnt(14)
	v_mfma_f32_32x32x16_f16 v[0:15], v[52:55], v[148:151], v[0:15]
	ds_read_b128 v[148:151], v240 offset:6144
	v_cvt_pk_f16_f32 v244, v220, v221
	v_cvt_pk_f16_f32 v245, v222, v223
	s_waitcnt lgkmcnt(14)
	v_mfma_f32_32x32x16_f16 v[0:15], v[56:59], v[152:155], v[0:15]
	ds_read_b128 v[152:155], v240 offset:7168
	v_cvt_pk_f16_f32 v246, v224, v225
	v_cvt_pk_f16_f32 v247, v226, v227
	s_waitcnt lgkmcnt(14)
	v_mfma_f32_32x32x16_f16 v[0:15], v[60:63], v[156:159], v[0:15]
	ds_read_b128 v[156:159], v240 offset:8192
	v_cvt_pk_f16_f32 v248, v228, v229
	v_cvt_pk_f16_f32 v249, v230, v231
	s_waitcnt lgkmcnt(14)
	v_mfma_f32_32x32x16_f16 v[0:15], v[64:67], v[160:163], v[0:15]
	ds_read_b128 v[160:163], v240 offset:9216
	v_cvt_pk_f16_f32 v250, v232, v233
	v_cvt_pk_f16_f32 v251, v234, v235
	s_waitcnt lgkmcnt(14)
	v_mfma_f32_32x32x16_f16 v[0:15], v[68:71], v[164:167], v[0:15]
	ds_read_b128 v[164:167], v240 offset:10240
	global_store_dwordx4 v241, v[244:247], s[26:27] sc1
	s_waitcnt lgkmcnt(14)
	v_mfma_f32_32x32x16_f16 v[0:15], v[72:75], v[168:171], v[0:15]
	ds_read_b128 v[168:171], v240 offset:11264
	global_store_dwordx4 v241, v[248:251], s[26:27] offset:1024 sc1
	s_waitcnt lgkmcnt(14)
	v_mfma_f32_32x32x16_f16 v[0:15], v[76:79], v[172:175], v[0:15]
	ds_read_b128 v[172:175], v240 offset:12288
	s_waitcnt lgkmcnt(14)
	v_mfma_f32_32x32x16_f16 v[0:15], v[80:83], v[176:179], v[0:15]
	ds_read_b128 v[176:179], v240 offset:13312
	s_waitcnt lgkmcnt(14)
	v_mfma_f32_32x32x16_f16 v[0:15], v[84:87], v[180:183], v[0:15]
	ds_read_b128 v[180:183], v240 offset:14336
	s_waitcnt lgkmcnt(14)
	v_mfma_f32_32x32x16_f16 v[0:15], v[88:91], v[184:187], v[0:15]
	ds_read_b128 v[184:187], v240 offset:15360
	s_waitcnt lgkmcnt(14)
	v_mfma_f32_32x32x16_f16 v[0:15], v[92:95], v[188:191], v[0:15]
	ds_read_b128 v[188:191], v240 offset:16384
	s_waitcnt lgkmcnt(14)
	v_mfma_f32_32x32x16_f16 v[0:15], v[96:99], v[192:195], v[0:15]
	ds_read_b128 v[192:195], v240 offset:17408
	s_waitcnt lgkmcnt(14)
	v_mfma_f32_32x32x16_f16 v[0:15], v[100:103], v[196:199], v[0:15]
	ds_read_b128 v[196:199], v240 offset:18432
	s_waitcnt lgkmcnt(14)
	v_mfma_f32_32x32x16_f16 v[0:15], v[104:107], v[200:203], v[0:15]
	ds_read_b128 v[200:203], v240 offset:19456
	s_waitcnt lgkmcnt(14)
	v_mfma_f32_32x32x16_f16 v[0:15], v[108:111], v[204:207], v[0:15]
	ds_read_b128 v[204:207], v240 offset:20480
	s_waitcnt lgkmcnt(14)
	v_mfma_f32_32x32x16_f16 v[0:15], v[112:115], v[208:211], v[0:15]
	ds_read_b128 v[208:211], v240 offset:21504
	s_waitcnt lgkmcnt(14)
	v_mfma_f32_32x32x16_f16 v[0:15], v[116:119], v[212:215], v[0:15]
	ds_read_b128 v[212:215], v240 offset:22528
	s_waitcnt lgkmcnt(14)
	v_mfma_f32_32x32x16_f16 v[0:15], v[120:123], v[216:219], v[0:15]
	ds_read_b128 v[216:219], v240 offset:23552
	s_waitcnt lgkmcnt(14)
	v_mfma_f32_32x32x16_f16 v[220:235], v[28:31], v[124:127], 0
	s_waitcnt lgkmcnt(14)
	v_mfma_f32_32x32x16_f16 v[220:235], v[32:35], v[128:131], v[220:235]
	s_add_i32 s20, s14, 7
	s_cmp_lt_u32 s20, 12
	s_cselect_b32 s26, s8, s10
	s_cselect_b32 s27, s9, s11
	s_waitcnt lgkmcnt(14)
	v_mfma_f32_32x32x16_f16 v[220:235], v[36:39], v[132:135], v[220:235]
	s_cselect_b32 s21, 0, 12
	s_cmp_lt_u32 s20, 24
	s_cselect_b32 s26, s26, s0
	s_cselect_b32 s27, s27, s1
	s_waitcnt lgkmcnt(14)
	v_mfma_f32_32x32x16_f16 v[220:235], v[40:43], v[136:139], v[220:235]
	s_cselect_b32 s21, s21, 24
	s_sub_i32 s20, s20, s21
	s_lshr_b32 s21, s20, 1
	s_and_b32 s20, s20, 1
	s_waitcnt lgkmcnt(14)
	v_mfma_f32_32x32x16_f16 v[220:235], v[44:47], v[140:143], v[220:235]
	s_add_i32 s21, s21, s15
	s_lshl_b32 s21, s21, 15
	s_lshl_b32 s20, s20, 11
	s_add_i32 s21, s21, s20
	s_waitcnt lgkmcnt(14)
	v_mfma_f32_32x32x16_f16 v[220:235], v[48:51], v[144:147], v[220:235]
	s_add_u32 s26, s26, s21
	s_addc_u32 s27, s27, 0
	s_waitcnt lgkmcnt(14)
	v_mfma_f32_32x32x16_f16 v[220:235], v[52:55], v[148:151], v[220:235]
	v_cvt_pk_f16_f32 v244, v0, v1
	v_cvt_pk_f16_f32 v245, v2, v3
	s_waitcnt lgkmcnt(14)
	v_mfma_f32_32x32x16_f16 v[220:235], v[56:59], v[152:155], v[220:235]
	v_cvt_pk_f16_f32 v246, v4, v5
	v_cvt_pk_f16_f32 v247, v6, v7
	s_waitcnt lgkmcnt(14)
	v_mfma_f32_32x32x16_f16 v[220:235], v[60:63], v[156:159], v[220:235]
	v_cvt_pk_f16_f32 v248, v8, v9
	v_cvt_pk_f16_f32 v249, v10, v11
	s_waitcnt lgkmcnt(14)
	v_mfma_f32_32x32x16_f16 v[220:235], v[64:67], v[160:163], v[220:235]
	v_cvt_pk_f16_f32 v250, v12, v13
	v_cvt_pk_f16_f32 v251, v14, v15
	s_waitcnt lgkmcnt(13)
	v_mfma_f32_32x32x16_f16 v[220:235], v[68:71], v[164:167], v[220:235]
	global_store_dwordx4 v241, v[244:247], s[26:27] sc1
	s_waitcnt lgkmcnt(12)
	v_mfma_f32_32x32x16_f16 v[220:235], v[72:75], v[168:171], v[220:235]
	global_store_dwordx4 v241, v[248:251], s[26:27] offset:1024 sc1
	s_waitcnt lgkmcnt(11)
	v_mfma_f32_32x32x16_f16 v[220:235], v[76:79], v[172:175], v[220:235]
	s_waitcnt lgkmcnt(10)
	v_mfma_f32_32x32x16_f16 v[220:235], v[80:83], v[176:179], v[220:235]
	s_waitcnt lgkmcnt(9)
	v_mfma_f32_32x32x16_f16 v[220:235], v[84:87], v[180:183], v[220:235]
	s_waitcnt lgkmcnt(8)
	v_mfma_f32_32x32x16_f16 v[220:235], v[88:91], v[184:187], v[220:235]
	s_waitcnt lgkmcnt(7)
	v_mfma_f32_32x32x16_f16 v[220:235], v[92:95], v[188:191], v[220:235]
	s_waitcnt lgkmcnt(6)
	v_mfma_f32_32x32x16_f16 v[220:235], v[96:99], v[192:195], v[220:235]
	s_waitcnt lgkmcnt(5)
	v_mfma_f32_32x32x16_f16 v[220:235], v[100:103], v[196:199], v[220:235]
	s_waitcnt lgkmcnt(4)
	v_mfma_f32_32x32x16_f16 v[220:235], v[104:107], v[200:203], v[220:235]
	s_waitcnt lgkmcnt(3)
	v_mfma_f32_32x32x16_f16 v[220:235], v[108:111], v[204:207], v[220:235]
	s_waitcnt lgkmcnt(2)
	v_mfma_f32_32x32x16_f16 v[220:235], v[112:115], v[208:211], v[220:235]
	s_waitcnt lgkmcnt(1)
	v_mfma_f32_32x32x16_f16 v[220:235], v[116:119], v[212:215], v[220:235]
	s_waitcnt lgkmcnt(0)
	v_mfma_f32_32x32x16_f16 v[220:235], v[120:123], v[216:219], v[220:235]
	s_add_i32 s20, s14, 8
	s_cmp_lt_u32 s20, 12
	s_cselect_b32 s26, s8, s10
	s_cselect_b32 s27, s9, s11
	s_cselect_b32 s21, 0, 12
	s_cmp_lt_u32 s20, 24
	s_cselect_b32 s26, s26, s0
	s_cselect_b32 s27, s27, s1
	s_cselect_b32 s21, s21, 24
	s_sub_i32 s20, s20, s21
	s_lshr_b32 s21, s20, 1
	s_and_b32 s20, s20, 1
	s_add_i32 s21, s21, s15
	s_lshl_b32 s21, s21, 15
	s_lshl_b32 s20, s20, 11
	s_add_i32 s21, s21, s20
	s_add_u32 s26, s26, s21
	s_addc_u32 s27, s27, 0
	s_nop 7
	v_cvt_pk_f16_f32 v244, v220, v221
	v_cvt_pk_f16_f32 v245, v222, v223
	v_cvt_pk_f16_f32 v246, v224, v225
	v_cvt_pk_f16_f32 v247, v226, v227
	v_cvt_pk_f16_f32 v248, v228, v229
	v_cvt_pk_f16_f32 v249, v230, v231
	v_cvt_pk_f16_f32 v250, v232, v233
	v_cvt_pk_f16_f32 v251, v234, v235
	global_store_dwordx4 v241, v[244:247], s[26:27] sc1
	global_store_dwordx4 v241, v[248:251], s[26:27] offset:1024 sc1
	s_endpgm
